# baseline (speedup 1.0000x reference)
.LBB1_26:
	s_waitcnt vmcnt(35)
	v_and_b32_e32 v113, 3, v0
	s_and_b32 s18, s2, 15
	v_cmp_eq_u32_e32 vcc, 0, v113
	v_cmp_gt_u32_e64 s[4:5], 12, v92
	s_and_b64 s[12:13], vcc, s[4:5]
	s_lshl_b32 s4, s3, 12
	s_lshl_b32 s5, s18, 8
	s_or_b32 s4, s4, s5
	s_mul_hi_i32 s5, s4, 0x6000
	s_mulk_i32 s4, 0x6000
	s_lshl_b32 s3, s3, 8
	s_add_u32 s16, s24, s4
	s_addc_u32 s17, s25, s5
	s_ashr_i32 s4, s21, 31
	s_lshr_b32 s4, s4, 29
	s_add_i32 s4, s21, s4
	s_ashr_i32 s19, s4, 3
	v_and_b32_e32 v101, 1, v74
	v_lshl_or_b32 v74, v91, 1, v95
	s_min_i32 s4, s19, 0xff
	v_mul_u32_u24_e32 v74, 0x60, v74
	v_lshlrev_b32_e32 v75, 1, v92
	s_mul_hi_i32 s5, s4, 0x6000
	s_mulk_i32 s4, 0x6000
	v_or3_b32 v88, v74, v75, v101
	s_add_u32 s4, s16, s4
	s_addc_u32 s5, s17, s5
	v_lshlrev_b64 v[102:103], 4, v[88:89]
	v_lshl_add_u64 v[104:105], s[4:5], 0, v[102:103]
	global_load_dwordx4 v[82:85], v[104:105], off
	global_load_dwordx4 v[74:77], v[104:105], off offset:512
	global_load_dwordx4 v[78:81], v[104:105], off offset:1024
	s_waitcnt vmcnt(5)
	v_mul_f32_e32 v88, 0xbfb8aa3b, v97
	v_mul_f32_e32 v99, 0x3c91a2b4, v88
	s_waitcnt vmcnt(4)
	v_mul_f32_e32 v88, 0x4038aa3b, v96
	v_mul_f32_e32 v104, 0x3c91a2b4, v88
	v_lshrrev_b32_e32 v88, 2, v92
	v_and_b32_e32 v92, 4, v92
	v_cmp_lt_u32_e64 s[4:5], 1, v93
	v_mov_b32_e32 v93, 0xd0
	v_cmp_ne_u32_e32 vcc, 0, v92
	v_lshlrev_b32_e32 v107, 3, v88
	v_sub_u32_e32 v88, 0, v107
	v_cndmask_b32_e32 v92, 0, v93, vcc
	v_add_u32_e32 v106, v92, v86
	v_and_b32_e32 v92, 12, v0
	v_mul_u32_u24_e32 v86, 0xd0, v101
	v_mad_u32_u24 v91, v91, 24, v92
	v_mul_u32_u24_e32 v93, 12, v95
	v_lshlrev_b32_e32 v92, 20, v101
	v_add3_u32 v112, v91, v86, v93
	v_lshl_or_b32 v86, s18, 21, v90
	v_add3_u32 v86, v86, s3, v92
	v_mul_f32_e32 v1, 0xbfb8aa3b, v1
	v_and_b32_e32 v114, 24, v88
	v_or_b32_e32 v88, v86, v94
	s_min_i32 s3, s19, 0xfe
	v_mul_f32_e32 v1, 0x3c91a2b4, v1
	s_waitcnt vmcnt(3)
	v_mul_f32_e32 v105, 0x4038aa3b, v100
	v_add_u32_e32 v108, 16, v106
	v_add_u32_e32 v109, 0x70, v106
	v_add_u32_e32 v110, 0x1b0, v106
	v_add_u32_e32 v111, 0x210, v106
	v_mul_u32_u24_e32 v113, 6, v113
	s_add_i32 s19, s3, 1
	v_lshl_add_u64 v[100:101], s[16:17], 0, v[102:103]
	v_lshl_add_u64 v[102:103], v[88:89], 1, s[14:15]
	s_sub_i32 s3, 0x7ff, s21
	v_mov_b32_e32 v115, 0x7f7f7f7f
	s_mov_b32 s16, 0x42700000
	s_mov_b32 s17, 0x41f00000
	s_mov_b32 s18, 0x41700000
	v_mov_b32_e32 v116, 0x6000
	v_mov_b32_e32 v117, 0x4b400000
	v_mov_b32_e32 v118, 0x4b400008
	v_mov_b32_e32 v119, 0x4b400010
	v_mbcnt_lo_u32_b32 v200, -1, 0
	v_mbcnt_hi_u32_b32 v200, -1, v200
	v_and_b32_e32 v201, 3, v200
	v_and_b32_e32 v202, 15, v200
	v_cmp_gt_u32_e32 vcc, 8, v202
	s_nop 1
	v_cndmask_b32_e64 v178, 0, v115, vcc
	v_cndmask_b32_e64 v179, v115, 0, vcc
	v_lshlrev_b32_e32 v181, 1, v201
	v_sub_u32_e32 v202, 22, v181
	v_lshlrev_b32_e64 v180, v202, 1
	v_sub_u32_e32 v202, 16, v181
	v_lshlrev_b32_e64 v181, v202, 1
	v_lshrrev_b32_e32 v202, 3, v107
	v_sub_u32_e32 v184, v112, v202
	v_add_u32_e32 v184, v184, v201
	v_add_u32_e32 v202, 0xc0, v202
	v_cmp_eq_u32_e32 vcc, 3, v201
	s_nop 1
	v_cndmask_b32_e32 v184, v184, v202, vcc
	v_subrev_u32_e32 v185, s14, v102
	s_mov_b32 s44, s21
	s_mov_b32 s45, s22
	s_lshr_b32 s46, s44, 3
	s_add_i32 s46, s46, 1
	s_mul_i32 s46, s46, 0x6000
	s_mov_b32 s47, 0
	v_lshl_add_u64 v[196:197], v[100:101], 0, s[46:47]
	s_mov_b32 s42, 0x6000
	s_mov_b32 s43, 0
	s_sub_i32 s46, s44, 1
	s_sub_i32 s47, 0x800, s44
	s_and_b64 s[40:41], s[6:7], exec
	s_cselect_b32 s46, s46, s47
	s_cselect_b32 s41, 0, -1
	s_xor_b32 s40, s41, 0x400
	s_sub_i32 s40, s40, s41
	s_ashr_i32 s47, s46, 31
	s_lshl_b64 s[46:47], s[46:47], 10
	s_add_u32 s48, s14, s46
	s_addc_u32 s49, s15, s47
	v_readfirstlane_b32 s51, v112
	s_waitcnt vmcnt(0) lgkmcnt(0)
	v_mov_b32_e32 v176, v87
	v_add_f32_e32 v169, -1.0, v87
	v_rcp_f32_e32 v186, v104
	s_nop 1
	v_mul_f32_e32 v188, v105, v186
	v_mov_b32_e32 v189, 0
	v_mov_b32_e32 v190, 0
	v_mov_b32_e32 v191, 0
	s_nop 1
	s_cmp_lt_i32 s44, s45
	s_cbranch_scc0 .Lscan_exit_st
	ds_read_b64 v[122:123], v106 offset:0
	ds_read_b64 v[124:125], v106 offset:8
	ds_read_b64 v[126:127], v106 offset:16
	s_waitcnt lgkmcnt(0)
	s_cmp_lt_u32 s51, 96
	s_cbranch_scc0 .Lscan_entry_b_st
	s_branch .Lscan_enter_a_st
	.p2align 6
.Lscan_loop_a_st:
	s_barrier
.Lscan_enter_a_st:
	ds_read_b64 v[128:129], v106 offset:96
	ds_read_b64 v[130:131], v106 offset:104
	ds_read_b64 v[132:133], v106 offset:112
	s_waitcnt vmcnt(8)
	global_load_dwordx4 v[146:149], v[196:197], off
	global_load_dwordx4 v[150:153], v[196:197], off offset:512
	global_load_dwordx4 v[154:157], v[196:197], off offset:1024
	v_lshl_add_u64 v[196:197], v[196:197], 0, s[42:43]
	s_waitcnt lgkmcnt(3)
	v_mfma_f32_16x16x128_f8f6f4 v[134:137], v[122:127], v[2:7], 0 cbsz:2 blgp:2
	v_mfma_f32_16x16x128_f8f6f4 v[138:141], v[122:127], v[14:19], 0 cbsz:2 blgp:2
	v_mfma_f32_16x16x128_f8f6f4 v[142:145], v[122:127], v[26:31], v[188:191] cbsz:2 blgp:2
	v_mfma_f32_16x16x128_f8f6f4 v[204:207], v[122:127], v[38:43], 0 cbsz:2 blgp:2
	v_mfma_f32_16x16x128_f8f6f4 v[208:211], v[122:127], v[50:55], 0 cbsz:2 blgp:2
	v_mfma_f32_16x16x128_f8f6f4 v[212:215], v[122:127], v[62:67], v[188:191] cbsz:2 blgp:2
	s_waitcnt lgkmcnt(0)
	v_mfma_f32_16x16x128_f8f6f4 v[134:137], v[128:133], v[8:13], v[134:137] cbsz:2 blgp:2
	v_mfma_f32_16x16x128_f8f6f4 v[204:207], v[128:133], v[44:49], v[204:207] cbsz:2 blgp:2
	v_mfma_f32_16x16x128_f8f6f4 v[138:141], v[128:133], v[20:25], v[138:141] cbsz:2 blgp:2
	v_mfma_f32_16x16x128_f8f6f4 v[208:211], v[128:133], v[56:61], v[208:211] cbsz:2 blgp:2
	v_mfma_f32_16x16x128_f8f6f4 v[142:145], v[128:133], v[32:37], v[142:145] cbsz:2 blgp:2
	v_mfma_f32_16x16x128_f8f6f4 v[212:215], v[128:133], v[68:73], v[212:215] cbsz:2 blgp:2
	v_cndmask_b32_e64 v158, v134, v204, s[4:5]
	v_fma_mix_f32 v158, v158, v1, v82 op_sel_hi:[0,0,1]
	v_exp_f32_e32 v158, v158
	v_cndmask_b32_e64 v159, v138, v208, s[4:5]
	v_fma_mix_f32 v159, v159, v99, v74 op_sel_hi:[0,0,1]
	v_exp_f32_e32 v159, v159
	v_fma_f32 v158, v158, v186, v186
	v_rcp_f32_e32 v158, v158
	v_add_f32_e32 v159, 1.0, v159
	v_rcp_f32_e32 v159, v159
	v_cndmask_b32_e64 v160, v142, v212, s[4:5]
	v_fma_mix_f32 v161, v158, v160, v78 op_sel_hi:[0,0,1]
	v_exp_f32_e32 v161, v161
	s_add_u32 s48, s48, s40
	v_add_f32_e32 v161, 1.0, v161
	v_rcp_f32_e32 v161, v161
	s_addc_u32 s49, s49, s41
	v_fma_f32 v162, v161, -2.0, 1.0
	v_sub_f32_e32 v163, v176, v162
	v_fma_f32 v176, v159, v163, v162
	v_fma_f32 v164, |v176|, s16, v117
	v_fma_f32 v165, |v176|, s17, v118
	v_fma_f32 v166, |v176|, s18, v119
	v_lshrrev_b32_e32 v167, 26, v176
	v_min3_u32 v164, v164, v165, v166
	v_bfi_b32 v168, 31, v164, v167
	s_nop 1
	v_mul_u32_u24_dpp v170, v168, v180 quad_perm:[1,2,3,3] row_mask:0xf bank_mask:0xf bound_ctrl:1
	v_mad_u32_u24 v171, v168, v181, v170
	ds_write_b8_d16_hi v184, v171 offset:416
	global_store_short_d16_hi v185, v176, s[48:49]
	s_waitcnt lgkmcnt(0)
	s_barrier
	ds_read_b64 v[122:123], v106 offset:416
	ds_read_b64 v[124:125], v106 offset:424
	ds_read_b64 v[126:127], v106 offset:432
	s_barrier
	ds_read_b64 v[128:129], v106 offset:512
	ds_read_b64 v[130:131], v106 offset:520
	ds_read_b64 v[132:133], v106 offset:528
	s_waitcnt lgkmcnt(3)
	v_mfma_f32_16x16x128_f8f6f4 v[134:137], v[122:127], v[2:7], 0 cbsz:2 blgp:2
	v_mfma_f32_16x16x128_f8f6f4 v[138:141], v[122:127], v[14:19], 0 cbsz:2 blgp:2
	v_mfma_f32_16x16x128_f8f6f4 v[142:145], v[122:127], v[26:31], v[188:191] cbsz:2 blgp:2
	v_mfma_f32_16x16x128_f8f6f4 v[204:207], v[122:127], v[38:43], 0 cbsz:2 blgp:2
	v_mfma_f32_16x16x128_f8f6f4 v[208:211], v[122:127], v[50:55], 0 cbsz:2 blgp:2
	v_mfma_f32_16x16x128_f8f6f4 v[212:215], v[122:127], v[62:67], v[188:191] cbsz:2 blgp:2
	s_waitcnt lgkmcnt(0)
	v_mfma_f32_16x16x128_f8f6f4 v[134:137], v[128:133], v[8:13], v[134:137] cbsz:2 blgp:2
	v_mfma_f32_16x16x128_f8f6f4 v[204:207], v[128:133], v[44:49], v[204:207] cbsz:2 blgp:2
	v_mfma_f32_16x16x128_f8f6f4 v[138:141], v[128:133], v[20:25], v[138:141] cbsz:2 blgp:2
	v_mfma_f32_16x16x128_f8f6f4 v[208:211], v[128:133], v[56:61], v[208:211] cbsz:2 blgp:2
	v_mfma_f32_16x16x128_f8f6f4 v[142:145], v[128:133], v[32:37], v[142:145] cbsz:2 blgp:2
	v_mfma_f32_16x16x128_f8f6f4 v[212:215], v[128:133], v[68:73], v[212:215] cbsz:2 blgp:2
	v_cndmask_b32_e64 v158, v134, v204, s[4:5]
	v_fma_mix_f32 v158, v158, v1, v82 op_sel:[0,0,1] op_sel_hi:[0,0,1]
	v_exp_f32_e32 v158, v158
	v_cndmask_b32_e64 v159, v138, v208, s[4:5]
	v_fma_mix_f32 v159, v159, v99, v74 op_sel:[0,0,1] op_sel_hi:[0,0,1]
	v_exp_f32_e32 v159, v159
	v_fma_f32 v158, v158, v186, v186
	v_rcp_f32_e32 v158, v158
	v_add_f32_e32 v159, 1.0, v159
	v_rcp_f32_e32 v159, v159
	v_cndmask_b32_e64 v160, v142, v212, s[4:5]
	v_fma_mix_f32 v161, v158, v160, v78 op_sel:[0,0,1] op_sel_hi:[0,0,1]
	v_exp_f32_e32 v161, v161
	s_add_u32 s48, s48, s40
	v_add_f32_e32 v161, 1.0, v161
	v_rcp_f32_e32 v161, v161
	s_addc_u32 s49, s49, s41
	v_fma_f32 v162, v161, -2.0, 1.0
	v_sub_f32_e32 v163, v176, v162
	v_fma_f32 v176, v159, v163, v162
	v_fma_f32 v164, |v176|, s16, v117
	v_fma_f32 v165, |v176|, s17, v118
	v_fma_f32 v166, |v176|, s18, v119
	v_lshrrev_b32_e32 v167, 26, v176
	v_min3_u32 v164, v164, v165, v166
	v_bfi_b32 v168, 31, v164, v167
	s_nop 1
	v_mul_u32_u24_dpp v170, v168, v180 quad_perm:[1,2,3,3] row_mask:0xf bank_mask:0xf bound_ctrl:1
	v_mad_u32_u24 v171, v168, v181, v170
	ds_write_b8_d16_hi v184, v171
	global_store_short_d16_hi v185, v176, s[48:49]
	s_waitcnt lgkmcnt(0)
	s_barrier
	ds_read_b64 v[122:123], v106 offset:0
	ds_read_b64 v[124:125], v106 offset:8
	ds_read_b64 v[126:127], v106 offset:16
	s_barrier
	ds_read_b64 v[128:129], v106 offset:96
	ds_read_b64 v[130:131], v106 offset:104
	ds_read_b64 v[132:133], v106 offset:112
	s_waitcnt lgkmcnt(3)
	v_mfma_f32_16x16x128_f8f6f4 v[134:137], v[122:127], v[2:7], 0 cbsz:2 blgp:2
	v_mfma_f32_16x16x128_f8f6f4 v[138:141], v[122:127], v[14:19], 0 cbsz:2 blgp:2
	v_mfma_f32_16x16x128_f8f6f4 v[142:145], v[122:127], v[26:31], v[188:191] cbsz:2 blgp:2
	v_mfma_f32_16x16x128_f8f6f4 v[204:207], v[122:127], v[38:43], 0 cbsz:2 blgp:2
	v_mfma_f32_16x16x128_f8f6f4 v[208:211], v[122:127], v[50:55], 0 cbsz:2 blgp:2
	v_mfma_f32_16x16x128_f8f6f4 v[212:215], v[122:127], v[62:67], v[188:191] cbsz:2 blgp:2
	s_waitcnt lgkmcnt(0)
	v_mfma_f32_16x16x128_f8f6f4 v[134:137], v[128:133], v[8:13], v[134:137] cbsz:2 blgp:2
	v_mfma_f32_16x16x128_f8f6f4 v[204:207], v[128:133], v[44:49], v[204:207] cbsz:2 blgp:2
	v_mfma_f32_16x16x128_f8f6f4 v[138:141], v[128:133], v[20:25], v[138:141] cbsz:2 blgp:2
	v_mfma_f32_16x16x128_f8f6f4 v[208:211], v[128:133], v[56:61], v[208:211] cbsz:2 blgp:2
	v_mfma_f32_16x16x128_f8f6f4 v[142:145], v[128:133], v[32:37], v[142:145] cbsz:2 blgp:2
	v_mfma_f32_16x16x128_f8f6f4 v[212:215], v[128:133], v[68:73], v[212:215] cbsz:2 blgp:2
	v_cndmask_b32_e64 v158, v134, v204, s[4:5]
	v_fma_mix_f32 v158, v158, v1, v83 op_sel_hi:[0,0,1]
	v_exp_f32_e32 v158, v158
	v_cndmask_b32_e64 v159, v138, v208, s[4:5]
	v_fma_mix_f32 v159, v159, v99, v75 op_sel_hi:[0,0,1]
	v_exp_f32_e32 v159, v159
	v_fma_f32 v158, v158, v186, v186
	v_rcp_f32_e32 v158, v158
	v_add_f32_e32 v159, 1.0, v159
	v_rcp_f32_e32 v159, v159
	v_cndmask_b32_e64 v160, v142, v212, s[4:5]
	v_fma_mix_f32 v161, v158, v160, v79 op_sel_hi:[0,0,1]
	v_exp_f32_e32 v161, v161
	s_add_u32 s48, s48, s40
	v_add_f32_e32 v161, 1.0, v161
	v_rcp_f32_e32 v161, v161
	s_addc_u32 s49, s49, s41
	v_fma_f32 v162, v161, -2.0, 1.0
	v_sub_f32_e32 v163, v176, v162
	v_fma_f32 v176, v159, v163, v162
	v_fma_f32 v164, |v176|, s16, v117
	v_fma_f32 v165, |v176|, s17, v118
	v_fma_f32 v166, |v176|, s18, v119
	v_lshrrev_b32_e32 v167, 26, v176
	v_min3_u32 v164, v164, v165, v166
	v_bfi_b32 v168, 31, v164, v167
	s_nop 1
	v_mul_u32_u24_dpp v170, v168, v180 quad_perm:[1,2,3,3] row_mask:0xf bank_mask:0xf bound_ctrl:1
	v_mad_u32_u24 v171, v168, v181, v170
	ds_write_b8_d16_hi v184, v171 offset:416
	global_store_short_d16_hi v185, v176, s[48:49]
	s_waitcnt lgkmcnt(0)
	s_barrier
	ds_read_b64 v[122:123], v106 offset:416
	ds_read_b64 v[124:125], v106 offset:424
	ds_read_b64 v[126:127], v106 offset:432
	s_barrier
	ds_read_b64 v[128:129], v106 offset:512
	ds_read_b64 v[130:131], v106 offset:520
	ds_read_b64 v[132:133], v106 offset:528
	s_waitcnt lgkmcnt(3)
	v_mfma_f32_16x16x128_f8f6f4 v[134:137], v[122:127], v[2:7], 0 cbsz:2 blgp:2
	v_mfma_f32_16x16x128_f8f6f4 v[138:141], v[122:127], v[14:19], 0 cbsz:2 blgp:2
	v_mfma_f32_16x16x128_f8f6f4 v[142:145], v[122:127], v[26:31], v[188:191] cbsz:2 blgp:2
	v_mfma_f32_16x16x128_f8f6f4 v[204:207], v[122:127], v[38:43], 0 cbsz:2 blgp:2
	v_mfma_f32_16x16x128_f8f6f4 v[208:211], v[122:127], v[50:55], 0 cbsz:2 blgp:2
	v_mfma_f32_16x16x128_f8f6f4 v[212:215], v[122:127], v[62:67], v[188:191] cbsz:2 blgp:2
	s_waitcnt lgkmcnt(0)
	v_mfma_f32_16x16x128_f8f6f4 v[134:137], v[128:133], v[8:13], v[134:137] cbsz:2 blgp:2
	v_mfma_f32_16x16x128_f8f6f4 v[204:207], v[128:133], v[44:49], v[204:207] cbsz:2 blgp:2
	v_mfma_f32_16x16x128_f8f6f4 v[138:141], v[128:133], v[20:25], v[138:141] cbsz:2 blgp:2
	v_mfma_f32_16x16x128_f8f6f4 v[208:211], v[128:133], v[56:61], v[208:211] cbsz:2 blgp:2
	v_mfma_f32_16x16x128_f8f6f4 v[142:145], v[128:133], v[32:37], v[142:145] cbsz:2 blgp:2
	v_mfma_f32_16x16x128_f8f6f4 v[212:215], v[128:133], v[68:73], v[212:215] cbsz:2 blgp:2
	v_cndmask_b32_e64 v158, v134, v204, s[4:5]
	v_fma_mix_f32 v158, v158, v1, v83 op_sel:[0,0,1] op_sel_hi:[0,0,1]
	v_exp_f32_e32 v158, v158
	v_cndmask_b32_e64 v159, v138, v208, s[4:5]
	v_fma_mix_f32 v159, v159, v99, v75 op_sel:[0,0,1] op_sel_hi:[0,0,1]
	v_exp_f32_e32 v159, v159
	v_fma_f32 v158, v158, v186, v186
	v_rcp_f32_e32 v158, v158
	v_add_f32_e32 v159, 1.0, v159
	v_rcp_f32_e32 v159, v159
	v_cndmask_b32_e64 v160, v142, v212, s[4:5]
	v_fma_mix_f32 v161, v158, v160, v79 op_sel:[0,0,1] op_sel_hi:[0,0,1]
	v_exp_f32_e32 v161, v161
	s_add_u32 s48, s48, s40
	v_add_f32_e32 v161, 1.0, v161
	v_rcp_f32_e32 v161, v161
	s_addc_u32 s49, s49, s41
	v_fma_f32 v162, v161, -2.0, 1.0
	v_sub_f32_e32 v163, v176, v162
	v_fma_f32 v176, v159, v163, v162
	v_fma_f32 v164, |v176|, s16, v117
	v_fma_f32 v165, |v176|, s17, v118
	v_fma_f32 v166, |v176|, s18, v119
	v_lshrrev_b32_e32 v167, 26, v176
	v_min3_u32 v164, v164, v165, v166
	v_bfi_b32 v168, 31, v164, v167
	s_nop 1
	v_mul_u32_u24_dpp v170, v168, v180 quad_perm:[1,2,3,3] row_mask:0xf bank_mask:0xf bound_ctrl:1
	v_mad_u32_u24 v171, v168, v181, v170
	ds_write_b8_d16_hi v184, v171
	global_store_short_d16_hi v185, v176, s[48:49]
	s_waitcnt lgkmcnt(0)
	s_barrier
	ds_read_b64 v[122:123], v106 offset:0
	ds_read_b64 v[124:125], v106 offset:8
	ds_read_b64 v[126:127], v106 offset:16
	s_barrier
	ds_read_b64 v[128:129], v106 offset:96
	ds_read_b64 v[130:131], v106 offset:104
	ds_read_b64 v[132:133], v106 offset:112
	s_waitcnt lgkmcnt(3)
	v_mfma_f32_16x16x128_f8f6f4 v[134:137], v[122:127], v[2:7], 0 cbsz:2 blgp:2
	v_mfma_f32_16x16x128_f8f6f4 v[138:141], v[122:127], v[14:19], 0 cbsz:2 blgp:2
	v_mfma_f32_16x16x128_f8f6f4 v[142:145], v[122:127], v[26:31], v[188:191] cbsz:2 blgp:2
	v_mfma_f32_16x16x128_f8f6f4 v[204:207], v[122:127], v[38:43], 0 cbsz:2 blgp:2
	v_mfma_f32_16x16x128_f8f6f4 v[208:211], v[122:127], v[50:55], 0 cbsz:2 blgp:2
	v_mfma_f32_16x16x128_f8f6f4 v[212:215], v[122:127], v[62:67], v[188:191] cbsz:2 blgp:2
	s_waitcnt lgkmcnt(0)
	v_mfma_f32_16x16x128_f8f6f4 v[134:137], v[128:133], v[8:13], v[134:137] cbsz:2 blgp:2
	v_mfma_f32_16x16x128_f8f6f4 v[204:207], v[128:133], v[44:49], v[204:207] cbsz:2 blgp:2
	v_mfma_f32_16x16x128_f8f6f4 v[138:141], v[128:133], v[20:25], v[138:141] cbsz:2 blgp:2
	v_mfma_f32_16x16x128_f8f6f4 v[208:211], v[128:133], v[56:61], v[208:211] cbsz:2 blgp:2
	v_mfma_f32_16x16x128_f8f6f4 v[142:145], v[128:133], v[32:37], v[142:145] cbsz:2 blgp:2
	v_mfma_f32_16x16x128_f8f6f4 v[212:215], v[128:133], v[68:73], v[212:215] cbsz:2 blgp:2
	v_cndmask_b32_e64 v158, v134, v204, s[4:5]
	v_fma_mix_f32 v158, v158, v1, v84 op_sel_hi:[0,0,1]
	v_exp_f32_e32 v158, v158
	v_cndmask_b32_e64 v159, v138, v208, s[4:5]
	v_fma_mix_f32 v159, v159, v99, v76 op_sel_hi:[0,0,1]
	v_exp_f32_e32 v159, v159
	v_fma_f32 v158, v158, v186, v186
	v_rcp_f32_e32 v158, v158
	v_add_f32_e32 v159, 1.0, v159
	v_rcp_f32_e32 v159, v159
	v_cndmask_b32_e64 v160, v142, v212, s[4:5]
	v_fma_mix_f32 v161, v158, v160, v80 op_sel_hi:[0,0,1]
	v_exp_f32_e32 v161, v161
	s_add_u32 s48, s48, s40
	v_add_f32_e32 v161, 1.0, v161
	v_rcp_f32_e32 v161, v161
	s_addc_u32 s49, s49, s41
	v_fma_f32 v162, v161, -2.0, 1.0
	v_sub_f32_e32 v163, v176, v162
	v_fma_f32 v176, v159, v163, v162
	v_fma_f32 v164, |v176|, s16, v117
	v_fma_f32 v165, |v176|, s17, v118
	v_fma_f32 v166, |v176|, s18, v119
	v_lshrrev_b32_e32 v167, 26, v176
	v_min3_u32 v164, v164, v165, v166
	v_bfi_b32 v168, 31, v164, v167
	s_nop 1
	v_mul_u32_u24_dpp v170, v168, v180 quad_perm:[1,2,3,3] row_mask:0xf bank_mask:0xf bound_ctrl:1
	v_mad_u32_u24 v171, v168, v181, v170
	ds_write_b8_d16_hi v184, v171 offset:416
	global_store_short_d16_hi v185, v176, s[48:49]
	s_waitcnt lgkmcnt(0)
	s_barrier
	ds_read_b64 v[122:123], v106 offset:416
	ds_read_b64 v[124:125], v106 offset:424
	ds_read_b64 v[126:127], v106 offset:432
	s_barrier
	ds_read_b64 v[128:129], v106 offset:512
	ds_read_b64 v[130:131], v106 offset:520
	ds_read_b64 v[132:133], v106 offset:528
	s_waitcnt lgkmcnt(3)
	v_mfma_f32_16x16x128_f8f6f4 v[134:137], v[122:127], v[2:7], 0 cbsz:2 blgp:2
	v_mfma_f32_16x16x128_f8f6f4 v[138:141], v[122:127], v[14:19], 0 cbsz:2 blgp:2
	v_mfma_f32_16x16x128_f8f6f4 v[142:145], v[122:127], v[26:31], v[188:191] cbsz:2 blgp:2
	v_mfma_f32_16x16x128_f8f6f4 v[204:207], v[122:127], v[38:43], 0 cbsz:2 blgp:2
	v_mfma_f32_16x16x128_f8f6f4 v[208:211], v[122:127], v[50:55], 0 cbsz:2 blgp:2
	v_mfma_f32_16x16x128_f8f6f4 v[212:215], v[122:127], v[62:67], v[188:191] cbsz:2 blgp:2
	s_waitcnt lgkmcnt(0)
	v_mfma_f32_16x16x128_f8f6f4 v[134:137], v[128:133], v[8:13], v[134:137] cbsz:2 blgp:2
	v_mfma_f32_16x16x128_f8f6f4 v[204:207], v[128:133], v[44:49], v[204:207] cbsz:2 blgp:2
	v_mfma_f32_16x16x128_f8f6f4 v[138:141], v[128:133], v[20:25], v[138:141] cbsz:2 blgp:2
	v_mfma_f32_16x16x128_f8f6f4 v[208:211], v[128:133], v[56:61], v[208:211] cbsz:2 blgp:2
	v_mfma_f32_16x16x128_f8f6f4 v[142:145], v[128:133], v[32:37], v[142:145] cbsz:2 blgp:2
	v_mfma_f32_16x16x128_f8f6f4 v[212:215], v[128:133], v[68:73], v[212:215] cbsz:2 blgp:2
	v_cndmask_b32_e64 v158, v134, v204, s[4:5]
	v_fma_mix_f32 v158, v158, v1, v84 op_sel:[0,0,1] op_sel_hi:[0,0,1]
	v_exp_f32_e32 v158, v158
	v_cndmask_b32_e64 v159, v138, v208, s[4:5]
	v_fma_mix_f32 v159, v159, v99, v76 op_sel:[0,0,1] op_sel_hi:[0,0,1]
	v_exp_f32_e32 v159, v159
	v_fma_f32 v158, v158, v186, v186
	v_rcp_f32_e32 v158, v158
	v_add_f32_e32 v159, 1.0, v159
	v_rcp_f32_e32 v159, v159
	v_cndmask_b32_e64 v160, v142, v212, s[4:5]
	v_fma_mix_f32 v161, v158, v160, v80 op_sel:[0,0,1] op_sel_hi:[0,0,1]
	v_exp_f32_e32 v161, v161
	s_add_u32 s48, s48, s40
	v_add_f32_e32 v161, 1.0, v161
	v_rcp_f32_e32 v161, v161
	s_addc_u32 s49, s49, s41
	v_fma_f32 v162, v161, -2.0, 1.0
	v_sub_f32_e32 v163, v176, v162
	v_fma_f32 v176, v159, v163, v162
	v_fma_f32 v164, |v176|, s16, v117
	v_fma_f32 v165, |v176|, s17, v118
	v_fma_f32 v166, |v176|, s18, v119
	v_lshrrev_b32_e32 v167, 26, v176
	v_min3_u32 v164, v164, v165, v166
	v_bfi_b32 v168, 31, v164, v167
	s_nop 1
	v_mul_u32_u24_dpp v170, v168, v180 quad_perm:[1,2,3,3] row_mask:0xf bank_mask:0xf bound_ctrl:1
	v_mad_u32_u24 v171, v168, v181, v170
	ds_write_b8_d16_hi v184, v171
	global_store_short_d16_hi v185, v176, s[48:49]
	s_waitcnt lgkmcnt(0)
	s_barrier
	ds_read_b64 v[122:123], v106 offset:0
	ds_read_b64 v[124:125], v106 offset:8
	ds_read_b64 v[126:127], v106 offset:16
	s_barrier
	ds_read_b64 v[128:129], v106 offset:96
	ds_read_b64 v[130:131], v106 offset:104
	ds_read_b64 v[132:133], v106 offset:112
	s_waitcnt lgkmcnt(3)
	v_mfma_f32_16x16x128_f8f6f4 v[134:137], v[122:127], v[2:7], 0 cbsz:2 blgp:2
	v_mfma_f32_16x16x128_f8f6f4 v[138:141], v[122:127], v[14:19], 0 cbsz:2 blgp:2
	v_mfma_f32_16x16x128_f8f6f4 v[142:145], v[122:127], v[26:31], v[188:191] cbsz:2 blgp:2
	v_mfma_f32_16x16x128_f8f6f4 v[204:207], v[122:127], v[38:43], 0 cbsz:2 blgp:2
	v_mfma_f32_16x16x128_f8f6f4 v[208:211], v[122:127], v[50:55], 0 cbsz:2 blgp:2
	v_mfma_f32_16x16x128_f8f6f4 v[212:215], v[122:127], v[62:67], v[188:191] cbsz:2 blgp:2
	s_waitcnt lgkmcnt(0)
	v_mfma_f32_16x16x128_f8f6f4 v[134:137], v[128:133], v[8:13], v[134:137] cbsz:2 blgp:2
	v_mfma_f32_16x16x128_f8f6f4 v[204:207], v[128:133], v[44:49], v[204:207] cbsz:2 blgp:2
	v_mfma_f32_16x16x128_f8f6f4 v[138:141], v[128:133], v[20:25], v[138:141] cbsz:2 blgp:2
	v_mfma_f32_16x16x128_f8f6f4 v[208:211], v[128:133], v[56:61], v[208:211] cbsz:2 blgp:2
	v_mfma_f32_16x16x128_f8f6f4 v[142:145], v[128:133], v[32:37], v[142:145] cbsz:2 blgp:2
	v_mfma_f32_16x16x128_f8f6f4 v[212:215], v[128:133], v[68:73], v[212:215] cbsz:2 blgp:2
	v_cndmask_b32_e64 v158, v134, v204, s[4:5]
	v_fma_mix_f32 v158, v158, v1, v85 op_sel_hi:[0,0,1]
	v_exp_f32_e32 v158, v158
	v_cndmask_b32_e64 v159, v138, v208, s[4:5]
	v_fma_mix_f32 v159, v159, v99, v77 op_sel_hi:[0,0,1]
	v_exp_f32_e32 v159, v159
	v_fma_f32 v158, v158, v186, v186
	v_rcp_f32_e32 v158, v158
	v_add_f32_e32 v159, 1.0, v159
	v_rcp_f32_e32 v159, v159
	v_cndmask_b32_e64 v160, v142, v212, s[4:5]
	v_fma_mix_f32 v161, v158, v160, v81 op_sel_hi:[0,0,1]
	v_exp_f32_e32 v161, v161
	s_add_u32 s48, s48, s40
	v_add_f32_e32 v161, 1.0, v161
	v_rcp_f32_e32 v161, v161
	s_addc_u32 s49, s49, s41
	v_fma_f32 v162, v161, -2.0, 1.0
	v_sub_f32_e32 v163, v176, v162
	v_fma_f32 v176, v159, v163, v162
	v_fma_f32 v164, |v176|, s16, v117
	v_fma_f32 v165, |v176|, s17, v118
	v_fma_f32 v166, |v176|, s18, v119
	v_lshrrev_b32_e32 v167, 26, v176
	v_min3_u32 v164, v164, v165, v166
	v_bfi_b32 v168, 31, v164, v167
	s_nop 1
	v_mul_u32_u24_dpp v170, v168, v180 quad_perm:[1,2,3,3] row_mask:0xf bank_mask:0xf bound_ctrl:1
	v_mad_u32_u24 v171, v168, v181, v170
	ds_write_b8_d16_hi v184, v171 offset:416
	global_store_short_d16_hi v185, v176, s[48:49]
	s_waitcnt lgkmcnt(0)
	s_barrier
	ds_read_b64 v[122:123], v106 offset:416
	ds_read_b64 v[124:125], v106 offset:424
	ds_read_b64 v[126:127], v106 offset:432
	s_barrier
	ds_read_b64 v[128:129], v106 offset:512
	ds_read_b64 v[130:131], v106 offset:520
	ds_read_b64 v[132:133], v106 offset:528
	s_waitcnt lgkmcnt(3)
	v_mfma_f32_16x16x128_f8f6f4 v[134:137], v[122:127], v[2:7], 0 cbsz:2 blgp:2
	v_mfma_f32_16x16x128_f8f6f4 v[138:141], v[122:127], v[14:19], 0 cbsz:2 blgp:2
	v_mfma_f32_16x16x128_f8f6f4 v[142:145], v[122:127], v[26:31], v[188:191] cbsz:2 blgp:2
	v_mfma_f32_16x16x128_f8f6f4 v[204:207], v[122:127], v[38:43], 0 cbsz:2 blgp:2
	v_mfma_f32_16x16x128_f8f6f4 v[208:211], v[122:127], v[50:55], 0 cbsz:2 blgp:2
	v_mfma_f32_16x16x128_f8f6f4 v[212:215], v[122:127], v[62:67], v[188:191] cbsz:2 blgp:2
	s_waitcnt lgkmcnt(0)
	v_mfma_f32_16x16x128_f8f6f4 v[134:137], v[128:133], v[8:13], v[134:137] cbsz:2 blgp:2
	v_mfma_f32_16x16x128_f8f6f4 v[204:207], v[128:133], v[44:49], v[204:207] cbsz:2 blgp:2
	v_mfma_f32_16x16x128_f8f6f4 v[138:141], v[128:133], v[20:25], v[138:141] cbsz:2 blgp:2
	v_mfma_f32_16x16x128_f8f6f4 v[208:211], v[128:133], v[56:61], v[208:211] cbsz:2 blgp:2
	v_mfma_f32_16x16x128_f8f6f4 v[142:145], v[128:133], v[32:37], v[142:145] cbsz:2 blgp:2
	v_mfma_f32_16x16x128_f8f6f4 v[212:215], v[128:133], v[68:73], v[212:215] cbsz:2 blgp:2
	v_cndmask_b32_e64 v158, v134, v204, s[4:5]
	v_fma_mix_f32 v158, v158, v1, v85 op_sel:[0,0,1] op_sel_hi:[0,0,1]
	v_exp_f32_e32 v158, v158
	v_cndmask_b32_e64 v159, v138, v208, s[4:5]
	v_fma_mix_f32 v159, v159, v99, v77 op_sel:[0,0,1] op_sel_hi:[0,0,1]
	v_exp_f32_e32 v159, v159
	v_fma_f32 v158, v158, v186, v186
	v_rcp_f32_e32 v158, v158
	v_add_f32_e32 v159, 1.0, v159
	v_rcp_f32_e32 v159, v159
	v_cndmask_b32_e64 v160, v142, v212, s[4:5]
	v_fma_mix_f32 v161, v158, v160, v81 op_sel:[0,0,1] op_sel_hi:[0,0,1]
	v_exp_f32_e32 v161, v161
	s_add_u32 s48, s48, s40
	v_add_f32_e32 v161, 1.0, v161
	v_rcp_f32_e32 v161, v161
	s_addc_u32 s49, s49, s41
	v_fma_f32 v162, v161, -2.0, 1.0
	v_sub_f32_e32 v163, v176, v162
	v_fma_f32 v176, v159, v163, v162
	v_fma_f32 v164, |v176|, s16, v117
	v_fma_f32 v165, |v176|, s17, v118
	v_fma_f32 v166, |v176|, s18, v119
	v_lshrrev_b32_e32 v167, 26, v176
	v_min3_u32 v164, v164, v165, v166
	v_bfi_b32 v168, 31, v164, v167
	s_nop 1
	v_mul_u32_u24_dpp v170, v168, v180 quad_perm:[1,2,3,3] row_mask:0xf bank_mask:0xf bound_ctrl:1
	v_mad_u32_u24 v171, v168, v181, v170
	ds_write_b8_d16_hi v184, v171
	global_store_short_d16_hi v185, v176, s[48:49]
	s_waitcnt lgkmcnt(0)
	s_barrier
	ds_read_b64 v[122:123], v106 offset:0
	ds_read_b64 v[124:125], v106 offset:8
	ds_read_b64 v[126:127], v106 offset:16
	s_barrier
	ds_read_b64 v[128:129], v106 offset:96
	ds_read_b64 v[130:131], v106 offset:104
	ds_read_b64 v[132:133], v106 offset:112
	s_waitcnt vmcnt(8)
	global_load_dwordx4 v[82:85], v[196:197], off
	global_load_dwordx4 v[74:77], v[196:197], off offset:512
	global_load_dwordx4 v[78:81], v[196:197], off offset:1024
	v_lshl_add_u64 v[196:197], v[196:197], 0, s[42:43]
	s_waitcnt lgkmcnt(3)
	v_mfma_f32_16x16x128_f8f6f4 v[134:137], v[122:127], v[2:7], 0 cbsz:2 blgp:2
	v_mfma_f32_16x16x128_f8f6f4 v[138:141], v[122:127], v[14:19], 0 cbsz:2 blgp:2
	v_mfma_f32_16x16x128_f8f6f4 v[142:145], v[122:127], v[26:31], v[188:191] cbsz:2 blgp:2
	v_mfma_f32_16x16x128_f8f6f4 v[204:207], v[122:127], v[38:43], 0 cbsz:2 blgp:2
	v_mfma_f32_16x16x128_f8f6f4 v[208:211], v[122:127], v[50:55], 0 cbsz:2 blgp:2
	v_mfma_f32_16x16x128_f8f6f4 v[212:215], v[122:127], v[62:67], v[188:191] cbsz:2 blgp:2
	s_waitcnt lgkmcnt(0)
	v_mfma_f32_16x16x128_f8f6f4 v[134:137], v[128:133], v[8:13], v[134:137] cbsz:2 blgp:2
	v_mfma_f32_16x16x128_f8f6f4 v[204:207], v[128:133], v[44:49], v[204:207] cbsz:2 blgp:2
	v_mfma_f32_16x16x128_f8f6f4 v[138:141], v[128:133], v[20:25], v[138:141] cbsz:2 blgp:2
	v_mfma_f32_16x16x128_f8f6f4 v[208:211], v[128:133], v[56:61], v[208:211] cbsz:2 blgp:2
	v_mfma_f32_16x16x128_f8f6f4 v[142:145], v[128:133], v[32:37], v[142:145] cbsz:2 blgp:2
	v_mfma_f32_16x16x128_f8f6f4 v[212:215], v[128:133], v[68:73], v[212:215] cbsz:2 blgp:2
	v_cndmask_b32_e64 v158, v134, v204, s[4:5]
	v_fma_mix_f32 v158, v158, v1, v146 op_sel_hi:[0,0,1]
	v_exp_f32_e32 v158, v158
	v_cndmask_b32_e64 v159, v138, v208, s[4:5]
	v_fma_mix_f32 v159, v159, v99, v150 op_sel_hi:[0,0,1]
	v_exp_f32_e32 v159, v159
	v_fma_f32 v158, v158, v186, v186
	v_rcp_f32_e32 v158, v158
	v_add_f32_e32 v159, 1.0, v159
	v_rcp_f32_e32 v159, v159
	v_cndmask_b32_e64 v160, v142, v212, s[4:5]
	v_fma_mix_f32 v161, v158, v160, v154 op_sel_hi:[0,0,1]
	v_exp_f32_e32 v161, v161
	s_add_u32 s48, s48, s40
	v_add_f32_e32 v161, 1.0, v161
	v_rcp_f32_e32 v161, v161
	s_addc_u32 s49, s49, s41
	v_fma_f32 v162, v161, -2.0, 1.0
	v_sub_f32_e32 v163, v176, v162
	v_fma_f32 v176, v159, v163, v162
	v_fma_f32 v164, |v176|, s16, v117
	v_fma_f32 v165, |v176|, s17, v118
	v_fma_f32 v166, |v176|, s18, v119
	v_lshrrev_b32_e32 v167, 26, v176
	v_min3_u32 v164, v164, v165, v166
	v_bfi_b32 v168, 31, v164, v167
	s_nop 1
	v_mul_u32_u24_dpp v170, v168, v180 quad_perm:[1,2,3,3] row_mask:0xf bank_mask:0xf bound_ctrl:1
	v_mad_u32_u24 v171, v168, v181, v170
	ds_write_b8_d16_hi v184, v171 offset:416
	global_store_short_d16_hi v185, v176, s[48:49]
	s_waitcnt lgkmcnt(0)
	s_barrier
	ds_read_b64 v[122:123], v106 offset:416
	ds_read_b64 v[124:125], v106 offset:424
	ds_read_b64 v[126:127], v106 offset:432
	s_barrier
	ds_read_b64 v[128:129], v106 offset:512
	ds_read_b64 v[130:131], v106 offset:520
	ds_read_b64 v[132:133], v106 offset:528
	s_waitcnt lgkmcnt(3)
	v_mfma_f32_16x16x128_f8f6f4 v[134:137], v[122:127], v[2:7], 0 cbsz:2 blgp:2
	v_mfma_f32_16x16x128_f8f6f4 v[138:141], v[122:127], v[14:19], 0 cbsz:2 blgp:2
	v_mfma_f32_16x16x128_f8f6f4 v[142:145], v[122:127], v[26:31], v[188:191] cbsz:2 blgp:2
	v_mfma_f32_16x16x128_f8f6f4 v[204:207], v[122:127], v[38:43], 0 cbsz:2 blgp:2
	v_mfma_f32_16x16x128_f8f6f4 v[208:211], v[122:127], v[50:55], 0 cbsz:2 blgp:2
	v_mfma_f32_16x16x128_f8f6f4 v[212:215], v[122:127], v[62:67], v[188:191] cbsz:2 blgp:2
	s_waitcnt lgkmcnt(0)
	v_mfma_f32_16x16x128_f8f6f4 v[134:137], v[128:133], v[8:13], v[134:137] cbsz:2 blgp:2
	v_mfma_f32_16x16x128_f8f6f4 v[204:207], v[128:133], v[44:49], v[204:207] cbsz:2 blgp:2
	v_mfma_f32_16x16x128_f8f6f4 v[138:141], v[128:133], v[20:25], v[138:141] cbsz:2 blgp:2
	v_mfma_f32_16x16x128_f8f6f4 v[208:211], v[128:133], v[56:61], v[208:211] cbsz:2 blgp:2
	v_mfma_f32_16x16x128_f8f6f4 v[142:145], v[128:133], v[32:37], v[142:145] cbsz:2 blgp:2
	v_mfma_f32_16x16x128_f8f6f4 v[212:215], v[128:133], v[68:73], v[212:215] cbsz:2 blgp:2
	v_cndmask_b32_e64 v158, v134, v204, s[4:5]
	v_fma_mix_f32 v158, v158, v1, v146 op_sel:[0,0,1] op_sel_hi:[0,0,1]
	v_exp_f32_e32 v158, v158
	v_cndmask_b32_e64 v159, v138, v208, s[4:5]
	v_fma_mix_f32 v159, v159, v99, v150 op_sel:[0,0,1] op_sel_hi:[0,0,1]
	v_exp_f32_e32 v159, v159
	v_fma_f32 v158, v158, v186, v186
	v_rcp_f32_e32 v158, v158
	v_add_f32_e32 v159, 1.0, v159
	v_rcp_f32_e32 v159, v159
	v_cndmask_b32_e64 v160, v142, v212, s[4:5]
	v_fma_mix_f32 v161, v158, v160, v154 op_sel:[0,0,1] op_sel_hi:[0,0,1]
	v_exp_f32_e32 v161, v161
	s_add_u32 s48, s48, s40
	v_add_f32_e32 v161, 1.0, v161
	v_rcp_f32_e32 v161, v161
	s_addc_u32 s49, s49, s41
	v_fma_f32 v162, v161, -2.0, 1.0
	v_sub_f32_e32 v163, v176, v162
	v_fma_f32 v176, v159, v163, v162
	v_fma_f32 v164, |v176|, s16, v117
	v_fma_f32 v165, |v176|, s17, v118
	v_fma_f32 v166, |v176|, s18, v119
	v_lshrrev_b32_e32 v167, 26, v176
	v_min3_u32 v164, v164, v165, v166
	v_bfi_b32 v168, 31, v164, v167
	s_nop 1
	v_mul_u32_u24_dpp v170, v168, v180 quad_perm:[1,2,3,3] row_mask:0xf bank_mask:0xf bound_ctrl:1
	v_mad_u32_u24 v171, v168, v181, v170
	ds_write_b8_d16_hi v184, v171
	global_store_short_d16_hi v185, v176, s[48:49]
	s_waitcnt lgkmcnt(0)
	s_barrier
	ds_read_b64 v[122:123], v106 offset:0
	ds_read_b64 v[124:125], v106 offset:8
	ds_read_b64 v[126:127], v106 offset:16
	s_barrier
	ds_read_b64 v[128:129], v106 offset:96
	ds_read_b64 v[130:131], v106 offset:104
	ds_read_b64 v[132:133], v106 offset:112
	s_waitcnt lgkmcnt(3)
	v_mfma_f32_16x16x128_f8f6f4 v[134:137], v[122:127], v[2:7], 0 cbsz:2 blgp:2
	v_mfma_f32_16x16x128_f8f6f4 v[138:141], v[122:127], v[14:19], 0 cbsz:2 blgp:2
	v_mfma_f32_16x16x128_f8f6f4 v[142:145], v[122:127], v[26:31], v[188:191] cbsz:2 blgp:2
	v_mfma_f32_16x16x128_f8f6f4 v[204:207], v[122:127], v[38:43], 0 cbsz:2 blgp:2
	v_mfma_f32_16x16x128_f8f6f4 v[208:211], v[122:127], v[50:55], 0 cbsz:2 blgp:2
	v_mfma_f32_16x16x128_f8f6f4 v[212:215], v[122:127], v[62:67], v[188:191] cbsz:2 blgp:2
	s_waitcnt lgkmcnt(0)
	v_mfma_f32_16x16x128_f8f6f4 v[134:137], v[128:133], v[8:13], v[134:137] cbsz:2 blgp:2
	v_mfma_f32_16x16x128_f8f6f4 v[204:207], v[128:133], v[44:49], v[204:207] cbsz:2 blgp:2
	v_mfma_f32_16x16x128_f8f6f4 v[138:141], v[128:133], v[20:25], v[138:141] cbsz:2 blgp:2
	v_mfma_f32_16x16x128_f8f6f4 v[208:211], v[128:133], v[56:61], v[208:211] cbsz:2 blgp:2
	v_mfma_f32_16x16x128_f8f6f4 v[142:145], v[128:133], v[32:37], v[142:145] cbsz:2 blgp:2
	v_mfma_f32_16x16x128_f8f6f4 v[212:215], v[128:133], v[68:73], v[212:215] cbsz:2 blgp:2
	v_cndmask_b32_e64 v158, v134, v204, s[4:5]
	v_fma_mix_f32 v158, v158, v1, v147 op_sel_hi:[0,0,1]
	v_exp_f32_e32 v158, v158
	v_cndmask_b32_e64 v159, v138, v208, s[4:5]
	v_fma_mix_f32 v159, v159, v99, v151 op_sel_hi:[0,0,1]
	v_exp_f32_e32 v159, v159
	v_fma_f32 v158, v158, v186, v186
	v_rcp_f32_e32 v158, v158
	v_add_f32_e32 v159, 1.0, v159
	v_rcp_f32_e32 v159, v159
	v_cndmask_b32_e64 v160, v142, v212, s[4:5]
	v_fma_mix_f32 v161, v158, v160, v155 op_sel_hi:[0,0,1]
	v_exp_f32_e32 v161, v161
	s_add_u32 s48, s48, s40
	v_add_f32_e32 v161, 1.0, v161
	v_rcp_f32_e32 v161, v161
	s_addc_u32 s49, s49, s41
	v_fma_f32 v162, v161, -2.0, 1.0
	v_sub_f32_e32 v163, v176, v162
	v_fma_f32 v176, v159, v163, v162
	v_fma_f32 v164, |v176|, s16, v117
	v_fma_f32 v165, |v176|, s17, v118
	v_fma_f32 v166, |v176|, s18, v119
	v_lshrrev_b32_e32 v167, 26, v176
	v_min3_u32 v164, v164, v165, v166
	v_bfi_b32 v168, 31, v164, v167
	s_nop 1
	v_mul_u32_u24_dpp v170, v168, v180 quad_perm:[1,2,3,3] row_mask:0xf bank_mask:0xf bound_ctrl:1
	v_mad_u32_u24 v171, v168, v181, v170
	ds_write_b8_d16_hi v184, v171 offset:416
	global_store_short_d16_hi v185, v176, s[48:49]
	s_waitcnt lgkmcnt(0)
	s_barrier
	ds_read_b64 v[122:123], v106 offset:416
	ds_read_b64 v[124:125], v106 offset:424
	ds_read_b64 v[126:127], v106 offset:432
	s_barrier
	ds_read_b64 v[128:129], v106 offset:512
	ds_read_b64 v[130:131], v106 offset:520
	ds_read_b64 v[132:133], v106 offset:528
	s_waitcnt lgkmcnt(3)
	v_mfma_f32_16x16x128_f8f6f4 v[134:137], v[122:127], v[2:7], 0 cbsz:2 blgp:2
	v_mfma_f32_16x16x128_f8f6f4 v[138:141], v[122:127], v[14:19], 0 cbsz:2 blgp:2
	v_mfma_f32_16x16x128_f8f6f4 v[142:145], v[122:127], v[26:31], v[188:191] cbsz:2 blgp:2
	v_mfma_f32_16x16x128_f8f6f4 v[204:207], v[122:127], v[38:43], 0 cbsz:2 blgp:2
	v_mfma_f32_16x16x128_f8f6f4 v[208:211], v[122:127], v[50:55], 0 cbsz:2 blgp:2
	v_mfma_f32_16x16x128_f8f6f4 v[212:215], v[122:127], v[62:67], v[188:191] cbsz:2 blgp:2
	s_waitcnt lgkmcnt(0)
	v_mfma_f32_16x16x128_f8f6f4 v[134:137], v[128:133], v[8:13], v[134:137] cbsz:2 blgp:2
	v_mfma_f32_16x16x128_f8f6f4 v[204:207], v[128:133], v[44:49], v[204:207] cbsz:2 blgp:2
	v_mfma_f32_16x16x128_f8f6f4 v[138:141], v[128:133], v[20:25], v[138:141] cbsz:2 blgp:2
	v_mfma_f32_16x16x128_f8f6f4 v[208:211], v[128:133], v[56:61], v[208:211] cbsz:2 blgp:2
	v_mfma_f32_16x16x128_f8f6f4 v[142:145], v[128:133], v[32:37], v[142:145] cbsz:2 blgp:2
	v_mfma_f32_16x16x128_f8f6f4 v[212:215], v[128:133], v[68:73], v[212:215] cbsz:2 blgp:2
	v_cndmask_b32_e64 v158, v134, v204, s[4:5]
	v_fma_mix_f32 v158, v158, v1, v147 op_sel:[0,0,1] op_sel_hi:[0,0,1]
	v_exp_f32_e32 v158, v158
	v_cndmask_b32_e64 v159, v138, v208, s[4:5]
	v_fma_mix_f32 v159, v159, v99, v151 op_sel:[0,0,1] op_sel_hi:[0,0,1]
	v_exp_f32_e32 v159, v159
	v_fma_f32 v158, v158, v186, v186
	v_rcp_f32_e32 v158, v158
	v_add_f32_e32 v159, 1.0, v159
	v_rcp_f32_e32 v159, v159
	v_cndmask_b32_e64 v160, v142, v212, s[4:5]
	v_fma_mix_f32 v161, v158, v160, v155 op_sel:[0,0,1] op_sel_hi:[0,0,1]
	v_exp_f32_e32 v161, v161
	s_add_u32 s48, s48, s40
	v_add_f32_e32 v161, 1.0, v161
	v_rcp_f32_e32 v161, v161
	s_addc_u32 s49, s49, s41
	v_fma_f32 v162, v161, -2.0, 1.0
	v_sub_f32_e32 v163, v176, v162
	v_fma_f32 v176, v159, v163, v162
	v_fma_f32 v164, |v176|, s16, v117
	v_fma_f32 v165, |v176|, s17, v118
	v_fma_f32 v166, |v176|, s18, v119
	v_lshrrev_b32_e32 v167, 26, v176
	v_min3_u32 v164, v164, v165, v166
	v_bfi_b32 v168, 31, v164, v167
	s_nop 1
	v_mul_u32_u24_dpp v170, v168, v180 quad_perm:[1,2,3,3] row_mask:0xf bank_mask:0xf bound_ctrl:1
	v_mad_u32_u24 v171, v168, v181, v170
	ds_write_b8_d16_hi v184, v171
	global_store_short_d16_hi v185, v176, s[48:49]
	s_waitcnt lgkmcnt(0)
	s_barrier
	ds_read_b64 v[122:123], v106 offset:0
	ds_read_b64 v[124:125], v106 offset:8
	ds_read_b64 v[126:127], v106 offset:16
	s_barrier
	ds_read_b64 v[128:129], v106 offset:96
	ds_read_b64 v[130:131], v106 offset:104
	ds_read_b64 v[132:133], v106 offset:112
	s_waitcnt lgkmcnt(3)
	v_mfma_f32_16x16x128_f8f6f4 v[134:137], v[122:127], v[2:7], 0 cbsz:2 blgp:2
	v_mfma_f32_16x16x128_f8f6f4 v[138:141], v[122:127], v[14:19], 0 cbsz:2 blgp:2
	v_mfma_f32_16x16x128_f8f6f4 v[142:145], v[122:127], v[26:31], v[188:191] cbsz:2 blgp:2
	v_mfma_f32_16x16x128_f8f6f4 v[204:207], v[122:127], v[38:43], 0 cbsz:2 blgp:2
	v_mfma_f32_16x16x128_f8f6f4 v[208:211], v[122:127], v[50:55], 0 cbsz:2 blgp:2
	v_mfma_f32_16x16x128_f8f6f4 v[212:215], v[122:127], v[62:67], v[188:191] cbsz:2 blgp:2
	s_waitcnt lgkmcnt(0)
	v_mfma_f32_16x16x128_f8f6f4 v[134:137], v[128:133], v[8:13], v[134:137] cbsz:2 blgp:2
	v_mfma_f32_16x16x128_f8f6f4 v[204:207], v[128:133], v[44:49], v[204:207] cbsz:2 blgp:2
	v_mfma_f32_16x16x128_f8f6f4 v[138:141], v[128:133], v[20:25], v[138:141] cbsz:2 blgp:2
	v_mfma_f32_16x16x128_f8f6f4 v[208:211], v[128:133], v[56:61], v[208:211] cbsz:2 blgp:2
	v_mfma_f32_16x16x128_f8f6f4 v[142:145], v[128:133], v[32:37], v[142:145] cbsz:2 blgp:2
	v_mfma_f32_16x16x128_f8f6f4 v[212:215], v[128:133], v[68:73], v[212:215] cbsz:2 blgp:2
	v_cndmask_b32_e64 v158, v134, v204, s[4:5]
	v_fma_mix_f32 v158, v158, v1, v148 op_sel_hi:[0,0,1]
	v_exp_f32_e32 v158, v158
	v_cndmask_b32_e64 v159, v138, v208, s[4:5]
	v_fma_mix_f32 v159, v159, v99, v152 op_sel_hi:[0,0,1]
	v_exp_f32_e32 v159, v159
	v_fma_f32 v158, v158, v186, v186
	v_rcp_f32_e32 v158, v158
	v_add_f32_e32 v159, 1.0, v159
	v_rcp_f32_e32 v159, v159
	v_cndmask_b32_e64 v160, v142, v212, s[4:5]
	v_fma_mix_f32 v161, v158, v160, v156 op_sel_hi:[0,0,1]
	v_exp_f32_e32 v161, v161
	s_add_u32 s48, s48, s40
	v_add_f32_e32 v161, 1.0, v161
	v_rcp_f32_e32 v161, v161
	s_addc_u32 s49, s49, s41
	v_fma_f32 v162, v161, -2.0, 1.0
	v_sub_f32_e32 v163, v176, v162
	v_fma_f32 v176, v159, v163, v162
	v_fma_f32 v164, |v176|, s16, v117
	v_fma_f32 v165, |v176|, s17, v118
	v_fma_f32 v166, |v176|, s18, v119
	v_lshrrev_b32_e32 v167, 26, v176
	v_min3_u32 v164, v164, v165, v166
	v_bfi_b32 v168, 31, v164, v167
	s_nop 1
	v_mul_u32_u24_dpp v170, v168, v180 quad_perm:[1,2,3,3] row_mask:0xf bank_mask:0xf bound_ctrl:1
	v_mad_u32_u24 v171, v168, v181, v170
	ds_write_b8_d16_hi v184, v171 offset:416
	global_store_short_d16_hi v185, v176, s[48:49]
	s_waitcnt lgkmcnt(0)
	s_barrier
	ds_read_b64 v[122:123], v106 offset:416
	ds_read_b64 v[124:125], v106 offset:424
	ds_read_b64 v[126:127], v106 offset:432
	s_barrier
	ds_read_b64 v[128:129], v106 offset:512
	ds_read_b64 v[130:131], v106 offset:520
	ds_read_b64 v[132:133], v106 offset:528
	s_waitcnt lgkmcnt(3)
	v_mfma_f32_16x16x128_f8f6f4 v[134:137], v[122:127], v[2:7], 0 cbsz:2 blgp:2
	v_mfma_f32_16x16x128_f8f6f4 v[138:141], v[122:127], v[14:19], 0 cbsz:2 blgp:2
	v_mfma_f32_16x16x128_f8f6f4 v[142:145], v[122:127], v[26:31], v[188:191] cbsz:2 blgp:2
	v_mfma_f32_16x16x128_f8f6f4 v[204:207], v[122:127], v[38:43], 0 cbsz:2 blgp:2
	v_mfma_f32_16x16x128_f8f6f4 v[208:211], v[122:127], v[50:55], 0 cbsz:2 blgp:2
	v_mfma_f32_16x16x128_f8f6f4 v[212:215], v[122:127], v[62:67], v[188:191] cbsz:2 blgp:2
	s_waitcnt lgkmcnt(0)
	v_mfma_f32_16x16x128_f8f6f4 v[134:137], v[128:133], v[8:13], v[134:137] cbsz:2 blgp:2
	v_mfma_f32_16x16x128_f8f6f4 v[204:207], v[128:133], v[44:49], v[204:207] cbsz:2 blgp:2
	v_mfma_f32_16x16x128_f8f6f4 v[138:141], v[128:133], v[20:25], v[138:141] cbsz:2 blgp:2
	v_mfma_f32_16x16x128_f8f6f4 v[208:211], v[128:133], v[56:61], v[208:211] cbsz:2 blgp:2
	v_mfma_f32_16x16x128_f8f6f4 v[142:145], v[128:133], v[32:37], v[142:145] cbsz:2 blgp:2
	v_mfma_f32_16x16x128_f8f6f4 v[212:215], v[128:133], v[68:73], v[212:215] cbsz:2 blgp:2
	v_cndmask_b32_e64 v158, v134, v204, s[4:5]
	v_fma_mix_f32 v158, v158, v1, v148 op_sel:[0,0,1] op_sel_hi:[0,0,1]
	v_exp_f32_e32 v158, v158
	v_cndmask_b32_e64 v159, v138, v208, s[4:5]
	v_fma_mix_f32 v159, v159, v99, v152 op_sel:[0,0,1] op_sel_hi:[0,0,1]
	v_exp_f32_e32 v159, v159
	v_fma_f32 v158, v158, v186, v186
	v_rcp_f32_e32 v158, v158
	v_add_f32_e32 v159, 1.0, v159
	v_rcp_f32_e32 v159, v159
	v_cndmask_b32_e64 v160, v142, v212, s[4:5]
	v_fma_mix_f32 v161, v158, v160, v156 op_sel:[0,0,1] op_sel_hi:[0,0,1]
	v_exp_f32_e32 v161, v161
	s_add_u32 s48, s48, s40
	v_add_f32_e32 v161, 1.0, v161
	v_rcp_f32_e32 v161, v161
	s_addc_u32 s49, s49, s41
	v_fma_f32 v162, v161, -2.0, 1.0
	v_sub_f32_e32 v163, v176, v162
	v_fma_f32 v176, v159, v163, v162
	v_fma_f32 v164, |v176|, s16, v117
	v_fma_f32 v165, |v176|, s17, v118
	v_fma_f32 v166, |v176|, s18, v119
	v_lshrrev_b32_e32 v167, 26, v176
	v_min3_u32 v164, v164, v165, v166
	v_bfi_b32 v168, 31, v164, v167
	s_nop 1
	v_mul_u32_u24_dpp v170, v168, v180 quad_perm:[1,2,3,3] row_mask:0xf bank_mask:0xf bound_ctrl:1
	v_mad_u32_u24 v171, v168, v181, v170
	ds_write_b8_d16_hi v184, v171
	global_store_short_d16_hi v185, v176, s[48:49]
	s_waitcnt lgkmcnt(0)
	s_barrier
	ds_read_b64 v[122:123], v106 offset:0
	ds_read_b64 v[124:125], v106 offset:8
	ds_read_b64 v[126:127], v106 offset:16
	s_barrier
	ds_read_b64 v[128:129], v106 offset:96
	ds_read_b64 v[130:131], v106 offset:104
	ds_read_b64 v[132:133], v106 offset:112
	s_waitcnt lgkmcnt(3)
	v_mfma_f32_16x16x128_f8f6f4 v[134:137], v[122:127], v[2:7], 0 cbsz:2 blgp:2
	v_mfma_f32_16x16x128_f8f6f4 v[138:141], v[122:127], v[14:19], 0 cbsz:2 blgp:2
	v_mfma_f32_16x16x128_f8f6f4 v[142:145], v[122:127], v[26:31], v[188:191] cbsz:2 blgp:2
	v_mfma_f32_16x16x128_f8f6f4 v[204:207], v[122:127], v[38:43], 0 cbsz:2 blgp:2
	v_mfma_f32_16x16x128_f8f6f4 v[208:211], v[122:127], v[50:55], 0 cbsz:2 blgp:2
	v_mfma_f32_16x16x128_f8f6f4 v[212:215], v[122:127], v[62:67], v[188:191] cbsz:2 blgp:2
	s_waitcnt lgkmcnt(0)
	v_mfma_f32_16x16x128_f8f6f4 v[134:137], v[128:133], v[8:13], v[134:137] cbsz:2 blgp:2
	v_mfma_f32_16x16x128_f8f6f4 v[204:207], v[128:133], v[44:49], v[204:207] cbsz:2 blgp:2
	v_mfma_f32_16x16x128_f8f6f4 v[138:141], v[128:133], v[20:25], v[138:141] cbsz:2 blgp:2
	v_mfma_f32_16x16x128_f8f6f4 v[208:211], v[128:133], v[56:61], v[208:211] cbsz:2 blgp:2
	v_mfma_f32_16x16x128_f8f6f4 v[142:145], v[128:133], v[32:37], v[142:145] cbsz:2 blgp:2
	v_mfma_f32_16x16x128_f8f6f4 v[212:215], v[128:133], v[68:73], v[212:215] cbsz:2 blgp:2
	v_cndmask_b32_e64 v158, v134, v204, s[4:5]
	v_fma_mix_f32 v158, v158, v1, v149 op_sel_hi:[0,0,1]
	v_exp_f32_e32 v158, v158
	v_cndmask_b32_e64 v159, v138, v208, s[4:5]
	v_fma_mix_f32 v159, v159, v99, v153 op_sel_hi:[0,0,1]
	v_exp_f32_e32 v159, v159
	v_fma_f32 v158, v158, v186, v186
	v_rcp_f32_e32 v158, v158
	v_add_f32_e32 v159, 1.0, v159
	v_rcp_f32_e32 v159, v159
	v_cndmask_b32_e64 v160, v142, v212, s[4:5]
	v_fma_mix_f32 v161, v158, v160, v157 op_sel_hi:[0,0,1]
	v_exp_f32_e32 v161, v161
	s_add_u32 s48, s48, s40
	v_add_f32_e32 v161, 1.0, v161
	v_rcp_f32_e32 v161, v161
	s_addc_u32 s49, s49, s41
	v_fma_f32 v162, v161, -2.0, 1.0
	v_sub_f32_e32 v163, v176, v162
	v_fma_f32 v176, v159, v163, v162
	v_fma_f32 v164, |v176|, s16, v117
	v_fma_f32 v165, |v176|, s17, v118
	v_fma_f32 v166, |v176|, s18, v119
	v_lshrrev_b32_e32 v167, 26, v176
	v_min3_u32 v164, v164, v165, v166
	v_bfi_b32 v168, 31, v164, v167
	s_nop 1
	v_mul_u32_u24_dpp v170, v168, v180 quad_perm:[1,2,3,3] row_mask:0xf bank_mask:0xf bound_ctrl:1
	v_mad_u32_u24 v171, v168, v181, v170
	ds_write_b8_d16_hi v184, v171 offset:416
	global_store_short_d16_hi v185, v176, s[48:49]
	s_waitcnt lgkmcnt(0)
	s_barrier
	ds_read_b64 v[122:123], v106 offset:416
	ds_read_b64 v[124:125], v106 offset:424
	ds_read_b64 v[126:127], v106 offset:432
	s_barrier
	ds_read_b64 v[128:129], v106 offset:512
	ds_read_b64 v[130:131], v106 offset:520
	ds_read_b64 v[132:133], v106 offset:528
	s_add_i32 s44, s44, 16
	s_waitcnt lgkmcnt(3)
	v_mfma_f32_16x16x128_f8f6f4 v[134:137], v[122:127], v[2:7], 0 cbsz:2 blgp:2
	v_mfma_f32_16x16x128_f8f6f4 v[138:141], v[122:127], v[14:19], 0 cbsz:2 blgp:2
	v_mfma_f32_16x16x128_f8f6f4 v[142:145], v[122:127], v[26:31], v[188:191] cbsz:2 blgp:2
	v_mfma_f32_16x16x128_f8f6f4 v[204:207], v[122:127], v[38:43], 0 cbsz:2 blgp:2
	v_mfma_f32_16x16x128_f8f6f4 v[208:211], v[122:127], v[50:55], 0 cbsz:2 blgp:2
	v_mfma_f32_16x16x128_f8f6f4 v[212:215], v[122:127], v[62:67], v[188:191] cbsz:2 blgp:2
	s_waitcnt lgkmcnt(0)
	v_mfma_f32_16x16x128_f8f6f4 v[134:137], v[128:133], v[8:13], v[134:137] cbsz:2 blgp:2
	v_mfma_f32_16x16x128_f8f6f4 v[204:207], v[128:133], v[44:49], v[204:207] cbsz:2 blgp:2
	v_mfma_f32_16x16x128_f8f6f4 v[138:141], v[128:133], v[20:25], v[138:141] cbsz:2 blgp:2
	v_mfma_f32_16x16x128_f8f6f4 v[208:211], v[128:133], v[56:61], v[208:211] cbsz:2 blgp:2
	v_mfma_f32_16x16x128_f8f6f4 v[142:145], v[128:133], v[32:37], v[142:145] cbsz:2 blgp:2
	v_mfma_f32_16x16x128_f8f6f4 v[212:215], v[128:133], v[68:73], v[212:215] cbsz:2 blgp:2
	v_cndmask_b32_e64 v158, v134, v204, s[4:5]
	v_fma_mix_f32 v158, v158, v1, v149 op_sel:[0,0,1] op_sel_hi:[0,0,1]
	v_exp_f32_e32 v158, v158
	v_cndmask_b32_e64 v159, v138, v208, s[4:5]
	v_fma_mix_f32 v159, v159, v99, v153 op_sel:[0,0,1] op_sel_hi:[0,0,1]
	v_exp_f32_e32 v159, v159
	v_fma_f32 v158, v158, v186, v186
	v_rcp_f32_e32 v158, v158
	v_add_f32_e32 v159, 1.0, v159
	v_rcp_f32_e32 v159, v159
	v_cndmask_b32_e64 v160, v142, v212, s[4:5]
	v_fma_mix_f32 v161, v158, v160, v157 op_sel:[0,0,1] op_sel_hi:[0,0,1]
	v_exp_f32_e32 v161, v161
	s_add_u32 s48, s48, s40
	v_add_f32_e32 v161, 1.0, v161
	v_rcp_f32_e32 v161, v161
	s_addc_u32 s49, s49, s41
	v_fma_f32 v162, v161, -2.0, 1.0
	v_sub_f32_e32 v163, v176, v162
	v_fma_f32 v176, v159, v163, v162
	v_fma_f32 v164, |v176|, s16, v117
	v_fma_f32 v165, |v176|, s17, v118
	v_fma_f32 v166, |v176|, s18, v119
	v_lshrrev_b32_e32 v167, 26, v176
	v_min3_u32 v164, v164, v165, v166
	v_bfi_b32 v168, 31, v164, v167
	s_nop 1
	v_mul_u32_u24_dpp v170, v168, v180 quad_perm:[1,2,3,3] row_mask:0xf bank_mask:0xf bound_ctrl:1
	v_mad_u32_u24 v171, v168, v181, v170
	ds_write_b8_d16_hi v184, v171
	global_store_short_d16_hi v185, v176, s[48:49]
	s_waitcnt lgkmcnt(0)
	s_barrier
	ds_read_b64 v[122:123], v106 offset:0
	ds_read_b64 v[124:125], v106 offset:8
	ds_read_b64 v[126:127], v106 offset:16
	s_cmp_lt_i32 s44, s45
	s_cbranch_scc1 .Lscan_loop_a_st
	s_barrier
	s_branch .Lscan_exit_st
.Lscan_entry_b_st:
	s_branch .Lscan_enter_b_st
	.p2align 6
.Lscan_loop_b_st:
	s_waitcnt lgkmcnt(0)
	s_barrier
.Lscan_enter_b_st:
	ds_read_b64 v[122:123], v106 offset:0
	ds_read_b64 v[124:125], v106 offset:8
	ds_read_b64 v[126:127], v106 offset:16
	ds_read_b64 v[128:129], v106 offset:96
	ds_read_b64 v[130:131], v106 offset:104
	ds_read_b64 v[132:133], v106 offset:112
	s_waitcnt vmcnt(8)
	global_load_dwordx4 v[146:149], v[196:197], off
	global_load_dwordx4 v[150:153], v[196:197], off offset:512
	global_load_dwordx4 v[154:157], v[196:197], off offset:1024
	v_lshl_add_u64 v[196:197], v[196:197], 0, s[42:43]
	s_waitcnt lgkmcnt(3)
	v_mfma_f32_16x16x128_f8f6f4 v[134:137], v[122:127], v[2:7], 0 cbsz:2 blgp:2
	v_mfma_f32_16x16x128_f8f6f4 v[138:141], v[122:127], v[14:19], 0 cbsz:2 blgp:2
	v_mfma_f32_16x16x128_f8f6f4 v[142:145], v[122:127], v[26:31], v[188:191] cbsz:2 blgp:2
	v_mfma_f32_16x16x128_f8f6f4 v[204:207], v[122:127], v[38:43], 0 cbsz:2 blgp:2
	v_mfma_f32_16x16x128_f8f6f4 v[208:211], v[122:127], v[50:55], 0 cbsz:2 blgp:2
	v_mfma_f32_16x16x128_f8f6f4 v[212:215], v[122:127], v[62:67], v[188:191] cbsz:2 blgp:2
	s_waitcnt lgkmcnt(0)
	v_mfma_f32_16x16x128_f8f6f4 v[134:137], v[128:133], v[8:13], v[134:137] cbsz:2 blgp:2
	v_mfma_f32_16x16x128_f8f6f4 v[204:207], v[128:133], v[44:49], v[204:207] cbsz:2 blgp:2
	v_mfma_f32_16x16x128_f8f6f4 v[138:141], v[128:133], v[20:25], v[138:141] cbsz:2 blgp:2
	v_mfma_f32_16x16x128_f8f6f4 v[208:211], v[128:133], v[56:61], v[208:211] cbsz:2 blgp:2
	v_mfma_f32_16x16x128_f8f6f4 v[142:145], v[128:133], v[32:37], v[142:145] cbsz:2 blgp:2
	v_mfma_f32_16x16x128_f8f6f4 v[212:215], v[128:133], v[68:73], v[212:215] cbsz:2 blgp:2
	v_cndmask_b32_e64 v158, v134, v204, s[4:5]
	v_fma_mix_f32 v158, v158, v1, v82 op_sel_hi:[0,0,1]
	v_exp_f32_e32 v158, v158
	v_cndmask_b32_e64 v159, v138, v208, s[4:5]
	v_fma_mix_f32 v159, v159, v99, v74 op_sel_hi:[0,0,1]
	v_exp_f32_e32 v159, v159
	v_fma_f32 v158, v158, v186, v186
	v_rcp_f32_e32 v158, v158
	v_add_f32_e32 v159, 1.0, v159
	v_rcp_f32_e32 v159, v159
	v_cndmask_b32_e64 v160, v142, v212, s[4:5]
	v_fma_mix_f32 v161, v158, v160, v78 op_sel_hi:[0,0,1]
	v_exp_f32_e32 v161, v161
	s_add_u32 s48, s48, s40
	v_add_f32_e32 v161, 1.0, v161
	v_rcp_f32_e32 v161, v161
	s_addc_u32 s49, s49, s41
	v_fma_f32 v162, v161, -2.0, 1.0
	v_sub_f32_e32 v163, v176, v162
	v_fma_f32 v176, v159, v163, v162
	v_fma_f32 v164, |v176|, s16, v117
	v_fma_f32 v165, |v176|, s17, v118
	v_fma_f32 v166, |v176|, s18, v119
	v_lshrrev_b32_e32 v167, 26, v176
	v_min3_u32 v164, v164, v165, v166
	v_bfi_b32 v168, 31, v164, v167
	s_nop 1
	v_mul_u32_u24_dpp v170, v168, v180 quad_perm:[1,2,3,3] row_mask:0xf bank_mask:0xf bound_ctrl:1
	v_mad_u32_u24 v171, v168, v181, v170
	ds_write_b8_d16_hi v184, v171 offset:416
	s_barrier
	global_store_short_d16_hi v185, v176, s[48:49]
	s_waitcnt lgkmcnt(0)
	s_barrier
	ds_read_b64 v[122:123], v106 offset:416
	ds_read_b64 v[124:125], v106 offset:424
	ds_read_b64 v[126:127], v106 offset:432
	ds_read_b64 v[128:129], v106 offset:512
	ds_read_b64 v[130:131], v106 offset:520
	ds_read_b64 v[132:133], v106 offset:528
	s_waitcnt lgkmcnt(3)
	v_mfma_f32_16x16x128_f8f6f4 v[134:137], v[122:127], v[2:7], 0 cbsz:2 blgp:2
	v_mfma_f32_16x16x128_f8f6f4 v[138:141], v[122:127], v[14:19], 0 cbsz:2 blgp:2
	v_mfma_f32_16x16x128_f8f6f4 v[142:145], v[122:127], v[26:31], v[188:191] cbsz:2 blgp:2
	v_mfma_f32_16x16x128_f8f6f4 v[204:207], v[122:127], v[38:43], 0 cbsz:2 blgp:2
	v_mfma_f32_16x16x128_f8f6f4 v[208:211], v[122:127], v[50:55], 0 cbsz:2 blgp:2
	v_mfma_f32_16x16x128_f8f6f4 v[212:215], v[122:127], v[62:67], v[188:191] cbsz:2 blgp:2
	s_waitcnt lgkmcnt(0)
	v_mfma_f32_16x16x128_f8f6f4 v[134:137], v[128:133], v[8:13], v[134:137] cbsz:2 blgp:2
	v_mfma_f32_16x16x128_f8f6f4 v[204:207], v[128:133], v[44:49], v[204:207] cbsz:2 blgp:2
	v_mfma_f32_16x16x128_f8f6f4 v[138:141], v[128:133], v[20:25], v[138:141] cbsz:2 blgp:2
	v_mfma_f32_16x16x128_f8f6f4 v[208:211], v[128:133], v[56:61], v[208:211] cbsz:2 blgp:2
	v_mfma_f32_16x16x128_f8f6f4 v[142:145], v[128:133], v[32:37], v[142:145] cbsz:2 blgp:2
	v_mfma_f32_16x16x128_f8f6f4 v[212:215], v[128:133], v[68:73], v[212:215] cbsz:2 blgp:2
	v_cndmask_b32_e64 v158, v134, v204, s[4:5]
	v_fma_mix_f32 v158, v158, v1, v82 op_sel:[0,0,1] op_sel_hi:[0,0,1]
	v_exp_f32_e32 v158, v158
	v_cndmask_b32_e64 v159, v138, v208, s[4:5]
	v_fma_mix_f32 v159, v159, v99, v74 op_sel:[0,0,1] op_sel_hi:[0,0,1]
	v_exp_f32_e32 v159, v159
	v_fma_f32 v158, v158, v186, v186
	v_rcp_f32_e32 v158, v158
	v_add_f32_e32 v159, 1.0, v159
	v_rcp_f32_e32 v159, v159
	v_cndmask_b32_e64 v160, v142, v212, s[4:5]
	v_fma_mix_f32 v161, v158, v160, v78 op_sel:[0,0,1] op_sel_hi:[0,0,1]
	v_exp_f32_e32 v161, v161
	s_add_u32 s48, s48, s40
	v_add_f32_e32 v161, 1.0, v161
	v_rcp_f32_e32 v161, v161
	s_addc_u32 s49, s49, s41
	v_fma_f32 v162, v161, -2.0, 1.0
	v_sub_f32_e32 v163, v176, v162
	v_fma_f32 v176, v159, v163, v162
	v_fma_f32 v164, |v176|, s16, v117
	v_fma_f32 v165, |v176|, s17, v118
	v_fma_f32 v166, |v176|, s18, v119
	v_lshrrev_b32_e32 v167, 26, v176
	v_min3_u32 v164, v164, v165, v166
	v_bfi_b32 v168, 31, v164, v167
	s_nop 1
	v_mul_u32_u24_dpp v170, v168, v180 quad_perm:[1,2,3,3] row_mask:0xf bank_mask:0xf bound_ctrl:1
	v_mad_u32_u24 v171, v168, v181, v170
	ds_write_b8_d16_hi v184, v171
	s_barrier
	global_store_short_d16_hi v185, v176, s[48:49]
	s_waitcnt lgkmcnt(0)
	s_barrier
	ds_read_b64 v[122:123], v106 offset:0
	ds_read_b64 v[124:125], v106 offset:8
	ds_read_b64 v[126:127], v106 offset:16
	ds_read_b64 v[128:129], v106 offset:96
	ds_read_b64 v[130:131], v106 offset:104
	ds_read_b64 v[132:133], v106 offset:112
	s_waitcnt lgkmcnt(3)
	v_mfma_f32_16x16x128_f8f6f4 v[134:137], v[122:127], v[2:7], 0 cbsz:2 blgp:2
	v_mfma_f32_16x16x128_f8f6f4 v[138:141], v[122:127], v[14:19], 0 cbsz:2 blgp:2
	v_mfma_f32_16x16x128_f8f6f4 v[142:145], v[122:127], v[26:31], v[188:191] cbsz:2 blgp:2
	v_mfma_f32_16x16x128_f8f6f4 v[204:207], v[122:127], v[38:43], 0 cbsz:2 blgp:2
	v_mfma_f32_16x16x128_f8f6f4 v[208:211], v[122:127], v[50:55], 0 cbsz:2 blgp:2
	v_mfma_f32_16x16x128_f8f6f4 v[212:215], v[122:127], v[62:67], v[188:191] cbsz:2 blgp:2
	s_waitcnt lgkmcnt(0)
	v_mfma_f32_16x16x128_f8f6f4 v[134:137], v[128:133], v[8:13], v[134:137] cbsz:2 blgp:2
	v_mfma_f32_16x16x128_f8f6f4 v[204:207], v[128:133], v[44:49], v[204:207] cbsz:2 blgp:2
	v_mfma_f32_16x16x128_f8f6f4 v[138:141], v[128:133], v[20:25], v[138:141] cbsz:2 blgp:2
	v_mfma_f32_16x16x128_f8f6f4 v[208:211], v[128:133], v[56:61], v[208:211] cbsz:2 blgp:2
	v_mfma_f32_16x16x128_f8f6f4 v[142:145], v[128:133], v[32:37], v[142:145] cbsz:2 blgp:2
	v_mfma_f32_16x16x128_f8f6f4 v[212:215], v[128:133], v[68:73], v[212:215] cbsz:2 blgp:2
	v_cndmask_b32_e64 v158, v134, v204, s[4:5]
	v_fma_mix_f32 v158, v158, v1, v83 op_sel_hi:[0,0,1]
	v_exp_f32_e32 v158, v158
	v_cndmask_b32_e64 v159, v138, v208, s[4:5]
	v_fma_mix_f32 v159, v159, v99, v75 op_sel_hi:[0,0,1]
	v_exp_f32_e32 v159, v159
	v_fma_f32 v158, v158, v186, v186
	v_rcp_f32_e32 v158, v158
	v_add_f32_e32 v159, 1.0, v159
	v_rcp_f32_e32 v159, v159
	v_cndmask_b32_e64 v160, v142, v212, s[4:5]
	v_fma_mix_f32 v161, v158, v160, v79 op_sel_hi:[0,0,1]
	v_exp_f32_e32 v161, v161
	s_add_u32 s48, s48, s40
	v_add_f32_e32 v161, 1.0, v161
	v_rcp_f32_e32 v161, v161
	s_addc_u32 s49, s49, s41
	v_fma_f32 v162, v161, -2.0, 1.0
	v_sub_f32_e32 v163, v176, v162
	v_fma_f32 v176, v159, v163, v162
	v_fma_f32 v164, |v176|, s16, v117
	v_fma_f32 v165, |v176|, s17, v118
	v_fma_f32 v166, |v176|, s18, v119
	v_lshrrev_b32_e32 v167, 26, v176
	v_min3_u32 v164, v164, v165, v166
	v_bfi_b32 v168, 31, v164, v167
	s_nop 1
	v_mul_u32_u24_dpp v170, v168, v180 quad_perm:[1,2,3,3] row_mask:0xf bank_mask:0xf bound_ctrl:1
	v_mad_u32_u24 v171, v168, v181, v170
	ds_write_b8_d16_hi v184, v171 offset:416
	s_barrier
	global_store_short_d16_hi v185, v176, s[48:49]
	s_waitcnt lgkmcnt(0)
	s_barrier
	ds_read_b64 v[122:123], v106 offset:416
	ds_read_b64 v[124:125], v106 offset:424
	ds_read_b64 v[126:127], v106 offset:432
	ds_read_b64 v[128:129], v106 offset:512
	ds_read_b64 v[130:131], v106 offset:520
	ds_read_b64 v[132:133], v106 offset:528
	s_waitcnt lgkmcnt(3)
	v_mfma_f32_16x16x128_f8f6f4 v[134:137], v[122:127], v[2:7], 0 cbsz:2 blgp:2
	v_mfma_f32_16x16x128_f8f6f4 v[138:141], v[122:127], v[14:19], 0 cbsz:2 blgp:2
	v_mfma_f32_16x16x128_f8f6f4 v[142:145], v[122:127], v[26:31], v[188:191] cbsz:2 blgp:2
	v_mfma_f32_16x16x128_f8f6f4 v[204:207], v[122:127], v[38:43], 0 cbsz:2 blgp:2
	v_mfma_f32_16x16x128_f8f6f4 v[208:211], v[122:127], v[50:55], 0 cbsz:2 blgp:2
	v_mfma_f32_16x16x128_f8f6f4 v[212:215], v[122:127], v[62:67], v[188:191] cbsz:2 blgp:2
	s_waitcnt lgkmcnt(0)
	v_mfma_f32_16x16x128_f8f6f4 v[134:137], v[128:133], v[8:13], v[134:137] cbsz:2 blgp:2
	v_mfma_f32_16x16x128_f8f6f4 v[204:207], v[128:133], v[44:49], v[204:207] cbsz:2 blgp:2
	v_mfma_f32_16x16x128_f8f6f4 v[138:141], v[128:133], v[20:25], v[138:141] cbsz:2 blgp:2
	v_mfma_f32_16x16x128_f8f6f4 v[208:211], v[128:133], v[56:61], v[208:211] cbsz:2 blgp:2
	v_mfma_f32_16x16x128_f8f6f4 v[142:145], v[128:133], v[32:37], v[142:145] cbsz:2 blgp:2
	v_mfma_f32_16x16x128_f8f6f4 v[212:215], v[128:133], v[68:73], v[212:215] cbsz:2 blgp:2
	v_cndmask_b32_e64 v158, v134, v204, s[4:5]
	v_fma_mix_f32 v158, v158, v1, v83 op_sel:[0,0,1] op_sel_hi:[0,0,1]
	v_exp_f32_e32 v158, v158
	v_cndmask_b32_e64 v159, v138, v208, s[4:5]
	v_fma_mix_f32 v159, v159, v99, v75 op_sel:[0,0,1] op_sel_hi:[0,0,1]
	v_exp_f32_e32 v159, v159
	v_fma_f32 v158, v158, v186, v186
	v_rcp_f32_e32 v158, v158
	v_add_f32_e32 v159, 1.0, v159
	v_rcp_f32_e32 v159, v159
	v_cndmask_b32_e64 v160, v142, v212, s[4:5]
	v_fma_mix_f32 v161, v158, v160, v79 op_sel:[0,0,1] op_sel_hi:[0,0,1]
	v_exp_f32_e32 v161, v161
	s_add_u32 s48, s48, s40
	v_add_f32_e32 v161, 1.0, v161
	v_rcp_f32_e32 v161, v161
	s_addc_u32 s49, s49, s41
	v_fma_f32 v162, v161, -2.0, 1.0
	v_sub_f32_e32 v163, v176, v162
	v_fma_f32 v176, v159, v163, v162
	v_fma_f32 v164, |v176|, s16, v117
	v_fma_f32 v165, |v176|, s17, v118
	v_fma_f32 v166, |v176|, s18, v119
	v_lshrrev_b32_e32 v167, 26, v176
	v_min3_u32 v164, v164, v165, v166
	v_bfi_b32 v168, 31, v164, v167
	s_nop 1
	v_mul_u32_u24_dpp v170, v168, v180 quad_perm:[1,2,3,3] row_mask:0xf bank_mask:0xf bound_ctrl:1
	v_mad_u32_u24 v171, v168, v181, v170
	ds_write_b8_d16_hi v184, v171
	s_barrier
	global_store_short_d16_hi v185, v176, s[48:49]
	s_waitcnt lgkmcnt(0)
	s_barrier
	ds_read_b64 v[122:123], v106 offset:0
	ds_read_b64 v[124:125], v106 offset:8
	ds_read_b64 v[126:127], v106 offset:16
	ds_read_b64 v[128:129], v106 offset:96
	ds_read_b64 v[130:131], v106 offset:104
	ds_read_b64 v[132:133], v106 offset:112
	s_waitcnt lgkmcnt(3)
	v_mfma_f32_16x16x128_f8f6f4 v[134:137], v[122:127], v[2:7], 0 cbsz:2 blgp:2
	v_mfma_f32_16x16x128_f8f6f4 v[138:141], v[122:127], v[14:19], 0 cbsz:2 blgp:2
	v_mfma_f32_16x16x128_f8f6f4 v[142:145], v[122:127], v[26:31], v[188:191] cbsz:2 blgp:2
	v_mfma_f32_16x16x128_f8f6f4 v[204:207], v[122:127], v[38:43], 0 cbsz:2 blgp:2
	v_mfma_f32_16x16x128_f8f6f4 v[208:211], v[122:127], v[50:55], 0 cbsz:2 blgp:2
	v_mfma_f32_16x16x128_f8f6f4 v[212:215], v[122:127], v[62:67], v[188:191] cbsz:2 blgp:2
	s_waitcnt lgkmcnt(0)
	v_mfma_f32_16x16x128_f8f6f4 v[134:137], v[128:133], v[8:13], v[134:137] cbsz:2 blgp:2
	v_mfma_f32_16x16x128_f8f6f4 v[204:207], v[128:133], v[44:49], v[204:207] cbsz:2 blgp:2
	v_mfma_f32_16x16x128_f8f6f4 v[138:141], v[128:133], v[20:25], v[138:141] cbsz:2 blgp:2
	v_mfma_f32_16x16x128_f8f6f4 v[208:211], v[128:133], v[56:61], v[208:211] cbsz:2 blgp:2
	v_mfma_f32_16x16x128_f8f6f4 v[142:145], v[128:133], v[32:37], v[142:145] cbsz:2 blgp:2
	v_mfma_f32_16x16x128_f8f6f4 v[212:215], v[128:133], v[68:73], v[212:215] cbsz:2 blgp:2
	v_cndmask_b32_e64 v158, v134, v204, s[4:5]
	v_fma_mix_f32 v158, v158, v1, v84 op_sel_hi:[0,0,1]
	v_exp_f32_e32 v158, v158
	v_cndmask_b32_e64 v159, v138, v208, s[4:5]
	v_fma_mix_f32 v159, v159, v99, v76 op_sel_hi:[0,0,1]
	v_exp_f32_e32 v159, v159
	v_fma_f32 v158, v158, v186, v186
	v_rcp_f32_e32 v158, v158
	v_add_f32_e32 v159, 1.0, v159
	v_rcp_f32_e32 v159, v159
	v_cndmask_b32_e64 v160, v142, v212, s[4:5]
	v_fma_mix_f32 v161, v158, v160, v80 op_sel_hi:[0,0,1]
	v_exp_f32_e32 v161, v161
	s_add_u32 s48, s48, s40
	v_add_f32_e32 v161, 1.0, v161
	v_rcp_f32_e32 v161, v161
	s_addc_u32 s49, s49, s41
	v_fma_f32 v162, v161, -2.0, 1.0
	v_sub_f32_e32 v163, v176, v162
	v_fma_f32 v176, v159, v163, v162
	v_fma_f32 v164, |v176|, s16, v117
	v_fma_f32 v165, |v176|, s17, v118
	v_fma_f32 v166, |v176|, s18, v119
	v_lshrrev_b32_e32 v167, 26, v176
	v_min3_u32 v164, v164, v165, v166
	v_bfi_b32 v168, 31, v164, v167
	s_nop 1
	v_mul_u32_u24_dpp v170, v168, v180 quad_perm:[1,2,3,3] row_mask:0xf bank_mask:0xf bound_ctrl:1
	v_mad_u32_u24 v171, v168, v181, v170
	ds_write_b8_d16_hi v184, v171 offset:416
	s_barrier
	global_store_short_d16_hi v185, v176, s[48:49]
	s_waitcnt lgkmcnt(0)
	s_barrier
	ds_read_b64 v[122:123], v106 offset:416
	ds_read_b64 v[124:125], v106 offset:424
	ds_read_b64 v[126:127], v106 offset:432
	ds_read_b64 v[128:129], v106 offset:512
	ds_read_b64 v[130:131], v106 offset:520
	ds_read_b64 v[132:133], v106 offset:528
	s_waitcnt lgkmcnt(3)
	v_mfma_f32_16x16x128_f8f6f4 v[134:137], v[122:127], v[2:7], 0 cbsz:2 blgp:2
	v_mfma_f32_16x16x128_f8f6f4 v[138:141], v[122:127], v[14:19], 0 cbsz:2 blgp:2
	v_mfma_f32_16x16x128_f8f6f4 v[142:145], v[122:127], v[26:31], v[188:191] cbsz:2 blgp:2
	v_mfma_f32_16x16x128_f8f6f4 v[204:207], v[122:127], v[38:43], 0 cbsz:2 blgp:2
	v_mfma_f32_16x16x128_f8f6f4 v[208:211], v[122:127], v[50:55], 0 cbsz:2 blgp:2
	v_mfma_f32_16x16x128_f8f6f4 v[212:215], v[122:127], v[62:67], v[188:191] cbsz:2 blgp:2
	s_waitcnt lgkmcnt(0)
	v_mfma_f32_16x16x128_f8f6f4 v[134:137], v[128:133], v[8:13], v[134:137] cbsz:2 blgp:2
	v_mfma_f32_16x16x128_f8f6f4 v[204:207], v[128:133], v[44:49], v[204:207] cbsz:2 blgp:2
	v_mfma_f32_16x16x128_f8f6f4 v[138:141], v[128:133], v[20:25], v[138:141] cbsz:2 blgp:2
	v_mfma_f32_16x16x128_f8f6f4 v[208:211], v[128:133], v[56:61], v[208:211] cbsz:2 blgp:2
	v_mfma_f32_16x16x128_f8f6f4 v[142:145], v[128:133], v[32:37], v[142:145] cbsz:2 blgp:2
	v_mfma_f32_16x16x128_f8f6f4 v[212:215], v[128:133], v[68:73], v[212:215] cbsz:2 blgp:2
	v_cndmask_b32_e64 v158, v134, v204, s[4:5]
	v_fma_mix_f32 v158, v158, v1, v84 op_sel:[0,0,1] op_sel_hi:[0,0,1]
	v_exp_f32_e32 v158, v158
	v_cndmask_b32_e64 v159, v138, v208, s[4:5]
	v_fma_mix_f32 v159, v159, v99, v76 op_sel:[0,0,1] op_sel_hi:[0,0,1]
	v_exp_f32_e32 v159, v159
	v_fma_f32 v158, v158, v186, v186
	v_rcp_f32_e32 v158, v158
	v_add_f32_e32 v159, 1.0, v159
	v_rcp_f32_e32 v159, v159
	v_cndmask_b32_e64 v160, v142, v212, s[4:5]
	v_fma_mix_f32 v161, v158, v160, v80 op_sel:[0,0,1] op_sel_hi:[0,0,1]
	v_exp_f32_e32 v161, v161
	s_add_u32 s48, s48, s40
	v_add_f32_e32 v161, 1.0, v161
	v_rcp_f32_e32 v161, v161
	s_addc_u32 s49, s49, s41
	v_fma_f32 v162, v161, -2.0, 1.0
	v_sub_f32_e32 v163, v176, v162
	v_fma_f32 v176, v159, v163, v162
	v_fma_f32 v164, |v176|, s16, v117
	v_fma_f32 v165, |v176|, s17, v118
	v_fma_f32 v166, |v176|, s18, v119
	v_lshrrev_b32_e32 v167, 26, v176
	v_min3_u32 v164, v164, v165, v166
	v_bfi_b32 v168, 31, v164, v167
	s_nop 1
	v_mul_u32_u24_dpp v170, v168, v180 quad_perm:[1,2,3,3] row_mask:0xf bank_mask:0xf bound_ctrl:1
	v_mad_u32_u24 v171, v168, v181, v170
	ds_write_b8_d16_hi v184, v171
	s_barrier
	global_store_short_d16_hi v185, v176, s[48:49]
	s_waitcnt lgkmcnt(0)
	s_barrier
	ds_read_b64 v[122:123], v106 offset:0
	ds_read_b64 v[124:125], v106 offset:8
	ds_read_b64 v[126:127], v106 offset:16
	ds_read_b64 v[128:129], v106 offset:96
	ds_read_b64 v[130:131], v106 offset:104
	ds_read_b64 v[132:133], v106 offset:112
	s_waitcnt lgkmcnt(3)
	v_mfma_f32_16x16x128_f8f6f4 v[134:137], v[122:127], v[2:7], 0 cbsz:2 blgp:2
	v_mfma_f32_16x16x128_f8f6f4 v[138:141], v[122:127], v[14:19], 0 cbsz:2 blgp:2
	v_mfma_f32_16x16x128_f8f6f4 v[142:145], v[122:127], v[26:31], v[188:191] cbsz:2 blgp:2
	v_mfma_f32_16x16x128_f8f6f4 v[204:207], v[122:127], v[38:43], 0 cbsz:2 blgp:2
	v_mfma_f32_16x16x128_f8f6f4 v[208:211], v[122:127], v[50:55], 0 cbsz:2 blgp:2
	v_mfma_f32_16x16x128_f8f6f4 v[212:215], v[122:127], v[62:67], v[188:191] cbsz:2 blgp:2
	s_waitcnt lgkmcnt(0)
	v_mfma_f32_16x16x128_f8f6f4 v[134:137], v[128:133], v[8:13], v[134:137] cbsz:2 blgp:2
	v_mfma_f32_16x16x128_f8f6f4 v[204:207], v[128:133], v[44:49], v[204:207] cbsz:2 blgp:2
	v_mfma_f32_16x16x128_f8f6f4 v[138:141], v[128:133], v[20:25], v[138:141] cbsz:2 blgp:2
	v_mfma_f32_16x16x128_f8f6f4 v[208:211], v[128:133], v[56:61], v[208:211] cbsz:2 blgp:2
	v_mfma_f32_16x16x128_f8f6f4 v[142:145], v[128:133], v[32:37], v[142:145] cbsz:2 blgp:2
	v_mfma_f32_16x16x128_f8f6f4 v[212:215], v[128:133], v[68:73], v[212:215] cbsz:2 blgp:2
	v_cndmask_b32_e64 v158, v134, v204, s[4:5]
	v_fma_mix_f32 v158, v158, v1, v85 op_sel_hi:[0,0,1]
	v_exp_f32_e32 v158, v158
	v_cndmask_b32_e64 v159, v138, v208, s[4:5]
	v_fma_mix_f32 v159, v159, v99, v77 op_sel_hi:[0,0,1]
	v_exp_f32_e32 v159, v159
	v_fma_f32 v158, v158, v186, v186
	v_rcp_f32_e32 v158, v158
	v_add_f32_e32 v159, 1.0, v159
	v_rcp_f32_e32 v159, v159
	v_cndmask_b32_e64 v160, v142, v212, s[4:5]
	v_fma_mix_f32 v161, v158, v160, v81 op_sel_hi:[0,0,1]
	v_exp_f32_e32 v161, v161
	s_add_u32 s48, s48, s40
	v_add_f32_e32 v161, 1.0, v161
	v_rcp_f32_e32 v161, v161
	s_addc_u32 s49, s49, s41
	v_fma_f32 v162, v161, -2.0, 1.0
	v_sub_f32_e32 v163, v176, v162
	v_fma_f32 v176, v159, v163, v162
	v_fma_f32 v164, |v176|, s16, v117
	v_fma_f32 v165, |v176|, s17, v118
	v_fma_f32 v166, |v176|, s18, v119
	v_lshrrev_b32_e32 v167, 26, v176
	v_min3_u32 v164, v164, v165, v166
	v_bfi_b32 v168, 31, v164, v167
	s_nop 1
	v_mul_u32_u24_dpp v170, v168, v180 quad_perm:[1,2,3,3] row_mask:0xf bank_mask:0xf bound_ctrl:1
	v_mad_u32_u24 v171, v168, v181, v170
	ds_write_b8_d16_hi v184, v171 offset:416
	s_barrier
	global_store_short_d16_hi v185, v176, s[48:49]
	s_waitcnt lgkmcnt(0)
	s_barrier
	ds_read_b64 v[122:123], v106 offset:416
	ds_read_b64 v[124:125], v106 offset:424
	ds_read_b64 v[126:127], v106 offset:432
	ds_read_b64 v[128:129], v106 offset:512
	ds_read_b64 v[130:131], v106 offset:520
	ds_read_b64 v[132:133], v106 offset:528
	s_waitcnt lgkmcnt(3)
	v_mfma_f32_16x16x128_f8f6f4 v[134:137], v[122:127], v[2:7], 0 cbsz:2 blgp:2
	v_mfma_f32_16x16x128_f8f6f4 v[138:141], v[122:127], v[14:19], 0 cbsz:2 blgp:2
	v_mfma_f32_16x16x128_f8f6f4 v[142:145], v[122:127], v[26:31], v[188:191] cbsz:2 blgp:2
	v_mfma_f32_16x16x128_f8f6f4 v[204:207], v[122:127], v[38:43], 0 cbsz:2 blgp:2
	v_mfma_f32_16x16x128_f8f6f4 v[208:211], v[122:127], v[50:55], 0 cbsz:2 blgp:2
	v_mfma_f32_16x16x128_f8f6f4 v[212:215], v[122:127], v[62:67], v[188:191] cbsz:2 blgp:2
	s_waitcnt lgkmcnt(0)
	v_mfma_f32_16x16x128_f8f6f4 v[134:137], v[128:133], v[8:13], v[134:137] cbsz:2 blgp:2
	v_mfma_f32_16x16x128_f8f6f4 v[204:207], v[128:133], v[44:49], v[204:207] cbsz:2 blgp:2
	v_mfma_f32_16x16x128_f8f6f4 v[138:141], v[128:133], v[20:25], v[138:141] cbsz:2 blgp:2
	v_mfma_f32_16x16x128_f8f6f4 v[208:211], v[128:133], v[56:61], v[208:211] cbsz:2 blgp:2
	v_mfma_f32_16x16x128_f8f6f4 v[142:145], v[128:133], v[32:37], v[142:145] cbsz:2 blgp:2
	v_mfma_f32_16x16x128_f8f6f4 v[212:215], v[128:133], v[68:73], v[212:215] cbsz:2 blgp:2
	v_cndmask_b32_e64 v158, v134, v204, s[4:5]
	v_fma_mix_f32 v158, v158, v1, v85 op_sel:[0,0,1] op_sel_hi:[0,0,1]
	v_exp_f32_e32 v158, v158
	v_cndmask_b32_e64 v159, v138, v208, s[4:5]
	v_fma_mix_f32 v159, v159, v99, v77 op_sel:[0,0,1] op_sel_hi:[0,0,1]
	v_exp_f32_e32 v159, v159
	v_fma_f32 v158, v158, v186, v186
	v_rcp_f32_e32 v158, v158
	v_add_f32_e32 v159, 1.0, v159
	v_rcp_f32_e32 v159, v159
	v_cndmask_b32_e64 v160, v142, v212, s[4:5]
	v_fma_mix_f32 v161, v158, v160, v81 op_sel:[0,0,1] op_sel_hi:[0,0,1]
	v_exp_f32_e32 v161, v161
	s_add_u32 s48, s48, s40
	v_add_f32_e32 v161, 1.0, v161
	v_rcp_f32_e32 v161, v161
	s_addc_u32 s49, s49, s41
	v_fma_f32 v162, v161, -2.0, 1.0
	v_sub_f32_e32 v163, v176, v162
	v_fma_f32 v176, v159, v163, v162
	v_fma_f32 v164, |v176|, s16, v117
	v_fma_f32 v165, |v176|, s17, v118
	v_fma_f32 v166, |v176|, s18, v119
	v_lshrrev_b32_e32 v167, 26, v176
	v_min3_u32 v164, v164, v165, v166
	v_bfi_b32 v168, 31, v164, v167
	s_nop 1
	v_mul_u32_u24_dpp v170, v168, v180 quad_perm:[1,2,3,3] row_mask:0xf bank_mask:0xf bound_ctrl:1
	v_mad_u32_u24 v171, v168, v181, v170
	ds_write_b8_d16_hi v184, v171
	s_barrier
	global_store_short_d16_hi v185, v176, s[48:49]
	s_waitcnt lgkmcnt(0)
	s_barrier
	ds_read_b64 v[122:123], v106 offset:0
	ds_read_b64 v[124:125], v106 offset:8
	ds_read_b64 v[126:127], v106 offset:16
	ds_read_b64 v[128:129], v106 offset:96
	ds_read_b64 v[130:131], v106 offset:104
	ds_read_b64 v[132:133], v106 offset:112
	s_waitcnt vmcnt(8)
	global_load_dwordx4 v[82:85], v[196:197], off
	global_load_dwordx4 v[74:77], v[196:197], off offset:512
	global_load_dwordx4 v[78:81], v[196:197], off offset:1024
	v_lshl_add_u64 v[196:197], v[196:197], 0, s[42:43]
	s_waitcnt lgkmcnt(3)
	v_mfma_f32_16x16x128_f8f6f4 v[134:137], v[122:127], v[2:7], 0 cbsz:2 blgp:2
	v_mfma_f32_16x16x128_f8f6f4 v[138:141], v[122:127], v[14:19], 0 cbsz:2 blgp:2
	v_mfma_f32_16x16x128_f8f6f4 v[142:145], v[122:127], v[26:31], v[188:191] cbsz:2 blgp:2
	v_mfma_f32_16x16x128_f8f6f4 v[204:207], v[122:127], v[38:43], 0 cbsz:2 blgp:2
	v_mfma_f32_16x16x128_f8f6f4 v[208:211], v[122:127], v[50:55], 0 cbsz:2 blgp:2
	v_mfma_f32_16x16x128_f8f6f4 v[212:215], v[122:127], v[62:67], v[188:191] cbsz:2 blgp:2
	s_waitcnt lgkmcnt(0)
	v_mfma_f32_16x16x128_f8f6f4 v[134:137], v[128:133], v[8:13], v[134:137] cbsz:2 blgp:2
	v_mfma_f32_16x16x128_f8f6f4 v[204:207], v[128:133], v[44:49], v[204:207] cbsz:2 blgp:2
	v_mfma_f32_16x16x128_f8f6f4 v[138:141], v[128:133], v[20:25], v[138:141] cbsz:2 blgp:2
	v_mfma_f32_16x16x128_f8f6f4 v[208:211], v[128:133], v[56:61], v[208:211] cbsz:2 blgp:2
	v_mfma_f32_16x16x128_f8f6f4 v[142:145], v[128:133], v[32:37], v[142:145] cbsz:2 blgp:2
	v_mfma_f32_16x16x128_f8f6f4 v[212:215], v[128:133], v[68:73], v[212:215] cbsz:2 blgp:2
	v_cndmask_b32_e64 v158, v134, v204, s[4:5]
	v_fma_mix_f32 v158, v158, v1, v146 op_sel_hi:[0,0,1]
	v_exp_f32_e32 v158, v158
	v_cndmask_b32_e64 v159, v138, v208, s[4:5]
	v_fma_mix_f32 v159, v159, v99, v150 op_sel_hi:[0,0,1]
	v_exp_f32_e32 v159, v159
	v_fma_f32 v158, v158, v186, v186
	v_rcp_f32_e32 v158, v158
	v_add_f32_e32 v159, 1.0, v159
	v_rcp_f32_e32 v159, v159
	v_cndmask_b32_e64 v160, v142, v212, s[4:5]
	v_fma_mix_f32 v161, v158, v160, v154 op_sel_hi:[0,0,1]
	v_exp_f32_e32 v161, v161
	s_add_u32 s48, s48, s40
	v_add_f32_e32 v161, 1.0, v161
	v_rcp_f32_e32 v161, v161
	s_addc_u32 s49, s49, s41
	v_fma_f32 v162, v161, -2.0, 1.0
	v_sub_f32_e32 v163, v176, v162
	v_fma_f32 v176, v159, v163, v162
	v_fma_f32 v164, |v176|, s16, v117
	v_fma_f32 v165, |v176|, s17, v118
	v_fma_f32 v166, |v176|, s18, v119
	v_lshrrev_b32_e32 v167, 26, v176
	v_min3_u32 v164, v164, v165, v166
	v_bfi_b32 v168, 31, v164, v167
	s_nop 1
	v_mul_u32_u24_dpp v170, v168, v180 quad_perm:[1,2,3,3] row_mask:0xf bank_mask:0xf bound_ctrl:1
	v_mad_u32_u24 v171, v168, v181, v170
	ds_write_b8_d16_hi v184, v171 offset:416
	s_barrier
	global_store_short_d16_hi v185, v176, s[48:49]
	s_waitcnt lgkmcnt(0)
	s_barrier
	ds_read_b64 v[122:123], v106 offset:416
	ds_read_b64 v[124:125], v106 offset:424
	ds_read_b64 v[126:127], v106 offset:432
	ds_read_b64 v[128:129], v106 offset:512
	ds_read_b64 v[130:131], v106 offset:520
	ds_read_b64 v[132:133], v106 offset:528
	s_waitcnt lgkmcnt(3)
	v_mfma_f32_16x16x128_f8f6f4 v[134:137], v[122:127], v[2:7], 0 cbsz:2 blgp:2
	v_mfma_f32_16x16x128_f8f6f4 v[138:141], v[122:127], v[14:19], 0 cbsz:2 blgp:2
	v_mfma_f32_16x16x128_f8f6f4 v[142:145], v[122:127], v[26:31], v[188:191] cbsz:2 blgp:2
	v_mfma_f32_16x16x128_f8f6f4 v[204:207], v[122:127], v[38:43], 0 cbsz:2 blgp:2
	v_mfma_f32_16x16x128_f8f6f4 v[208:211], v[122:127], v[50:55], 0 cbsz:2 blgp:2
	v_mfma_f32_16x16x128_f8f6f4 v[212:215], v[122:127], v[62:67], v[188:191] cbsz:2 blgp:2
	s_waitcnt lgkmcnt(0)
	v_mfma_f32_16x16x128_f8f6f4 v[134:137], v[128:133], v[8:13], v[134:137] cbsz:2 blgp:2
	v_mfma_f32_16x16x128_f8f6f4 v[204:207], v[128:133], v[44:49], v[204:207] cbsz:2 blgp:2
	v_mfma_f32_16x16x128_f8f6f4 v[138:141], v[128:133], v[20:25], v[138:141] cbsz:2 blgp:2
	v_mfma_f32_16x16x128_f8f6f4 v[208:211], v[128:133], v[56:61], v[208:211] cbsz:2 blgp:2
	v_mfma_f32_16x16x128_f8f6f4 v[142:145], v[128:133], v[32:37], v[142:145] cbsz:2 blgp:2
	v_mfma_f32_16x16x128_f8f6f4 v[212:215], v[128:133], v[68:73], v[212:215] cbsz:2 blgp:2
	v_cndmask_b32_e64 v158, v134, v204, s[4:5]
	v_fma_mix_f32 v158, v158, v1, v146 op_sel:[0,0,1] op_sel_hi:[0,0,1]
	v_exp_f32_e32 v158, v158
	v_cndmask_b32_e64 v159, v138, v208, s[4:5]
	v_fma_mix_f32 v159, v159, v99, v150 op_sel:[0,0,1] op_sel_hi:[0,0,1]
	v_exp_f32_e32 v159, v159
	v_fma_f32 v158, v158, v186, v186
	v_rcp_f32_e32 v158, v158
	v_add_f32_e32 v159, 1.0, v159
	v_rcp_f32_e32 v159, v159
	v_cndmask_b32_e64 v160, v142, v212, s[4:5]
	v_fma_mix_f32 v161, v158, v160, v154 op_sel:[0,0,1] op_sel_hi:[0,0,1]
	v_exp_f32_e32 v161, v161
	s_add_u32 s48, s48, s40
	v_add_f32_e32 v161, 1.0, v161
	v_rcp_f32_e32 v161, v161
	s_addc_u32 s49, s49, s41
	v_fma_f32 v162, v161, -2.0, 1.0
	v_sub_f32_e32 v163, v176, v162
	v_fma_f32 v176, v159, v163, v162
	v_fma_f32 v164, |v176|, s16, v117
	v_fma_f32 v165, |v176|, s17, v118
	v_fma_f32 v166, |v176|, s18, v119
	v_lshrrev_b32_e32 v167, 26, v176
	v_min3_u32 v164, v164, v165, v166
	v_bfi_b32 v168, 31, v164, v167
	s_nop 1
	v_mul_u32_u24_dpp v170, v168, v180 quad_perm:[1,2,3,3] row_mask:0xf bank_mask:0xf bound_ctrl:1
	v_mad_u32_u24 v171, v168, v181, v170
	ds_write_b8_d16_hi v184, v171
	s_barrier
	global_store_short_d16_hi v185, v176, s[48:49]
	s_waitcnt lgkmcnt(0)
	s_barrier
	ds_read_b64 v[122:123], v106 offset:0
	ds_read_b64 v[124:125], v106 offset:8
	ds_read_b64 v[126:127], v106 offset:16
	ds_read_b64 v[128:129], v106 offset:96
	ds_read_b64 v[130:131], v106 offset:104
	ds_read_b64 v[132:133], v106 offset:112
	s_waitcnt lgkmcnt(3)
	v_mfma_f32_16x16x128_f8f6f4 v[134:137], v[122:127], v[2:7], 0 cbsz:2 blgp:2
	v_mfma_f32_16x16x128_f8f6f4 v[138:141], v[122:127], v[14:19], 0 cbsz:2 blgp:2
	v_mfma_f32_16x16x128_f8f6f4 v[142:145], v[122:127], v[26:31], v[188:191] cbsz:2 blgp:2
	v_mfma_f32_16x16x128_f8f6f4 v[204:207], v[122:127], v[38:43], 0 cbsz:2 blgp:2
	v_mfma_f32_16x16x128_f8f6f4 v[208:211], v[122:127], v[50:55], 0 cbsz:2 blgp:2
	v_mfma_f32_16x16x128_f8f6f4 v[212:215], v[122:127], v[62:67], v[188:191] cbsz:2 blgp:2
	s_waitcnt lgkmcnt(0)
	v_mfma_f32_16x16x128_f8f6f4 v[134:137], v[128:133], v[8:13], v[134:137] cbsz:2 blgp:2
	v_mfma_f32_16x16x128_f8f6f4 v[204:207], v[128:133], v[44:49], v[204:207] cbsz:2 blgp:2
	v_mfma_f32_16x16x128_f8f6f4 v[138:141], v[128:133], v[20:25], v[138:141] cbsz:2 blgp:2
	v_mfma_f32_16x16x128_f8f6f4 v[208:211], v[128:133], v[56:61], v[208:211] cbsz:2 blgp:2
	v_mfma_f32_16x16x128_f8f6f4 v[142:145], v[128:133], v[32:37], v[142:145] cbsz:2 blgp:2
	v_mfma_f32_16x16x128_f8f6f4 v[212:215], v[128:133], v[68:73], v[212:215] cbsz:2 blgp:2
	v_cndmask_b32_e64 v158, v134, v204, s[4:5]
	v_fma_mix_f32 v158, v158, v1, v147 op_sel_hi:[0,0,1]
	v_exp_f32_e32 v158, v158
	v_cndmask_b32_e64 v159, v138, v208, s[4:5]
	v_fma_mix_f32 v159, v159, v99, v151 op_sel_hi:[0,0,1]
	v_exp_f32_e32 v159, v159
	v_fma_f32 v158, v158, v186, v186
	v_rcp_f32_e32 v158, v158
	v_add_f32_e32 v159, 1.0, v159
	v_rcp_f32_e32 v159, v159
	v_cndmask_b32_e64 v160, v142, v212, s[4:5]
	v_fma_mix_f32 v161, v158, v160, v155 op_sel_hi:[0,0,1]
	v_exp_f32_e32 v161, v161
	s_add_u32 s48, s48, s40
	v_add_f32_e32 v161, 1.0, v161
	v_rcp_f32_e32 v161, v161
	s_addc_u32 s49, s49, s41
	v_fma_f32 v162, v161, -2.0, 1.0
	v_sub_f32_e32 v163, v176, v162
	v_fma_f32 v176, v159, v163, v162
	v_fma_f32 v164, |v176|, s16, v117
	v_fma_f32 v165, |v176|, s17, v118
	v_fma_f32 v166, |v176|, s18, v119
	v_lshrrev_b32_e32 v167, 26, v176
	v_min3_u32 v164, v164, v165, v166
	v_bfi_b32 v168, 31, v164, v167
	s_nop 1
	v_mul_u32_u24_dpp v170, v168, v180 quad_perm:[1,2,3,3] row_mask:0xf bank_mask:0xf bound_ctrl:1
	v_mad_u32_u24 v171, v168, v181, v170
	ds_write_b8_d16_hi v184, v171 offset:416
	s_barrier
	global_store_short_d16_hi v185, v176, s[48:49]
	s_waitcnt lgkmcnt(0)
	s_barrier
	ds_read_b64 v[122:123], v106 offset:416
	ds_read_b64 v[124:125], v106 offset:424
	ds_read_b64 v[126:127], v106 offset:432
	ds_read_b64 v[128:129], v106 offset:512
	ds_read_b64 v[130:131], v106 offset:520
	ds_read_b64 v[132:133], v106 offset:528
	s_waitcnt lgkmcnt(3)
	v_mfma_f32_16x16x128_f8f6f4 v[134:137], v[122:127], v[2:7], 0 cbsz:2 blgp:2
	v_mfma_f32_16x16x128_f8f6f4 v[138:141], v[122:127], v[14:19], 0 cbsz:2 blgp:2
	v_mfma_f32_16x16x128_f8f6f4 v[142:145], v[122:127], v[26:31], v[188:191] cbsz:2 blgp:2
	v_mfma_f32_16x16x128_f8f6f4 v[204:207], v[122:127], v[38:43], 0 cbsz:2 blgp:2
	v_mfma_f32_16x16x128_f8f6f4 v[208:211], v[122:127], v[50:55], 0 cbsz:2 blgp:2
	v_mfma_f32_16x16x128_f8f6f4 v[212:215], v[122:127], v[62:67], v[188:191] cbsz:2 blgp:2
	s_waitcnt lgkmcnt(0)
	v_mfma_f32_16x16x128_f8f6f4 v[134:137], v[128:133], v[8:13], v[134:137] cbsz:2 blgp:2
	v_mfma_f32_16x16x128_f8f6f4 v[204:207], v[128:133], v[44:49], v[204:207] cbsz:2 blgp:2
	v_mfma_f32_16x16x128_f8f6f4 v[138:141], v[128:133], v[20:25], v[138:141] cbsz:2 blgp:2
	v_mfma_f32_16x16x128_f8f6f4 v[208:211], v[128:133], v[56:61], v[208:211] cbsz:2 blgp:2
	v_mfma_f32_16x16x128_f8f6f4 v[142:145], v[128:133], v[32:37], v[142:145] cbsz:2 blgp:2
	v_mfma_f32_16x16x128_f8f6f4 v[212:215], v[128:133], v[68:73], v[212:215] cbsz:2 blgp:2
	v_cndmask_b32_e64 v158, v134, v204, s[4:5]
	v_fma_mix_f32 v158, v158, v1, v147 op_sel:[0,0,1] op_sel_hi:[0,0,1]
	v_exp_f32_e32 v158, v158
	v_cndmask_b32_e64 v159, v138, v208, s[4:5]
	v_fma_mix_f32 v159, v159, v99, v151 op_sel:[0,0,1] op_sel_hi:[0,0,1]
	v_exp_f32_e32 v159, v159
	v_fma_f32 v158, v158, v186, v186
	v_rcp_f32_e32 v158, v158
	v_add_f32_e32 v159, 1.0, v159
	v_rcp_f32_e32 v159, v159
	v_cndmask_b32_e64 v160, v142, v212, s[4:5]
	v_fma_mix_f32 v161, v158, v160, v155 op_sel:[0,0,1] op_sel_hi:[0,0,1]
	v_exp_f32_e32 v161, v161
	s_add_u32 s48, s48, s40
	v_add_f32_e32 v161, 1.0, v161
	v_rcp_f32_e32 v161, v161
	s_addc_u32 s49, s49, s41
	v_fma_f32 v162, v161, -2.0, 1.0
	v_sub_f32_e32 v163, v176, v162
	v_fma_f32 v176, v159, v163, v162
	v_fma_f32 v164, |v176|, s16, v117
	v_fma_f32 v165, |v176|, s17, v118
	v_fma_f32 v166, |v176|, s18, v119
	v_lshrrev_b32_e32 v167, 26, v176
	v_min3_u32 v164, v164, v165, v166
	v_bfi_b32 v168, 31, v164, v167
	s_nop 1
	v_mul_u32_u24_dpp v170, v168, v180 quad_perm:[1,2,3,3] row_mask:0xf bank_mask:0xf bound_ctrl:1
	v_mad_u32_u24 v171, v168, v181, v170
	ds_write_b8_d16_hi v184, v171
	s_barrier
	global_store_short_d16_hi v185, v176, s[48:49]
	s_waitcnt lgkmcnt(0)
	s_barrier
	ds_read_b64 v[122:123], v106 offset:0
	ds_read_b64 v[124:125], v106 offset:8
	ds_read_b64 v[126:127], v106 offset:16
	ds_read_b64 v[128:129], v106 offset:96
	ds_read_b64 v[130:131], v106 offset:104
	ds_read_b64 v[132:133], v106 offset:112
	s_waitcnt lgkmcnt(3)
	v_mfma_f32_16x16x128_f8f6f4 v[134:137], v[122:127], v[2:7], 0 cbsz:2 blgp:2
	v_mfma_f32_16x16x128_f8f6f4 v[138:141], v[122:127], v[14:19], 0 cbsz:2 blgp:2
	v_mfma_f32_16x16x128_f8f6f4 v[142:145], v[122:127], v[26:31], v[188:191] cbsz:2 blgp:2
	v_mfma_f32_16x16x128_f8f6f4 v[204:207], v[122:127], v[38:43], 0 cbsz:2 blgp:2
	v_mfma_f32_16x16x128_f8f6f4 v[208:211], v[122:127], v[50:55], 0 cbsz:2 blgp:2
	v_mfma_f32_16x16x128_f8f6f4 v[212:215], v[122:127], v[62:67], v[188:191] cbsz:2 blgp:2
	s_waitcnt lgkmcnt(0)
	v_mfma_f32_16x16x128_f8f6f4 v[134:137], v[128:133], v[8:13], v[134:137] cbsz:2 blgp:2
	v_mfma_f32_16x16x128_f8f6f4 v[204:207], v[128:133], v[44:49], v[204:207] cbsz:2 blgp:2
	v_mfma_f32_16x16x128_f8f6f4 v[138:141], v[128:133], v[20:25], v[138:141] cbsz:2 blgp:2
	v_mfma_f32_16x16x128_f8f6f4 v[208:211], v[128:133], v[56:61], v[208:211] cbsz:2 blgp:2
	v_mfma_f32_16x16x128_f8f6f4 v[142:145], v[128:133], v[32:37], v[142:145] cbsz:2 blgp:2
	v_mfma_f32_16x16x128_f8f6f4 v[212:215], v[128:133], v[68:73], v[212:215] cbsz:2 blgp:2
	v_cndmask_b32_e64 v158, v134, v204, s[4:5]
	v_fma_mix_f32 v158, v158, v1, v148 op_sel_hi:[0,0,1]
	v_exp_f32_e32 v158, v158
	v_cndmask_b32_e64 v159, v138, v208, s[4:5]
	v_fma_mix_f32 v159, v159, v99, v152 op_sel_hi:[0,0,1]
	v_exp_f32_e32 v159, v159
	v_fma_f32 v158, v158, v186, v186
	v_rcp_f32_e32 v158, v158
	v_add_f32_e32 v159, 1.0, v159
	v_rcp_f32_e32 v159, v159
	v_cndmask_b32_e64 v160, v142, v212, s[4:5]
	v_fma_mix_f32 v161, v158, v160, v156 op_sel_hi:[0,0,1]
	v_exp_f32_e32 v161, v161
	s_add_u32 s48, s48, s40
	v_add_f32_e32 v161, 1.0, v161
	v_rcp_f32_e32 v161, v161
	s_addc_u32 s49, s49, s41
	v_fma_f32 v162, v161, -2.0, 1.0
	v_sub_f32_e32 v163, v176, v162
	v_fma_f32 v176, v159, v163, v162
	v_fma_f32 v164, |v176|, s16, v117
	v_fma_f32 v165, |v176|, s17, v118
	v_fma_f32 v166, |v176|, s18, v119
	v_lshrrev_b32_e32 v167, 26, v176
	v_min3_u32 v164, v164, v165, v166
	v_bfi_b32 v168, 31, v164, v167
	s_nop 1
	v_mul_u32_u24_dpp v170, v168, v180 quad_perm:[1,2,3,3] row_mask:0xf bank_mask:0xf bound_ctrl:1
	v_mad_u32_u24 v171, v168, v181, v170
	ds_write_b8_d16_hi v184, v171 offset:416
	s_barrier
	global_store_short_d16_hi v185, v176, s[48:49]
	s_waitcnt lgkmcnt(0)
	s_barrier
	ds_read_b64 v[122:123], v106 offset:416
	ds_read_b64 v[124:125], v106 offset:424
	ds_read_b64 v[126:127], v106 offset:432
	ds_read_b64 v[128:129], v106 offset:512
	ds_read_b64 v[130:131], v106 offset:520
	ds_read_b64 v[132:133], v106 offset:528
	s_waitcnt lgkmcnt(3)
	v_mfma_f32_16x16x128_f8f6f4 v[134:137], v[122:127], v[2:7], 0 cbsz:2 blgp:2
	v_mfma_f32_16x16x128_f8f6f4 v[138:141], v[122:127], v[14:19], 0 cbsz:2 blgp:2
	v_mfma_f32_16x16x128_f8f6f4 v[142:145], v[122:127], v[26:31], v[188:191] cbsz:2 blgp:2
	v_mfma_f32_16x16x128_f8f6f4 v[204:207], v[122:127], v[38:43], 0 cbsz:2 blgp:2
	v_mfma_f32_16x16x128_f8f6f4 v[208:211], v[122:127], v[50:55], 0 cbsz:2 blgp:2
	v_mfma_f32_16x16x128_f8f6f4 v[212:215], v[122:127], v[62:67], v[188:191] cbsz:2 blgp:2
	s_waitcnt lgkmcnt(0)
	v_mfma_f32_16x16x128_f8f6f4 v[134:137], v[128:133], v[8:13], v[134:137] cbsz:2 blgp:2
	v_mfma_f32_16x16x128_f8f6f4 v[204:207], v[128:133], v[44:49], v[204:207] cbsz:2 blgp:2
	v_mfma_f32_16x16x128_f8f6f4 v[138:141], v[128:133], v[20:25], v[138:141] cbsz:2 blgp:2
	v_mfma_f32_16x16x128_f8f6f4 v[208:211], v[128:133], v[56:61], v[208:211] cbsz:2 blgp:2
	v_mfma_f32_16x16x128_f8f6f4 v[142:145], v[128:133], v[32:37], v[142:145] cbsz:2 blgp:2
	v_mfma_f32_16x16x128_f8f6f4 v[212:215], v[128:133], v[68:73], v[212:215] cbsz:2 blgp:2
	v_cndmask_b32_e64 v158, v134, v204, s[4:5]
	v_fma_mix_f32 v158, v158, v1, v148 op_sel:[0,0,1] op_sel_hi:[0,0,1]
	v_exp_f32_e32 v158, v158
	v_cndmask_b32_e64 v159, v138, v208, s[4:5]
	v_fma_mix_f32 v159, v159, v99, v152 op_sel:[0,0,1] op_sel_hi:[0,0,1]
	v_exp_f32_e32 v159, v159
	v_fma_f32 v158, v158, v186, v186
	v_rcp_f32_e32 v158, v158
	v_add_f32_e32 v159, 1.0, v159
	v_rcp_f32_e32 v159, v159
	v_cndmask_b32_e64 v160, v142, v212, s[4:5]
	v_fma_mix_f32 v161, v158, v160, v156 op_sel:[0,0,1] op_sel_hi:[0,0,1]
	v_exp_f32_e32 v161, v161
	s_add_u32 s48, s48, s40
	v_add_f32_e32 v161, 1.0, v161
	v_rcp_f32_e32 v161, v161
	s_addc_u32 s49, s49, s41
	v_fma_f32 v162, v161, -2.0, 1.0
	v_sub_f32_e32 v163, v176, v162
	v_fma_f32 v176, v159, v163, v162
	v_fma_f32 v164, |v176|, s16, v117
	v_fma_f32 v165, |v176|, s17, v118
	v_fma_f32 v166, |v176|, s18, v119
	v_lshrrev_b32_e32 v167, 26, v176
	v_min3_u32 v164, v164, v165, v166
	v_bfi_b32 v168, 31, v164, v167
	s_nop 1
	v_mul_u32_u24_dpp v170, v168, v180 quad_perm:[1,2,3,3] row_mask:0xf bank_mask:0xf bound_ctrl:1
	v_mad_u32_u24 v171, v168, v181, v170
	ds_write_b8_d16_hi v184, v171
	s_barrier
	global_store_short_d16_hi v185, v176, s[48:49]
	s_waitcnt lgkmcnt(0)
	s_barrier
	ds_read_b64 v[122:123], v106 offset:0
	ds_read_b64 v[124:125], v106 offset:8
	ds_read_b64 v[126:127], v106 offset:16
	ds_read_b64 v[128:129], v106 offset:96
	ds_read_b64 v[130:131], v106 offset:104
	ds_read_b64 v[132:133], v106 offset:112
	s_waitcnt lgkmcnt(3)
	v_mfma_f32_16x16x128_f8f6f4 v[134:137], v[122:127], v[2:7], 0 cbsz:2 blgp:2
	v_mfma_f32_16x16x128_f8f6f4 v[138:141], v[122:127], v[14:19], 0 cbsz:2 blgp:2
	v_mfma_f32_16x16x128_f8f6f4 v[142:145], v[122:127], v[26:31], v[188:191] cbsz:2 blgp:2
	v_mfma_f32_16x16x128_f8f6f4 v[204:207], v[122:127], v[38:43], 0 cbsz:2 blgp:2
	v_mfma_f32_16x16x128_f8f6f4 v[208:211], v[122:127], v[50:55], 0 cbsz:2 blgp:2
	v_mfma_f32_16x16x128_f8f6f4 v[212:215], v[122:127], v[62:67], v[188:191] cbsz:2 blgp:2
	s_waitcnt lgkmcnt(0)
	v_mfma_f32_16x16x128_f8f6f4 v[134:137], v[128:133], v[8:13], v[134:137] cbsz:2 blgp:2
	v_mfma_f32_16x16x128_f8f6f4 v[204:207], v[128:133], v[44:49], v[204:207] cbsz:2 blgp:2
	v_mfma_f32_16x16x128_f8f6f4 v[138:141], v[128:133], v[20:25], v[138:141] cbsz:2 blgp:2
	v_mfma_f32_16x16x128_f8f6f4 v[208:211], v[128:133], v[56:61], v[208:211] cbsz:2 blgp:2
	v_mfma_f32_16x16x128_f8f6f4 v[142:145], v[128:133], v[32:37], v[142:145] cbsz:2 blgp:2
	v_mfma_f32_16x16x128_f8f6f4 v[212:215], v[128:133], v[68:73], v[212:215] cbsz:2 blgp:2
	v_cndmask_b32_e64 v158, v134, v204, s[4:5]
	v_fma_mix_f32 v158, v158, v1, v149 op_sel_hi:[0,0,1]
	v_exp_f32_e32 v158, v158
	v_cndmask_b32_e64 v159, v138, v208, s[4:5]
	v_fma_mix_f32 v159, v159, v99, v153 op_sel_hi:[0,0,1]
	v_exp_f32_e32 v159, v159
	v_fma_f32 v158, v158, v186, v186
	v_rcp_f32_e32 v158, v158
	v_add_f32_e32 v159, 1.0, v159
	v_rcp_f32_e32 v159, v159
	v_cndmask_b32_e64 v160, v142, v212, s[4:5]
	v_fma_mix_f32 v161, v158, v160, v157 op_sel_hi:[0,0,1]
	v_exp_f32_e32 v161, v161
	s_add_u32 s48, s48, s40
	v_add_f32_e32 v161, 1.0, v161
	v_rcp_f32_e32 v161, v161
	s_addc_u32 s49, s49, s41
	v_fma_f32 v162, v161, -2.0, 1.0
	v_sub_f32_e32 v163, v176, v162
	v_fma_f32 v176, v159, v163, v162
	v_fma_f32 v164, |v176|, s16, v117
	v_fma_f32 v165, |v176|, s17, v118
	v_fma_f32 v166, |v176|, s18, v119
	v_lshrrev_b32_e32 v167, 26, v176
	v_min3_u32 v164, v164, v165, v166
	v_bfi_b32 v168, 31, v164, v167
	s_nop 1
	v_mul_u32_u24_dpp v170, v168, v180 quad_perm:[1,2,3,3] row_mask:0xf bank_mask:0xf bound_ctrl:1
	v_mad_u32_u24 v171, v168, v181, v170
	ds_write_b8_d16_hi v184, v171 offset:416
	s_barrier
	global_store_short_d16_hi v185, v176, s[48:49]
	s_waitcnt lgkmcnt(0)
	s_barrier
	ds_read_b64 v[122:123], v106 offset:416
	ds_read_b64 v[124:125], v106 offset:424
	ds_read_b64 v[126:127], v106 offset:432
	ds_read_b64 v[128:129], v106 offset:512
	ds_read_b64 v[130:131], v106 offset:520
	ds_read_b64 v[132:133], v106 offset:528
	s_add_i32 s44, s44, 16
	s_waitcnt lgkmcnt(3)
	v_mfma_f32_16x16x128_f8f6f4 v[134:137], v[122:127], v[2:7], 0 cbsz:2 blgp:2
	v_mfma_f32_16x16x128_f8f6f4 v[138:141], v[122:127], v[14:19], 0 cbsz:2 blgp:2
	v_mfma_f32_16x16x128_f8f6f4 v[142:145], v[122:127], v[26:31], v[188:191] cbsz:2 blgp:2
	v_mfma_f32_16x16x128_f8f6f4 v[204:207], v[122:127], v[38:43], 0 cbsz:2 blgp:2
	v_mfma_f32_16x16x128_f8f6f4 v[208:211], v[122:127], v[50:55], 0 cbsz:2 blgp:2
	v_mfma_f32_16x16x128_f8f6f4 v[212:215], v[122:127], v[62:67], v[188:191] cbsz:2 blgp:2
	s_waitcnt lgkmcnt(0)
	v_mfma_f32_16x16x128_f8f6f4 v[134:137], v[128:133], v[8:13], v[134:137] cbsz:2 blgp:2
	v_mfma_f32_16x16x128_f8f6f4 v[204:207], v[128:133], v[44:49], v[204:207] cbsz:2 blgp:2
	v_mfma_f32_16x16x128_f8f6f4 v[138:141], v[128:133], v[20:25], v[138:141] cbsz:2 blgp:2
	v_mfma_f32_16x16x128_f8f6f4 v[208:211], v[128:133], v[56:61], v[208:211] cbsz:2 blgp:2
	v_mfma_f32_16x16x128_f8f6f4 v[142:145], v[128:133], v[32:37], v[142:145] cbsz:2 blgp:2
	v_mfma_f32_16x16x128_f8f6f4 v[212:215], v[128:133], v[68:73], v[212:215] cbsz:2 blgp:2
	v_cndmask_b32_e64 v158, v134, v204, s[4:5]
	v_fma_mix_f32 v158, v158, v1, v149 op_sel:[0,0,1] op_sel_hi:[0,0,1]
	v_exp_f32_e32 v158, v158
	v_cndmask_b32_e64 v159, v138, v208, s[4:5]
	v_fma_mix_f32 v159, v159, v99, v153 op_sel:[0,0,1] op_sel_hi:[0,0,1]
	v_exp_f32_e32 v159, v159
	v_fma_f32 v158, v158, v186, v186
	v_rcp_f32_e32 v158, v158
	v_add_f32_e32 v159, 1.0, v159
	v_rcp_f32_e32 v159, v159
	v_cndmask_b32_e64 v160, v142, v212, s[4:5]
	v_fma_mix_f32 v161, v158, v160, v157 op_sel:[0,0,1] op_sel_hi:[0,0,1]
	v_exp_f32_e32 v161, v161
	s_add_u32 s48, s48, s40
	v_add_f32_e32 v161, 1.0, v161
	v_rcp_f32_e32 v161, v161
	s_addc_u32 s49, s49, s41
	v_fma_f32 v162, v161, -2.0, 1.0
	v_sub_f32_e32 v163, v176, v162
	v_fma_f32 v176, v159, v163, v162
	v_fma_f32 v164, |v176|, s16, v117
	v_fma_f32 v165, |v176|, s17, v118
	v_fma_f32 v166, |v176|, s18, v119
	v_lshrrev_b32_e32 v167, 26, v176
	v_min3_u32 v164, v164, v165, v166
	v_bfi_b32 v168, 31, v164, v167
	s_nop 1
	v_mul_u32_u24_dpp v170, v168, v180 quad_perm:[1,2,3,3] row_mask:0xf bank_mask:0xf bound_ctrl:1
	v_mad_u32_u24 v171, v168, v181, v170
	ds_write_b8_d16_hi v184, v171
	s_barrier
	global_store_short_d16_hi v185, v176, s[48:49]
	s_cmp_lt_i32 s44, s45
	s_cbranch_scc1 .Lscan_loop_b_st
	s_waitcnt lgkmcnt(0)
	s_barrier

.LBB2_12:
	s_or_b64 exec, exec, s[0:1]
	v_and_b32_e32 v97, 1, v74
	v_mov_b32_e32 v74, s8
	v_mov_b32_e32 v75, s9
	v_lshl_or_b32 v76, s2, 9, v0
	v_mov_b32_e32 v77, v87
	v_lshl_add_u64 v[74:75], v[76:77], 2, v[74:75]
	s_waitcnt lgkmcnt(0)
	s_barrier
	global_load_dword v118, v[74:75], off
	v_and_b32_e32 v74, 4, v90
	v_mov_b32_e32 v75, 0xd0
	v_cmp_ne_u32_e32 vcc, 0, v74
	v_and_b32_e32 v110, 3, v0
	v_cmp_gt_u32_e64 s[0:1], 12, v90
	v_cndmask_b32_e32 v74, 0, v75, vcc
	v_cmp_eq_u32_e32 vcc, 0, v110
	s_and_b64 s[4:5], vcc, s[0:1]
	s_lshl_b32 s1, s2, 21
	v_add_u32_e32 v109, v74, v86
	s_mul_i32 s0, s2, 0x600000
	v_lshl_or_b32 v74, v89, 1, v88
	s_and_b32 s2, s1, 0x1e00000
	v_mul_u32_u24_e32 v74, 0x60, v74
	v_lshlrev_b32_e32 v75, 1, v90
	s_add_u32 s0, s14, s0
	s_addc_u32 s1, s15, 0
	v_or3_b32 v86, v74, v75, v97
	v_lshl_add_u64 v[98:99], v[86:87], 4, s[0:1]
	s_mov_b64 s[0:1], 0x5a0000
	v_lshl_add_u64 v[100:101], v[98:99], 0, s[0:1]
	s_mov_b32 s0, 0x5a0000
	v_add_co_u32_e32 v102, vcc, s0, v98
	s_waitcnt vmcnt(4)
	v_mul_f32_e32 v86, 0xbfb8aa3b, v95
	v_addc_co_u32_e32 v103, vcc, 0, v99, vcc
	global_load_dwordx4 v[82:85], v[102:103], off
	global_load_dwordx4 v[74:77], v[100:101], off offset:512
	global_load_dwordx4 v[78:81], v[100:101], off offset:1024
	v_mul_f32_e32 v100, 0x3c91a2b4, v86
	s_waitcnt vmcnt(6)
	v_mul_f32_e32 v86, 0xbfb8aa3b, v94
	v_mul_f32_e32 v101, 0x3c91a2b4, v86
	s_waitcnt vmcnt(5)
	v_mul_f32_e32 v86, 0x4038aa3b, v93
	v_and_b32_e32 v0, 12, v0
	v_mul_f32_e32 v102, 0x3c91a2b4, v86
	v_lshrrev_b32_e32 v86, 2, v90
	v_mul_u32_u24_e32 v90, 0xd0, v97
	v_mad_u32_u24 v0, v89, 24, v0
	v_mul_u32_u24_e32 v88, 12, v88
	v_add3_u32 v93, v0, v90, v88
	v_or_b32_e32 v0, s2, v1
	v_lshlrev_b32_e32 v104, 3, v86
	v_lshlrev_b32_e32 v89, 20, v97
	v_lshl_add_u32 v0, s22, 8, v0
	v_sub_u32_e32 v86, 0, v104
	v_or3_b32 v0, v0, v89, v92
	v_and_b32_e32 v111, 24, v86
	v_lshlrev_b32_e32 v86, 1, v0
	s_mov_b64 s[6:7], 0x5a6000
	v_lshl_add_u64 v[0:1], s[12:13], 0, v[86:87]
	v_lshl_add_u64 v[86:87], v[98:99], 0, s[6:7]
	s_mov_b64 s[6:7], 0x5a6200
	v_lshl_add_u64 v[88:89], v[98:99], 0, s[6:7]
	s_mov_b64 s[6:7], 0x5a6400
	v_cmp_lt_u32_e64 s[0:1], 1, v91
	s_waitcnt vmcnt(4)
	v_mul_f32_e32 v103, 0x4038aa3b, v96
	s_mov_b32 s3, 0
	v_or_b32_e32 v105, 0x1c400, v109
	v_add_u32_e32 v106, 0x1c410, v109
	v_add_u32_e32 v107, 0x1c470, v109
	v_add_u32_e32 v108, 0x1c5b0, v109
	v_add_u32_e32 v109, 0x1c610, v109
	v_mul_u32_u24_e32 v110, 6, v110
	v_lshl_add_u64 v[90:91], v[98:99], 0, s[6:7]
	s_movk_i32 s22, 0x780
	s_movk_i32 s14, 0x7f
	s_movk_i32 s15, 0xf0
	v_mov_b32_e32 v112, 0x7f7f7f7f
	s_mov_b32 s17, 0x42700000
	s_mov_b32 s18, 0x41f00000
	s_mov_b32 s19, 0x41700000
	s_mov_b64 s[6:7], 0x12000
	s_mov_b64 s[8:9], 0x12200
	s_mov_b64 s[10:11], 0x12400
	v_mov_b32_e32 v113, 0x4b400000
	v_mov_b32_e32 v114, 0x4b400008
	v_mov_b32_e32 v115, 0x4b400010
	v_add_u32_e32 v116, 0x1c5a0, v93
	v_add_u32_e32 v117, 0x1c400, v93
	v_mbcnt_lo_u32_b32 v200, -1, 0
	v_mbcnt_hi_u32_b32 v200, -1, v200
	v_and_b32_e32 v201, 3, v200
	v_and_b32_e32 v202, 15, v200
	v_cmp_gt_u32_e32 vcc, 8, v202
	s_nop 1
	v_cndmask_b32_e64 v178, 0, v112, vcc
	v_cndmask_b32_e64 v179, v112, 0, vcc
	v_lshlrev_b32_e32 v181, 1, v201
	v_sub_u32_e32 v202, 22, v181
	v_lshlrev_b32_e64 v180, v202, 1
	v_sub_u32_e32 v202, 16, v181
	v_lshlrev_b32_e64 v181, v202, 1
	v_lshrrev_b32_e32 v202, 3, v104
	v_sub_u32_e32 v184, v117, v202
	v_add_u32_e32 v184, v184, v201
	v_add_u32_e32 v202, 0x1c4c0, v202
	v_cmp_eq_u32_e32 vcc, 3, v201
	s_nop 1
	v_cndmask_b32_e32 v184, v184, v202, vcc
	v_subrev_u32_e32 v185, s12, v0
	s_movk_i32 s44, 0x780
	s_movk_i32 s45, 0x800
	s_lshr_b32 s46, s44, 3
	s_add_i32 s46, s46, 1
	s_mul_i32 s46, s46, 0x6000
	s_mov_b32 s47, 0
	v_lshl_add_u64 v[196:197], v[98:99], 0, s[46:47]
	s_mov_b32 s42, 0x6000
	s_mov_b32 s43, 0
	s_sub_i32 s46, s44, 1
	s_sub_i32 s47, 0x800, s44
	s_and_b64 s[40:41], s[20:21], exec
	s_cselect_b32 s46, s46, s47
	s_cselect_b32 s41, 0, -1
	s_xor_b32 s40, s41, 0x400
	s_sub_i32 s40, s40, s41
	s_ashr_i32 s47, s46, 31
	s_lshl_b64 s[46:47], s[46:47], 10
	s_add_u32 s48, s12, s46
	s_addc_u32 s49, s13, s47
	v_readfirstlane_b32 s51, v117
	s_waitcnt vmcnt(0) lgkmcnt(0)
	v_mov_b32_e32 v176, v118
	v_add_f32_e32 v169, -1.0, v118
	v_rcp_f32_e32 v186, v102
	s_nop 1
	v_mul_f32_e32 v188, v103, v186
	v_mov_b32_e32 v189, 0
	v_mov_b32_e32 v190, 0
	v_mov_b32_e32 v191, 0
	s_nop 1
	s_sub_u32 s51, s51, 0x1c400
	s_cmp_lt_i32 s44, s45
	s_cbranch_scc0 .Lscan_exit_f2
	ds_read_b64 v[122:123], v105 offset:0
	ds_read_b64 v[124:125], v105 offset:8
	ds_read_b64 v[126:127], v105 offset:16
	s_waitcnt lgkmcnt(0)
	s_cmp_lt_u32 s51, 96
	s_cbranch_scc0 .Lscan_entry_b_f2
	s_branch .Lscan_enter_a_f2
	.p2align 6

.Lscan_enter_a_f2:
	ds_read_b64 v[128:129], v105 offset:96
	ds_read_b64 v[130:131], v105 offset:104
	ds_read_b64 v[132:133], v105 offset:112
	s_waitcnt vmcnt(8)
	global_load_dwordx4 v[146:149], v[196:197], off
	global_load_dwordx4 v[150:153], v[196:197], off offset:512
	global_load_dwordx4 v[154:157], v[196:197], off offset:1024
	v_lshl_add_u64 v[196:197], v[196:197], 0, s[42:43]
	s_waitcnt lgkmcnt(3)
	v_mfma_f32_16x16x128_f8f6f4 v[134:137], v[122:127], v[2:7], 0 cbsz:2 blgp:2
	v_mfma_f32_16x16x128_f8f6f4 v[138:141], v[122:127], v[14:19], 0 cbsz:2 blgp:2
	v_mfma_f32_16x16x128_f8f6f4 v[142:145], v[122:127], v[26:31], v[188:191] cbsz:2 blgp:2
	v_mfma_f32_16x16x128_f8f6f4 v[204:207], v[122:127], v[38:43], 0 cbsz:2 blgp:2
	v_mfma_f32_16x16x128_f8f6f4 v[208:211], v[122:127], v[50:55], 0 cbsz:2 blgp:2
	v_mfma_f32_16x16x128_f8f6f4 v[212:215], v[122:127], v[62:67], v[188:191] cbsz:2 blgp:2
	s_waitcnt lgkmcnt(0)
	v_mfma_f32_16x16x128_f8f6f4 v[134:137], v[128:133], v[8:13], v[134:137] cbsz:2 blgp:2
	v_mfma_f32_16x16x128_f8f6f4 v[204:207], v[128:133], v[44:49], v[204:207] cbsz:2 blgp:2
	v_mfma_f32_16x16x128_f8f6f4 v[138:141], v[128:133], v[20:25], v[138:141] cbsz:2 blgp:2
	v_mfma_f32_16x16x128_f8f6f4 v[208:211], v[128:133], v[56:61], v[208:211] cbsz:2 blgp:2
	v_mfma_f32_16x16x128_f8f6f4 v[142:145], v[128:133], v[32:37], v[142:145] cbsz:2 blgp:2
	v_mfma_f32_16x16x128_f8f6f4 v[212:215], v[128:133], v[68:73], v[212:215] cbsz:2 blgp:2
	v_cndmask_b32_e64 v158, v134, v204, s[0:1]
	v_fma_mix_f32 v158, v158, v100, v82 op_sel_hi:[0,0,1]
	v_exp_f32_e32 v158, v158
	v_cndmask_b32_e64 v159, v138, v208, s[0:1]
	v_fma_mix_f32 v159, v159, v101, v74 op_sel_hi:[0,0,1]
	v_exp_f32_e32 v159, v159
	v_fma_f32 v158, v158, v186, v186
	v_rcp_f32_e32 v158, v158
	v_add_f32_e32 v159, 1.0, v159
	v_rcp_f32_e32 v159, v159
	v_cndmask_b32_e64 v160, v142, v212, s[0:1]
	v_fma_mix_f32 v161, v158, v160, v78 op_sel_hi:[0,0,1]
	v_exp_f32_e32 v161, v161
	s_add_u32 s48, s48, s40
	v_add_f32_e32 v161, 1.0, v161
	v_rcp_f32_e32 v161, v161
	s_addc_u32 s49, s49, s41
	v_fma_f32 v162, v161, -2.0, 1.0
	v_sub_f32_e32 v163, v176, v162
	v_fma_f32 v176, v159, v163, v162
	v_fma_f32 v164, |v176|, s17, v113
	v_fma_f32 v165, |v176|, s18, v114
	v_fma_f32 v166, |v176|, s19, v115
	v_lshrrev_b32_e32 v167, 26, v176
	v_min3_u32 v164, v164, v165, v166
	v_bfi_b32 v168, 31, v164, v167
	s_nop 1
	v_mul_u32_u24_dpp v170, v168, v180 quad_perm:[1,2,3,3] row_mask:0xf bank_mask:0xf bound_ctrl:1
	v_mad_u32_u24 v171, v168, v181, v170
	ds_write_b8_d16_hi v184, v171 offset:416
	global_store_short_d16_hi v185, v176, s[48:49]
	s_waitcnt lgkmcnt(0)
	s_barrier
	ds_read_b64 v[122:123], v105 offset:416
	ds_read_b64 v[124:125], v105 offset:424
	ds_read_b64 v[126:127], v105 offset:432
	s_barrier
	ds_read_b64 v[128:129], v105 offset:512
	ds_read_b64 v[130:131], v105 offset:520
	ds_read_b64 v[132:133], v105 offset:528
	s_waitcnt lgkmcnt(3)
	v_mfma_f32_16x16x128_f8f6f4 v[134:137], v[122:127], v[2:7], 0 cbsz:2 blgp:2
	v_mfma_f32_16x16x128_f8f6f4 v[138:141], v[122:127], v[14:19], 0 cbsz:2 blgp:2
	v_mfma_f32_16x16x128_f8f6f4 v[142:145], v[122:127], v[26:31], v[188:191] cbsz:2 blgp:2
	v_mfma_f32_16x16x128_f8f6f4 v[204:207], v[122:127], v[38:43], 0 cbsz:2 blgp:2
	v_mfma_f32_16x16x128_f8f6f4 v[208:211], v[122:127], v[50:55], 0 cbsz:2 blgp:2
	v_mfma_f32_16x16x128_f8f6f4 v[212:215], v[122:127], v[62:67], v[188:191] cbsz:2 blgp:2
	s_waitcnt lgkmcnt(0)
	v_mfma_f32_16x16x128_f8f6f4 v[134:137], v[128:133], v[8:13], v[134:137] cbsz:2 blgp:2
	v_mfma_f32_16x16x128_f8f6f4 v[204:207], v[128:133], v[44:49], v[204:207] cbsz:2 blgp:2
	v_mfma_f32_16x16x128_f8f6f4 v[138:141], v[128:133], v[20:25], v[138:141] cbsz:2 blgp:2
	v_mfma_f32_16x16x128_f8f6f4 v[208:211], v[128:133], v[56:61], v[208:211] cbsz:2 blgp:2
	v_mfma_f32_16x16x128_f8f6f4 v[142:145], v[128:133], v[32:37], v[142:145] cbsz:2 blgp:2
	v_mfma_f32_16x16x128_f8f6f4 v[212:215], v[128:133], v[68:73], v[212:215] cbsz:2 blgp:2
	v_cndmask_b32_e64 v158, v134, v204, s[0:1]
	v_fma_mix_f32 v158, v158, v100, v82 op_sel:[0,0,1] op_sel_hi:[0,0,1]
	v_exp_f32_e32 v158, v158
	v_cndmask_b32_e64 v159, v138, v208, s[0:1]
	v_fma_mix_f32 v159, v159, v101, v74 op_sel:[0,0,1] op_sel_hi:[0,0,1]
	v_exp_f32_e32 v159, v159
	v_fma_f32 v158, v158, v186, v186
	v_rcp_f32_e32 v158, v158
	v_add_f32_e32 v159, 1.0, v159
	v_rcp_f32_e32 v159, v159
	v_cndmask_b32_e64 v160, v142, v212, s[0:1]
	v_fma_mix_f32 v161, v158, v160, v78 op_sel:[0,0,1] op_sel_hi:[0,0,1]
	v_exp_f32_e32 v161, v161
	s_add_u32 s48, s48, s40
	v_add_f32_e32 v161, 1.0, v161
	v_rcp_f32_e32 v161, v161
	s_addc_u32 s49, s49, s41
	v_fma_f32 v162, v161, -2.0, 1.0
	v_sub_f32_e32 v163, v176, v162
	v_fma_f32 v176, v159, v163, v162
	v_fma_f32 v164, |v176|, s17, v113
	v_fma_f32 v165, |v176|, s18, v114
	v_fma_f32 v166, |v176|, s19, v115
	v_lshrrev_b32_e32 v167, 26, v176
	v_min3_u32 v164, v164, v165, v166
	v_bfi_b32 v168, 31, v164, v167
	s_nop 1
	v_mul_u32_u24_dpp v170, v168, v180 quad_perm:[1,2,3,3] row_mask:0xf bank_mask:0xf bound_ctrl:1
	v_mad_u32_u24 v171, v168, v181, v170
	ds_write_b8_d16_hi v184, v171
	global_store_short_d16_hi v185, v176, s[48:49]
	s_waitcnt lgkmcnt(0)
	s_barrier
	ds_read_b64 v[122:123], v105 offset:0
	ds_read_b64 v[124:125], v105 offset:8
	ds_read_b64 v[126:127], v105 offset:16
	s_barrier
	ds_read_b64 v[128:129], v105 offset:96
	ds_read_b64 v[130:131], v105 offset:104
	ds_read_b64 v[132:133], v105 offset:112
	s_waitcnt lgkmcnt(3)
	v_mfma_f32_16x16x128_f8f6f4 v[134:137], v[122:127], v[2:7], 0 cbsz:2 blgp:2
	v_mfma_f32_16x16x128_f8f6f4 v[138:141], v[122:127], v[14:19], 0 cbsz:2 blgp:2
	v_mfma_f32_16x16x128_f8f6f4 v[142:145], v[122:127], v[26:31], v[188:191] cbsz:2 blgp:2
	v_mfma_f32_16x16x128_f8f6f4 v[204:207], v[122:127], v[38:43], 0 cbsz:2 blgp:2
	v_mfma_f32_16x16x128_f8f6f4 v[208:211], v[122:127], v[50:55], 0 cbsz:2 blgp:2
	v_mfma_f32_16x16x128_f8f6f4 v[212:215], v[122:127], v[62:67], v[188:191] cbsz:2 blgp:2
	s_waitcnt lgkmcnt(0)
	v_mfma_f32_16x16x128_f8f6f4 v[134:137], v[128:133], v[8:13], v[134:137] cbsz:2 blgp:2
	v_mfma_f32_16x16x128_f8f6f4 v[204:207], v[128:133], v[44:49], v[204:207] cbsz:2 blgp:2
	v_mfma_f32_16x16x128_f8f6f4 v[138:141], v[128:133], v[20:25], v[138:141] cbsz:2 blgp:2
	v_mfma_f32_16x16x128_f8f6f4 v[208:211], v[128:133], v[56:61], v[208:211] cbsz:2 blgp:2
	v_mfma_f32_16x16x128_f8f6f4 v[142:145], v[128:133], v[32:37], v[142:145] cbsz:2 blgp:2
	v_mfma_f32_16x16x128_f8f6f4 v[212:215], v[128:133], v[68:73], v[212:215] cbsz:2 blgp:2
	v_cndmask_b32_e64 v158, v134, v204, s[0:1]
	v_fma_mix_f32 v158, v158, v100, v83 op_sel_hi:[0,0,1]
	v_exp_f32_e32 v158, v158
	v_cndmask_b32_e64 v159, v138, v208, s[0:1]
	v_fma_mix_f32 v159, v159, v101, v75 op_sel_hi:[0,0,1]
	v_exp_f32_e32 v159, v159
	v_fma_f32 v158, v158, v186, v186
	v_rcp_f32_e32 v158, v158
	v_add_f32_e32 v159, 1.0, v159
	v_rcp_f32_e32 v159, v159
	v_cndmask_b32_e64 v160, v142, v212, s[0:1]
	v_fma_mix_f32 v161, v158, v160, v79 op_sel_hi:[0,0,1]
	v_exp_f32_e32 v161, v161
	s_add_u32 s48, s48, s40
	v_add_f32_e32 v161, 1.0, v161
	v_rcp_f32_e32 v161, v161
	s_addc_u32 s49, s49, s41
	v_fma_f32 v162, v161, -2.0, 1.0
	v_sub_f32_e32 v163, v176, v162
	v_fma_f32 v176, v159, v163, v162
	v_fma_f32 v164, |v176|, s17, v113
	v_fma_f32 v165, |v176|, s18, v114
	v_fma_f32 v166, |v176|, s19, v115
	v_lshrrev_b32_e32 v167, 26, v176
	v_min3_u32 v164, v164, v165, v166
	v_bfi_b32 v168, 31, v164, v167
	s_nop 1
	v_mul_u32_u24_dpp v170, v168, v180 quad_perm:[1,2,3,3] row_mask:0xf bank_mask:0xf bound_ctrl:1
	v_mad_u32_u24 v171, v168, v181, v170
	ds_write_b8_d16_hi v184, v171 offset:416
	global_store_short_d16_hi v185, v176, s[48:49]
	s_waitcnt lgkmcnt(0)
	s_barrier
	ds_read_b64 v[122:123], v105 offset:416
	ds_read_b64 v[124:125], v105 offset:424
	ds_read_b64 v[126:127], v105 offset:432
	s_barrier
	ds_read_b64 v[128:129], v105 offset:512
	ds_read_b64 v[130:131], v105 offset:520
	ds_read_b64 v[132:133], v105 offset:528
	s_waitcnt lgkmcnt(3)
	v_mfma_f32_16x16x128_f8f6f4 v[134:137], v[122:127], v[2:7], 0 cbsz:2 blgp:2
	v_mfma_f32_16x16x128_f8f6f4 v[138:141], v[122:127], v[14:19], 0 cbsz:2 blgp:2
	v_mfma_f32_16x16x128_f8f6f4 v[142:145], v[122:127], v[26:31], v[188:191] cbsz:2 blgp:2
	v_mfma_f32_16x16x128_f8f6f4 v[204:207], v[122:127], v[38:43], 0 cbsz:2 blgp:2
	v_mfma_f32_16x16x128_f8f6f4 v[208:211], v[122:127], v[50:55], 0 cbsz:2 blgp:2
	v_mfma_f32_16x16x128_f8f6f4 v[212:215], v[122:127], v[62:67], v[188:191] cbsz:2 blgp:2
	s_waitcnt lgkmcnt(0)
	v_mfma_f32_16x16x128_f8f6f4 v[134:137], v[128:133], v[8:13], v[134:137] cbsz:2 blgp:2
	v_mfma_f32_16x16x128_f8f6f4 v[204:207], v[128:133], v[44:49], v[204:207] cbsz:2 blgp:2
	v_mfma_f32_16x16x128_f8f6f4 v[138:141], v[128:133], v[20:25], v[138:141] cbsz:2 blgp:2
	v_mfma_f32_16x16x128_f8f6f4 v[208:211], v[128:133], v[56:61], v[208:211] cbsz:2 blgp:2
	v_mfma_f32_16x16x128_f8f6f4 v[142:145], v[128:133], v[32:37], v[142:145] cbsz:2 blgp:2
	v_mfma_f32_16x16x128_f8f6f4 v[212:215], v[128:133], v[68:73], v[212:215] cbsz:2 blgp:2
	v_cndmask_b32_e64 v158, v134, v204, s[0:1]
	v_fma_mix_f32 v158, v158, v100, v83 op_sel:[0,0,1] op_sel_hi:[0,0,1]
	v_exp_f32_e32 v158, v158
	v_cndmask_b32_e64 v159, v138, v208, s[0:1]
	v_fma_mix_f32 v159, v159, v101, v75 op_sel:[0,0,1] op_sel_hi:[0,0,1]
	v_exp_f32_e32 v159, v159
	v_fma_f32 v158, v158, v186, v186
	v_rcp_f32_e32 v158, v158
	v_add_f32_e32 v159, 1.0, v159
	v_rcp_f32_e32 v159, v159
	v_cndmask_b32_e64 v160, v142, v212, s[0:1]
	v_fma_mix_f32 v161, v158, v160, v79 op_sel:[0,0,1] op_sel_hi:[0,0,1]
	v_exp_f32_e32 v161, v161
	s_add_u32 s48, s48, s40
	v_add_f32_e32 v161, 1.0, v161
	v_rcp_f32_e32 v161, v161
	s_addc_u32 s49, s49, s41
	v_fma_f32 v162, v161, -2.0, 1.0
	v_sub_f32_e32 v163, v176, v162
	v_fma_f32 v176, v159, v163, v162
	v_fma_f32 v164, |v176|, s17, v113
	v_fma_f32 v165, |v176|, s18, v114
	v_fma_f32 v166, |v176|, s19, v115
	v_lshrrev_b32_e32 v167, 26, v176
	v_min3_u32 v164, v164, v165, v166
	v_bfi_b32 v168, 31, v164, v167
	s_nop 1
	v_mul_u32_u24_dpp v170, v168, v180 quad_perm:[1,2,3,3] row_mask:0xf bank_mask:0xf bound_ctrl:1
	v_mad_u32_u24 v171, v168, v181, v170
	ds_write_b8_d16_hi v184, v171
	global_store_short_d16_hi v185, v176, s[48:49]
	s_waitcnt lgkmcnt(0)
	s_barrier
	ds_read_b64 v[122:123], v105 offset:0
	ds_read_b64 v[124:125], v105 offset:8
	ds_read_b64 v[126:127], v105 offset:16
	s_barrier
	ds_read_b64 v[128:129], v105 offset:96
	ds_read_b64 v[130:131], v105 offset:104
	ds_read_b64 v[132:133], v105 offset:112
	s_waitcnt lgkmcnt(3)
	v_mfma_f32_16x16x128_f8f6f4 v[134:137], v[122:127], v[2:7], 0 cbsz:2 blgp:2
	v_mfma_f32_16x16x128_f8f6f4 v[138:141], v[122:127], v[14:19], 0 cbsz:2 blgp:2
	v_mfma_f32_16x16x128_f8f6f4 v[142:145], v[122:127], v[26:31], v[188:191] cbsz:2 blgp:2
	v_mfma_f32_16x16x128_f8f6f4 v[204:207], v[122:127], v[38:43], 0 cbsz:2 blgp:2
	v_mfma_f32_16x16x128_f8f6f4 v[208:211], v[122:127], v[50:55], 0 cbsz:2 blgp:2
	v_mfma_f32_16x16x128_f8f6f4 v[212:215], v[122:127], v[62:67], v[188:191] cbsz:2 blgp:2
	s_waitcnt lgkmcnt(0)
	v_mfma_f32_16x16x128_f8f6f4 v[134:137], v[128:133], v[8:13], v[134:137] cbsz:2 blgp:2
	v_mfma_f32_16x16x128_f8f6f4 v[204:207], v[128:133], v[44:49], v[204:207] cbsz:2 blgp:2
	v_mfma_f32_16x16x128_f8f6f4 v[138:141], v[128:133], v[20:25], v[138:141] cbsz:2 blgp:2
	v_mfma_f32_16x16x128_f8f6f4 v[208:211], v[128:133], v[56:61], v[208:211] cbsz:2 blgp:2
	v_mfma_f32_16x16x128_f8f6f4 v[142:145], v[128:133], v[32:37], v[142:145] cbsz:2 blgp:2
	v_mfma_f32_16x16x128_f8f6f4 v[212:215], v[128:133], v[68:73], v[212:215] cbsz:2 blgp:2
	v_cndmask_b32_e64 v158, v134, v204, s[0:1]
	v_fma_mix_f32 v158, v158, v100, v84 op_sel_hi:[0,0,1]
	v_exp_f32_e32 v158, v158
	v_cndmask_b32_e64 v159, v138, v208, s[0:1]
	v_fma_mix_f32 v159, v159, v101, v76 op_sel_hi:[0,0,1]
	v_exp_f32_e32 v159, v159
	v_fma_f32 v158, v158, v186, v186
	v_rcp_f32_e32 v158, v158
	v_add_f32_e32 v159, 1.0, v159
	v_rcp_f32_e32 v159, v159
	v_cndmask_b32_e64 v160, v142, v212, s[0:1]
	v_fma_mix_f32 v161, v158, v160, v80 op_sel_hi:[0,0,1]
	v_exp_f32_e32 v161, v161
	s_add_u32 s48, s48, s40
	v_add_f32_e32 v161, 1.0, v161
	v_rcp_f32_e32 v161, v161
	s_addc_u32 s49, s49, s41
	v_fma_f32 v162, v161, -2.0, 1.0
	v_sub_f32_e32 v163, v176, v162
	v_fma_f32 v176, v159, v163, v162
	v_fma_f32 v164, |v176|, s17, v113
	v_fma_f32 v165, |v176|, s18, v114
	v_fma_f32 v166, |v176|, s19, v115
	v_lshrrev_b32_e32 v167, 26, v176
	v_min3_u32 v164, v164, v165, v166
	v_bfi_b32 v168, 31, v164, v167
	s_nop 1
	v_mul_u32_u24_dpp v170, v168, v180 quad_perm:[1,2,3,3] row_mask:0xf bank_mask:0xf bound_ctrl:1
	v_mad_u32_u24 v171, v168, v181, v170
	ds_write_b8_d16_hi v184, v171 offset:416
	global_store_short_d16_hi v185, v176, s[48:49]
	s_waitcnt lgkmcnt(0)
	s_barrier
	ds_read_b64 v[122:123], v105 offset:416
	ds_read_b64 v[124:125], v105 offset:424
	ds_read_b64 v[126:127], v105 offset:432
	s_barrier
	ds_read_b64 v[128:129], v105 offset:512
	ds_read_b64 v[130:131], v105 offset:520
	ds_read_b64 v[132:133], v105 offset:528
	s_waitcnt lgkmcnt(3)
	v_mfma_f32_16x16x128_f8f6f4 v[134:137], v[122:127], v[2:7], 0 cbsz:2 blgp:2
	v_mfma_f32_16x16x128_f8f6f4 v[138:141], v[122:127], v[14:19], 0 cbsz:2 blgp:2
	v_mfma_f32_16x16x128_f8f6f4 v[142:145], v[122:127], v[26:31], v[188:191] cbsz:2 blgp:2
	v_mfma_f32_16x16x128_f8f6f4 v[204:207], v[122:127], v[38:43], 0 cbsz:2 blgp:2
	v_mfma_f32_16x16x128_f8f6f4 v[208:211], v[122:127], v[50:55], 0 cbsz:2 blgp:2
	v_mfma_f32_16x16x128_f8f6f4 v[212:215], v[122:127], v[62:67], v[188:191] cbsz:2 blgp:2
	s_waitcnt lgkmcnt(0)
	v_mfma_f32_16x16x128_f8f6f4 v[134:137], v[128:133], v[8:13], v[134:137] cbsz:2 blgp:2
	v_mfma_f32_16x16x128_f8f6f4 v[204:207], v[128:133], v[44:49], v[204:207] cbsz:2 blgp:2
	v_mfma_f32_16x16x128_f8f6f4 v[138:141], v[128:133], v[20:25], v[138:141] cbsz:2 blgp:2
	v_mfma_f32_16x16x128_f8f6f4 v[208:211], v[128:133], v[56:61], v[208:211] cbsz:2 blgp:2
	v_mfma_f32_16x16x128_f8f6f4 v[142:145], v[128:133], v[32:37], v[142:145] cbsz:2 blgp:2
	v_mfma_f32_16x16x128_f8f6f4 v[212:215], v[128:133], v[68:73], v[212:215] cbsz:2 blgp:2
	v_cndmask_b32_e64 v158, v134, v204, s[0:1]
	v_fma_mix_f32 v158, v158, v100, v84 op_sel:[0,0,1] op_sel_hi:[0,0,1]
	v_exp_f32_e32 v158, v158
	v_cndmask_b32_e64 v159, v138, v208, s[0:1]
	v_fma_mix_f32 v159, v159, v101, v76 op_sel:[0,0,1] op_sel_hi:[0,0,1]
	v_exp_f32_e32 v159, v159
	v_fma_f32 v158, v158, v186, v186
	v_rcp_f32_e32 v158, v158
	v_add_f32_e32 v159, 1.0, v159
	v_rcp_f32_e32 v159, v159
	v_cndmask_b32_e64 v160, v142, v212, s[0:1]
	v_fma_mix_f32 v161, v158, v160, v80 op_sel:[0,0,1] op_sel_hi:[0,0,1]
	v_exp_f32_e32 v161, v161
	s_add_u32 s48, s48, s40
	v_add_f32_e32 v161, 1.0, v161
	v_rcp_f32_e32 v161, v161
	s_addc_u32 s49, s49, s41
	v_fma_f32 v162, v161, -2.0, 1.0
	v_sub_f32_e32 v163, v176, v162
	v_fma_f32 v176, v159, v163, v162
	v_fma_f32 v164, |v176|, s17, v113
	v_fma_f32 v165, |v176|, s18, v114
	v_fma_f32 v166, |v176|, s19, v115
	v_lshrrev_b32_e32 v167, 26, v176
	v_min3_u32 v164, v164, v165, v166
	v_bfi_b32 v168, 31, v164, v167
	s_nop 1
	v_mul_u32_u24_dpp v170, v168, v180 quad_perm:[1,2,3,3] row_mask:0xf bank_mask:0xf bound_ctrl:1
	v_mad_u32_u24 v171, v168, v181, v170
	ds_write_b8_d16_hi v184, v171
	global_store_short_d16_hi v185, v176, s[48:49]
	s_waitcnt lgkmcnt(0)
	s_barrier
	ds_read_b64 v[122:123], v105 offset:0
	ds_read_b64 v[124:125], v105 offset:8
	ds_read_b64 v[126:127], v105 offset:16
	s_barrier
	ds_read_b64 v[128:129], v105 offset:96
	ds_read_b64 v[130:131], v105 offset:104
	ds_read_b64 v[132:133], v105 offset:112
	s_waitcnt lgkmcnt(3)
	v_mfma_f32_16x16x128_f8f6f4 v[134:137], v[122:127], v[2:7], 0 cbsz:2 blgp:2
	v_mfma_f32_16x16x128_f8f6f4 v[138:141], v[122:127], v[14:19], 0 cbsz:2 blgp:2
	v_mfma_f32_16x16x128_f8f6f4 v[142:145], v[122:127], v[26:31], v[188:191] cbsz:2 blgp:2
	v_mfma_f32_16x16x128_f8f6f4 v[204:207], v[122:127], v[38:43], 0 cbsz:2 blgp:2
	v_mfma_f32_16x16x128_f8f6f4 v[208:211], v[122:127], v[50:55], 0 cbsz:2 blgp:2
	v_mfma_f32_16x16x128_f8f6f4 v[212:215], v[122:127], v[62:67], v[188:191] cbsz:2 blgp:2
	s_waitcnt lgkmcnt(0)
	v_mfma_f32_16x16x128_f8f6f4 v[134:137], v[128:133], v[8:13], v[134:137] cbsz:2 blgp:2
	v_mfma_f32_16x16x128_f8f6f4 v[204:207], v[128:133], v[44:49], v[204:207] cbsz:2 blgp:2
	v_mfma_f32_16x16x128_f8f6f4 v[138:141], v[128:133], v[20:25], v[138:141] cbsz:2 blgp:2
	v_mfma_f32_16x16x128_f8f6f4 v[208:211], v[128:133], v[56:61], v[208:211] cbsz:2 blgp:2
	v_mfma_f32_16x16x128_f8f6f4 v[142:145], v[128:133], v[32:37], v[142:145] cbsz:2 blgp:2
	v_mfma_f32_16x16x128_f8f6f4 v[212:215], v[128:133], v[68:73], v[212:215] cbsz:2 blgp:2
	v_cndmask_b32_e64 v158, v134, v204, s[0:1]
	v_fma_mix_f32 v158, v158, v100, v85 op_sel_hi:[0,0,1]
	v_exp_f32_e32 v158, v158
	v_cndmask_b32_e64 v159, v138, v208, s[0:1]
	v_fma_mix_f32 v159, v159, v101, v77 op_sel_hi:[0,0,1]
	v_exp_f32_e32 v159, v159
	v_fma_f32 v158, v158, v186, v186
	v_rcp_f32_e32 v158, v158
	v_add_f32_e32 v159, 1.0, v159
	v_rcp_f32_e32 v159, v159
	v_cndmask_b32_e64 v160, v142, v212, s[0:1]
	v_fma_mix_f32 v161, v158, v160, v81 op_sel_hi:[0,0,1]
	v_exp_f32_e32 v161, v161
	s_add_u32 s48, s48, s40
	v_add_f32_e32 v161, 1.0, v161
	v_rcp_f32_e32 v161, v161
	s_addc_u32 s49, s49, s41
	v_fma_f32 v162, v161, -2.0, 1.0
	v_sub_f32_e32 v163, v176, v162
	v_fma_f32 v176, v159, v163, v162
	v_fma_f32 v164, |v176|, s17, v113
	v_fma_f32 v165, |v176|, s18, v114
	v_fma_f32 v166, |v176|, s19, v115
	v_lshrrev_b32_e32 v167, 26, v176
	v_min3_u32 v164, v164, v165, v166
	v_bfi_b32 v168, 31, v164, v167
	s_nop 1
	v_mul_u32_u24_dpp v170, v168, v180 quad_perm:[1,2,3,3] row_mask:0xf bank_mask:0xf bound_ctrl:1
	v_mad_u32_u24 v171, v168, v181, v170
	ds_write_b8_d16_hi v184, v171 offset:416
	global_store_short_d16_hi v185, v176, s[48:49]
	s_waitcnt lgkmcnt(0)
	s_barrier
	ds_read_b64 v[122:123], v105 offset:416
	ds_read_b64 v[124:125], v105 offset:424
	ds_read_b64 v[126:127], v105 offset:432
	s_barrier
	ds_read_b64 v[128:129], v105 offset:512
	ds_read_b64 v[130:131], v105 offset:520
	ds_read_b64 v[132:133], v105 offset:528
	s_waitcnt lgkmcnt(3)
	v_mfma_f32_16x16x128_f8f6f4 v[134:137], v[122:127], v[2:7], 0 cbsz:2 blgp:2
	v_mfma_f32_16x16x128_f8f6f4 v[138:141], v[122:127], v[14:19], 0 cbsz:2 blgp:2
	v_mfma_f32_16x16x128_f8f6f4 v[142:145], v[122:127], v[26:31], v[188:191] cbsz:2 blgp:2
	v_mfma_f32_16x16x128_f8f6f4 v[204:207], v[122:127], v[38:43], 0 cbsz:2 blgp:2
	v_mfma_f32_16x16x128_f8f6f4 v[208:211], v[122:127], v[50:55], 0 cbsz:2 blgp:2
	v_mfma_f32_16x16x128_f8f6f4 v[212:215], v[122:127], v[62:67], v[188:191] cbsz:2 blgp:2
	s_waitcnt lgkmcnt(0)
	v_mfma_f32_16x16x128_f8f6f4 v[134:137], v[128:133], v[8:13], v[134:137] cbsz:2 blgp:2
	v_mfma_f32_16x16x128_f8f6f4 v[204:207], v[128:133], v[44:49], v[204:207] cbsz:2 blgp:2
	v_mfma_f32_16x16x128_f8f6f4 v[138:141], v[128:133], v[20:25], v[138:141] cbsz:2 blgp:2
	v_mfma_f32_16x16x128_f8f6f4 v[208:211], v[128:133], v[56:61], v[208:211] cbsz:2 blgp:2
	v_mfma_f32_16x16x128_f8f6f4 v[142:145], v[128:133], v[32:37], v[142:145] cbsz:2 blgp:2
	v_mfma_f32_16x16x128_f8f6f4 v[212:215], v[128:133], v[68:73], v[212:215] cbsz:2 blgp:2
	v_cndmask_b32_e64 v158, v134, v204, s[0:1]
	v_fma_mix_f32 v158, v158, v100, v85 op_sel:[0,0,1] op_sel_hi:[0,0,1]
	v_exp_f32_e32 v158, v158
	v_cndmask_b32_e64 v159, v138, v208, s[0:1]
	v_fma_mix_f32 v159, v159, v101, v77 op_sel:[0,0,1] op_sel_hi:[0,0,1]
	v_exp_f32_e32 v159, v159
	v_fma_f32 v158, v158, v186, v186
	v_rcp_f32_e32 v158, v158
	v_add_f32_e32 v159, 1.0, v159
	v_rcp_f32_e32 v159, v159
	v_cndmask_b32_e64 v160, v142, v212, s[0:1]
	v_fma_mix_f32 v161, v158, v160, v81 op_sel:[0,0,1] op_sel_hi:[0,0,1]
	v_exp_f32_e32 v161, v161
	s_add_u32 s48, s48, s40
	v_add_f32_e32 v161, 1.0, v161
	v_rcp_f32_e32 v161, v161
	s_addc_u32 s49, s49, s41
	v_fma_f32 v162, v161, -2.0, 1.0
	v_sub_f32_e32 v163, v176, v162
	v_fma_f32 v176, v159, v163, v162
	v_fma_f32 v164, |v176|, s17, v113
	v_fma_f32 v165, |v176|, s18, v114
	v_fma_f32 v166, |v176|, s19, v115
	v_lshrrev_b32_e32 v167, 26, v176
	v_min3_u32 v164, v164, v165, v166
	v_bfi_b32 v168, 31, v164, v167
	s_nop 1
	v_mul_u32_u24_dpp v170, v168, v180 quad_perm:[1,2,3,3] row_mask:0xf bank_mask:0xf bound_ctrl:1
	v_mad_u32_u24 v171, v168, v181, v170
	ds_write_b8_d16_hi v184, v171
	global_store_short_d16_hi v185, v176, s[48:49]
	s_waitcnt lgkmcnt(0)
	s_barrier
	ds_read_b64 v[122:123], v105 offset:0
	ds_read_b64 v[124:125], v105 offset:8
	ds_read_b64 v[126:127], v105 offset:16
	s_barrier
	ds_read_b64 v[128:129], v105 offset:96
	ds_read_b64 v[130:131], v105 offset:104
	ds_read_b64 v[132:133], v105 offset:112
	s_waitcnt vmcnt(8)
	global_load_dwordx4 v[82:85], v[196:197], off
	global_load_dwordx4 v[74:77], v[196:197], off offset:512
	global_load_dwordx4 v[78:81], v[196:197], off offset:1024
	v_lshl_add_u64 v[196:197], v[196:197], 0, s[42:43]
	s_waitcnt lgkmcnt(3)
	v_mfma_f32_16x16x128_f8f6f4 v[134:137], v[122:127], v[2:7], 0 cbsz:2 blgp:2
	v_mfma_f32_16x16x128_f8f6f4 v[138:141], v[122:127], v[14:19], 0 cbsz:2 blgp:2
	v_mfma_f32_16x16x128_f8f6f4 v[142:145], v[122:127], v[26:31], v[188:191] cbsz:2 blgp:2
	v_mfma_f32_16x16x128_f8f6f4 v[204:207], v[122:127], v[38:43], 0 cbsz:2 blgp:2
	v_mfma_f32_16x16x128_f8f6f4 v[208:211], v[122:127], v[50:55], 0 cbsz:2 blgp:2
	v_mfma_f32_16x16x128_f8f6f4 v[212:215], v[122:127], v[62:67], v[188:191] cbsz:2 blgp:2
	s_waitcnt lgkmcnt(0)
	v_mfma_f32_16x16x128_f8f6f4 v[134:137], v[128:133], v[8:13], v[134:137] cbsz:2 blgp:2
	v_mfma_f32_16x16x128_f8f6f4 v[204:207], v[128:133], v[44:49], v[204:207] cbsz:2 blgp:2
	v_mfma_f32_16x16x128_f8f6f4 v[138:141], v[128:133], v[20:25], v[138:141] cbsz:2 blgp:2
	v_mfma_f32_16x16x128_f8f6f4 v[208:211], v[128:133], v[56:61], v[208:211] cbsz:2 blgp:2
	v_mfma_f32_16x16x128_f8f6f4 v[142:145], v[128:133], v[32:37], v[142:145] cbsz:2 blgp:2
	v_mfma_f32_16x16x128_f8f6f4 v[212:215], v[128:133], v[68:73], v[212:215] cbsz:2 blgp:2
	v_cndmask_b32_e64 v158, v134, v204, s[0:1]
	v_fma_mix_f32 v158, v158, v100, v146 op_sel_hi:[0,0,1]
	v_exp_f32_e32 v158, v158
	v_cndmask_b32_e64 v159, v138, v208, s[0:1]
	v_fma_mix_f32 v159, v159, v101, v150 op_sel_hi:[0,0,1]
	v_exp_f32_e32 v159, v159
	v_fma_f32 v158, v158, v186, v186
	v_rcp_f32_e32 v158, v158
	v_add_f32_e32 v159, 1.0, v159
	v_rcp_f32_e32 v159, v159
	v_cndmask_b32_e64 v160, v142, v212, s[0:1]
	v_fma_mix_f32 v161, v158, v160, v154 op_sel_hi:[0,0,1]
	v_exp_f32_e32 v161, v161
	s_add_u32 s48, s48, s40
	v_add_f32_e32 v161, 1.0, v161
	v_rcp_f32_e32 v161, v161
	s_addc_u32 s49, s49, s41
	v_fma_f32 v162, v161, -2.0, 1.0
	v_sub_f32_e32 v163, v176, v162
	v_fma_f32 v176, v159, v163, v162
	v_fma_f32 v164, |v176|, s17, v113
	v_fma_f32 v165, |v176|, s18, v114
	v_fma_f32 v166, |v176|, s19, v115
	v_lshrrev_b32_e32 v167, 26, v176
	v_min3_u32 v164, v164, v165, v166
	v_bfi_b32 v168, 31, v164, v167
	s_nop 1
	v_mul_u32_u24_dpp v170, v168, v180 quad_perm:[1,2,3,3] row_mask:0xf bank_mask:0xf bound_ctrl:1
	v_mad_u32_u24 v171, v168, v181, v170
	ds_write_b8_d16_hi v184, v171 offset:416
	global_store_short_d16_hi v185, v176, s[48:49]
	s_waitcnt lgkmcnt(0)
	s_barrier
	ds_read_b64 v[122:123], v105 offset:416
	ds_read_b64 v[124:125], v105 offset:424
	ds_read_b64 v[126:127], v105 offset:432
	s_barrier
	ds_read_b64 v[128:129], v105 offset:512
	ds_read_b64 v[130:131], v105 offset:520
	ds_read_b64 v[132:133], v105 offset:528
	s_waitcnt lgkmcnt(3)
	v_mfma_f32_16x16x128_f8f6f4 v[134:137], v[122:127], v[2:7], 0 cbsz:2 blgp:2
	v_mfma_f32_16x16x128_f8f6f4 v[138:141], v[122:127], v[14:19], 0 cbsz:2 blgp:2
	v_mfma_f32_16x16x128_f8f6f4 v[142:145], v[122:127], v[26:31], v[188:191] cbsz:2 blgp:2
	v_mfma_f32_16x16x128_f8f6f4 v[204:207], v[122:127], v[38:43], 0 cbsz:2 blgp:2
	v_mfma_f32_16x16x128_f8f6f4 v[208:211], v[122:127], v[50:55], 0 cbsz:2 blgp:2
	v_mfma_f32_16x16x128_f8f6f4 v[212:215], v[122:127], v[62:67], v[188:191] cbsz:2 blgp:2
	s_waitcnt lgkmcnt(0)
	v_mfma_f32_16x16x128_f8f6f4 v[134:137], v[128:133], v[8:13], v[134:137] cbsz:2 blgp:2
	v_mfma_f32_16x16x128_f8f6f4 v[204:207], v[128:133], v[44:49], v[204:207] cbsz:2 blgp:2
	v_mfma_f32_16x16x128_f8f6f4 v[138:141], v[128:133], v[20:25], v[138:141] cbsz:2 blgp:2
	v_mfma_f32_16x16x128_f8f6f4 v[208:211], v[128:133], v[56:61], v[208:211] cbsz:2 blgp:2
	v_mfma_f32_16x16x128_f8f6f4 v[142:145], v[128:133], v[32:37], v[142:145] cbsz:2 blgp:2
	v_mfma_f32_16x16x128_f8f6f4 v[212:215], v[128:133], v[68:73], v[212:215] cbsz:2 blgp:2
	v_cndmask_b32_e64 v158, v134, v204, s[0:1]
	v_fma_mix_f32 v158, v158, v100, v146 op_sel:[0,0,1] op_sel_hi:[0,0,1]
	v_exp_f32_e32 v158, v158
	v_cndmask_b32_e64 v159, v138, v208, s[0:1]
	v_fma_mix_f32 v159, v159, v101, v150 op_sel:[0,0,1] op_sel_hi:[0,0,1]
	v_exp_f32_e32 v159, v159
	v_fma_f32 v158, v158, v186, v186
	v_rcp_f32_e32 v158, v158
	v_add_f32_e32 v159, 1.0, v159
	v_rcp_f32_e32 v159, v159
	v_cndmask_b32_e64 v160, v142, v212, s[0:1]
	v_fma_mix_f32 v161, v158, v160, v154 op_sel:[0,0,1] op_sel_hi:[0,0,1]
	v_exp_f32_e32 v161, v161
	s_add_u32 s48, s48, s40
	v_add_f32_e32 v161, 1.0, v161
	v_rcp_f32_e32 v161, v161
	s_addc_u32 s49, s49, s41
	v_fma_f32 v162, v161, -2.0, 1.0
	v_sub_f32_e32 v163, v176, v162
	v_fma_f32 v176, v159, v163, v162
	v_fma_f32 v164, |v176|, s17, v113
	v_fma_f32 v165, |v176|, s18, v114
	v_fma_f32 v166, |v176|, s19, v115
	v_lshrrev_b32_e32 v167, 26, v176
	v_min3_u32 v164, v164, v165, v166
	v_bfi_b32 v168, 31, v164, v167
	s_nop 1
	v_mul_u32_u24_dpp v170, v168, v180 quad_perm:[1,2,3,3] row_mask:0xf bank_mask:0xf bound_ctrl:1
	v_mad_u32_u24 v171, v168, v181, v170
	ds_write_b8_d16_hi v184, v171
	global_store_short_d16_hi v185, v176, s[48:49]
	s_waitcnt lgkmcnt(0)
	s_barrier
	ds_read_b64 v[122:123], v105 offset:0
	ds_read_b64 v[124:125], v105 offset:8
	ds_read_b64 v[126:127], v105 offset:16
	s_barrier
	ds_read_b64 v[128:129], v105 offset:96
	ds_read_b64 v[130:131], v105 offset:104
	ds_read_b64 v[132:133], v105 offset:112
	s_waitcnt lgkmcnt(3)
	v_mfma_f32_16x16x128_f8f6f4 v[134:137], v[122:127], v[2:7], 0 cbsz:2 blgp:2
	v_mfma_f32_16x16x128_f8f6f4 v[138:141], v[122:127], v[14:19], 0 cbsz:2 blgp:2
	v_mfma_f32_16x16x128_f8f6f4 v[142:145], v[122:127], v[26:31], v[188:191] cbsz:2 blgp:2
	v_mfma_f32_16x16x128_f8f6f4 v[204:207], v[122:127], v[38:43], 0 cbsz:2 blgp:2
	v_mfma_f32_16x16x128_f8f6f4 v[208:211], v[122:127], v[50:55], 0 cbsz:2 blgp:2
	v_mfma_f32_16x16x128_f8f6f4 v[212:215], v[122:127], v[62:67], v[188:191] cbsz:2 blgp:2
	s_waitcnt lgkmcnt(0)
	v_mfma_f32_16x16x128_f8f6f4 v[134:137], v[128:133], v[8:13], v[134:137] cbsz:2 blgp:2
	v_mfma_f32_16x16x128_f8f6f4 v[204:207], v[128:133], v[44:49], v[204:207] cbsz:2 blgp:2
	v_mfma_f32_16x16x128_f8f6f4 v[138:141], v[128:133], v[20:25], v[138:141] cbsz:2 blgp:2
	v_mfma_f32_16x16x128_f8f6f4 v[208:211], v[128:133], v[56:61], v[208:211] cbsz:2 blgp:2
	v_mfma_f32_16x16x128_f8f6f4 v[142:145], v[128:133], v[32:37], v[142:145] cbsz:2 blgp:2
	v_mfma_f32_16x16x128_f8f6f4 v[212:215], v[128:133], v[68:73], v[212:215] cbsz:2 blgp:2
	v_cndmask_b32_e64 v158, v134, v204, s[0:1]
	v_fma_mix_f32 v158, v158, v100, v147 op_sel_hi:[0,0,1]
	v_exp_f32_e32 v158, v158
	v_cndmask_b32_e64 v159, v138, v208, s[0:1]
	v_fma_mix_f32 v159, v159, v101, v151 op_sel_hi:[0,0,1]
	v_exp_f32_e32 v159, v159
	v_fma_f32 v158, v158, v186, v186
	v_rcp_f32_e32 v158, v158
	v_add_f32_e32 v159, 1.0, v159
	v_rcp_f32_e32 v159, v159
	v_cndmask_b32_e64 v160, v142, v212, s[0:1]
	v_fma_mix_f32 v161, v158, v160, v155 op_sel_hi:[0,0,1]
	v_exp_f32_e32 v161, v161
	s_add_u32 s48, s48, s40
	v_add_f32_e32 v161, 1.0, v161
	v_rcp_f32_e32 v161, v161
	s_addc_u32 s49, s49, s41
	v_fma_f32 v162, v161, -2.0, 1.0
	v_sub_f32_e32 v163, v176, v162
	v_fma_f32 v176, v159, v163, v162
	v_fma_f32 v164, |v176|, s17, v113
	v_fma_f32 v165, |v176|, s18, v114
	v_fma_f32 v166, |v176|, s19, v115
	v_lshrrev_b32_e32 v167, 26, v176
	v_min3_u32 v164, v164, v165, v166
	v_bfi_b32 v168, 31, v164, v167
	s_nop 1
	v_mul_u32_u24_dpp v170, v168, v180 quad_perm:[1,2,3,3] row_mask:0xf bank_mask:0xf bound_ctrl:1
	v_mad_u32_u24 v171, v168, v181, v170
	ds_write_b8_d16_hi v184, v171 offset:416
	global_store_short_d16_hi v185, v176, s[48:49]
	s_waitcnt lgkmcnt(0)
	s_barrier
	ds_read_b64 v[122:123], v105 offset:416
	ds_read_b64 v[124:125], v105 offset:424
	ds_read_b64 v[126:127], v105 offset:432
	s_barrier
	ds_read_b64 v[128:129], v105 offset:512
	ds_read_b64 v[130:131], v105 offset:520
	ds_read_b64 v[132:133], v105 offset:528
	s_waitcnt lgkmcnt(3)
	v_mfma_f32_16x16x128_f8f6f4 v[134:137], v[122:127], v[2:7], 0 cbsz:2 blgp:2
	v_mfma_f32_16x16x128_f8f6f4 v[138:141], v[122:127], v[14:19], 0 cbsz:2 blgp:2
	v_mfma_f32_16x16x128_f8f6f4 v[142:145], v[122:127], v[26:31], v[188:191] cbsz:2 blgp:2
	v_mfma_f32_16x16x128_f8f6f4 v[204:207], v[122:127], v[38:43], 0 cbsz:2 blgp:2
	v_mfma_f32_16x16x128_f8f6f4 v[208:211], v[122:127], v[50:55], 0 cbsz:2 blgp:2
	v_mfma_f32_16x16x128_f8f6f4 v[212:215], v[122:127], v[62:67], v[188:191] cbsz:2 blgp:2
	s_waitcnt lgkmcnt(0)
	v_mfma_f32_16x16x128_f8f6f4 v[134:137], v[128:133], v[8:13], v[134:137] cbsz:2 blgp:2
	v_mfma_f32_16x16x128_f8f6f4 v[204:207], v[128:133], v[44:49], v[204:207] cbsz:2 blgp:2
	v_mfma_f32_16x16x128_f8f6f4 v[138:141], v[128:133], v[20:25], v[138:141] cbsz:2 blgp:2
	v_mfma_f32_16x16x128_f8f6f4 v[208:211], v[128:133], v[56:61], v[208:211] cbsz:2 blgp:2
	v_mfma_f32_16x16x128_f8f6f4 v[142:145], v[128:133], v[32:37], v[142:145] cbsz:2 blgp:2
	v_mfma_f32_16x16x128_f8f6f4 v[212:215], v[128:133], v[68:73], v[212:215] cbsz:2 blgp:2
	v_cndmask_b32_e64 v158, v134, v204, s[0:1]
	v_fma_mix_f32 v158, v158, v100, v147 op_sel:[0,0,1] op_sel_hi:[0,0,1]
	v_exp_f32_e32 v158, v158
	v_cndmask_b32_e64 v159, v138, v208, s[0:1]
	v_fma_mix_f32 v159, v159, v101, v151 op_sel:[0,0,1] op_sel_hi:[0,0,1]
	v_exp_f32_e32 v159, v159
	v_fma_f32 v158, v158, v186, v186
	v_rcp_f32_e32 v158, v158
	v_add_f32_e32 v159, 1.0, v159
	v_rcp_f32_e32 v159, v159
	v_cndmask_b32_e64 v160, v142, v212, s[0:1]
	v_fma_mix_f32 v161, v158, v160, v155 op_sel:[0,0,1] op_sel_hi:[0,0,1]
	v_exp_f32_e32 v161, v161
	s_add_u32 s48, s48, s40
	v_add_f32_e32 v161, 1.0, v161
	v_rcp_f32_e32 v161, v161
	s_addc_u32 s49, s49, s41
	v_fma_f32 v162, v161, -2.0, 1.0
	v_sub_f32_e32 v163, v176, v162
	v_fma_f32 v176, v159, v163, v162
	v_fma_f32 v164, |v176|, s17, v113
	v_fma_f32 v165, |v176|, s18, v114
	v_fma_f32 v166, |v176|, s19, v115
	v_lshrrev_b32_e32 v167, 26, v176
	v_min3_u32 v164, v164, v165, v166
	v_bfi_b32 v168, 31, v164, v167
	s_nop 1
	v_mul_u32_u24_dpp v170, v168, v180 quad_perm:[1,2,3,3] row_mask:0xf bank_mask:0xf bound_ctrl:1
	v_mad_u32_u24 v171, v168, v181, v170
	ds_write_b8_d16_hi v184, v171
	global_store_short_d16_hi v185, v176, s[48:49]
	s_waitcnt lgkmcnt(0)
	s_barrier
	ds_read_b64 v[122:123], v105 offset:0
	ds_read_b64 v[124:125], v105 offset:8
	ds_read_b64 v[126:127], v105 offset:16
	s_barrier
	ds_read_b64 v[128:129], v105 offset:96
	ds_read_b64 v[130:131], v105 offset:104
	ds_read_b64 v[132:133], v105 offset:112
	s_waitcnt lgkmcnt(3)
	v_mfma_f32_16x16x128_f8f6f4 v[134:137], v[122:127], v[2:7], 0 cbsz:2 blgp:2
	v_mfma_f32_16x16x128_f8f6f4 v[138:141], v[122:127], v[14:19], 0 cbsz:2 blgp:2
	v_mfma_f32_16x16x128_f8f6f4 v[142:145], v[122:127], v[26:31], v[188:191] cbsz:2 blgp:2
	v_mfma_f32_16x16x128_f8f6f4 v[204:207], v[122:127], v[38:43], 0 cbsz:2 blgp:2
	v_mfma_f32_16x16x128_f8f6f4 v[208:211], v[122:127], v[50:55], 0 cbsz:2 blgp:2
	v_mfma_f32_16x16x128_f8f6f4 v[212:215], v[122:127], v[62:67], v[188:191] cbsz:2 blgp:2
	s_waitcnt lgkmcnt(0)
	v_mfma_f32_16x16x128_f8f6f4 v[134:137], v[128:133], v[8:13], v[134:137] cbsz:2 blgp:2
	v_mfma_f32_16x16x128_f8f6f4 v[204:207], v[128:133], v[44:49], v[204:207] cbsz:2 blgp:2
	v_mfma_f32_16x16x128_f8f6f4 v[138:141], v[128:133], v[20:25], v[138:141] cbsz:2 blgp:2
	v_mfma_f32_16x16x128_f8f6f4 v[208:211], v[128:133], v[56:61], v[208:211] cbsz:2 blgp:2
	v_mfma_f32_16x16x128_f8f6f4 v[142:145], v[128:133], v[32:37], v[142:145] cbsz:2 blgp:2
	v_mfma_f32_16x16x128_f8f6f4 v[212:215], v[128:133], v[68:73], v[212:215] cbsz:2 blgp:2
	v_cndmask_b32_e64 v158, v134, v204, s[0:1]
	v_fma_mix_f32 v158, v158, v100, v148 op_sel_hi:[0,0,1]
	v_exp_f32_e32 v158, v158
	v_cndmask_b32_e64 v159, v138, v208, s[0:1]
	v_fma_mix_f32 v159, v159, v101, v152 op_sel_hi:[0,0,1]
	v_exp_f32_e32 v159, v159
	v_fma_f32 v158, v158, v186, v186
	v_rcp_f32_e32 v158, v158
	v_add_f32_e32 v159, 1.0, v159
	v_rcp_f32_e32 v159, v159
	v_cndmask_b32_e64 v160, v142, v212, s[0:1]
	v_fma_mix_f32 v161, v158, v160, v156 op_sel_hi:[0,0,1]
	v_exp_f32_e32 v161, v161
	s_add_u32 s48, s48, s40
	v_add_f32_e32 v161, 1.0, v161
	v_rcp_f32_e32 v161, v161
	s_addc_u32 s49, s49, s41
	v_fma_f32 v162, v161, -2.0, 1.0
	v_sub_f32_e32 v163, v176, v162
	v_fma_f32 v176, v159, v163, v162
	v_fma_f32 v164, |v176|, s17, v113
	v_fma_f32 v165, |v176|, s18, v114
	v_fma_f32 v166, |v176|, s19, v115
	v_lshrrev_b32_e32 v167, 26, v176
	v_min3_u32 v164, v164, v165, v166
	v_bfi_b32 v168, 31, v164, v167
	s_nop 1
	v_mul_u32_u24_dpp v170, v168, v180 quad_perm:[1,2,3,3] row_mask:0xf bank_mask:0xf bound_ctrl:1
	v_mad_u32_u24 v171, v168, v181, v170
	ds_write_b8_d16_hi v184, v171 offset:416
	global_store_short_d16_hi v185, v176, s[48:49]
	s_waitcnt lgkmcnt(0)
	s_barrier
	ds_read_b64 v[122:123], v105 offset:416
	ds_read_b64 v[124:125], v105 offset:424
	ds_read_b64 v[126:127], v105 offset:432
	s_barrier
	ds_read_b64 v[128:129], v105 offset:512
	ds_read_b64 v[130:131], v105 offset:520
	ds_read_b64 v[132:133], v105 offset:528
	s_waitcnt lgkmcnt(3)
	v_mfma_f32_16x16x128_f8f6f4 v[134:137], v[122:127], v[2:7], 0 cbsz:2 blgp:2
	v_mfma_f32_16x16x128_f8f6f4 v[138:141], v[122:127], v[14:19], 0 cbsz:2 blgp:2
	v_mfma_f32_16x16x128_f8f6f4 v[142:145], v[122:127], v[26:31], v[188:191] cbsz:2 blgp:2
	v_mfma_f32_16x16x128_f8f6f4 v[204:207], v[122:127], v[38:43], 0 cbsz:2 blgp:2
	v_mfma_f32_16x16x128_f8f6f4 v[208:211], v[122:127], v[50:55], 0 cbsz:2 blgp:2
	v_mfma_f32_16x16x128_f8f6f4 v[212:215], v[122:127], v[62:67], v[188:191] cbsz:2 blgp:2
	s_waitcnt lgkmcnt(0)
	v_mfma_f32_16x16x128_f8f6f4 v[134:137], v[128:133], v[8:13], v[134:137] cbsz:2 blgp:2
	v_mfma_f32_16x16x128_f8f6f4 v[204:207], v[128:133], v[44:49], v[204:207] cbsz:2 blgp:2
	v_mfma_f32_16x16x128_f8f6f4 v[138:141], v[128:133], v[20:25], v[138:141] cbsz:2 blgp:2
	v_mfma_f32_16x16x128_f8f6f4 v[208:211], v[128:133], v[56:61], v[208:211] cbsz:2 blgp:2
	v_mfma_f32_16x16x128_f8f6f4 v[142:145], v[128:133], v[32:37], v[142:145] cbsz:2 blgp:2
	v_mfma_f32_16x16x128_f8f6f4 v[212:215], v[128:133], v[68:73], v[212:215] cbsz:2 blgp:2
	v_cndmask_b32_e64 v158, v134, v204, s[0:1]
	v_fma_mix_f32 v158, v158, v100, v148 op_sel:[0,0,1] op_sel_hi:[0,0,1]
	v_exp_f32_e32 v158, v158
	v_cndmask_b32_e64 v159, v138, v208, s[0:1]
	v_fma_mix_f32 v159, v159, v101, v152 op_sel:[0,0,1] op_sel_hi:[0,0,1]
	v_exp_f32_e32 v159, v159
	v_fma_f32 v158, v158, v186, v186
	v_rcp_f32_e32 v158, v158
	v_add_f32_e32 v159, 1.0, v159
	v_rcp_f32_e32 v159, v159
	v_cndmask_b32_e64 v160, v142, v212, s[0:1]
	v_fma_mix_f32 v161, v158, v160, v156 op_sel:[0,0,1] op_sel_hi:[0,0,1]
	v_exp_f32_e32 v161, v161
	s_add_u32 s48, s48, s40
	v_add_f32_e32 v161, 1.0, v161
	v_rcp_f32_e32 v161, v161
	s_addc_u32 s49, s49, s41
	v_fma_f32 v162, v161, -2.0, 1.0
	v_sub_f32_e32 v163, v176, v162
	v_fma_f32 v176, v159, v163, v162
	v_fma_f32 v164, |v176|, s17, v113
	v_fma_f32 v165, |v176|, s18, v114
	v_fma_f32 v166, |v176|, s19, v115
	v_lshrrev_b32_e32 v167, 26, v176
	v_min3_u32 v164, v164, v165, v166
	v_bfi_b32 v168, 31, v164, v167
	s_nop 1
	v_mul_u32_u24_dpp v170, v168, v180 quad_perm:[1,2,3,3] row_mask:0xf bank_mask:0xf bound_ctrl:1
	v_mad_u32_u24 v171, v168, v181, v170
	ds_write_b8_d16_hi v184, v171
	global_store_short_d16_hi v185, v176, s[48:49]
	s_waitcnt lgkmcnt(0)
	s_barrier
	ds_read_b64 v[122:123], v105 offset:0
	ds_read_b64 v[124:125], v105 offset:8
	ds_read_b64 v[126:127], v105 offset:16
	s_barrier
	ds_read_b64 v[128:129], v105 offset:96
	ds_read_b64 v[130:131], v105 offset:104
	ds_read_b64 v[132:133], v105 offset:112
	s_waitcnt lgkmcnt(3)
	v_mfma_f32_16x16x128_f8f6f4 v[134:137], v[122:127], v[2:7], 0 cbsz:2 blgp:2
	v_mfma_f32_16x16x128_f8f6f4 v[138:141], v[122:127], v[14:19], 0 cbsz:2 blgp:2
	v_mfma_f32_16x16x128_f8f6f4 v[142:145], v[122:127], v[26:31], v[188:191] cbsz:2 blgp:2
	v_mfma_f32_16x16x128_f8f6f4 v[204:207], v[122:127], v[38:43], 0 cbsz:2 blgp:2
	v_mfma_f32_16x16x128_f8f6f4 v[208:211], v[122:127], v[50:55], 0 cbsz:2 blgp:2
	v_mfma_f32_16x16x128_f8f6f4 v[212:215], v[122:127], v[62:67], v[188:191] cbsz:2 blgp:2
	s_waitcnt lgkmcnt(0)
	v_mfma_f32_16x16x128_f8f6f4 v[134:137], v[128:133], v[8:13], v[134:137] cbsz:2 blgp:2
	v_mfma_f32_16x16x128_f8f6f4 v[204:207], v[128:133], v[44:49], v[204:207] cbsz:2 blgp:2
	v_mfma_f32_16x16x128_f8f6f4 v[138:141], v[128:133], v[20:25], v[138:141] cbsz:2 blgp:2
	v_mfma_f32_16x16x128_f8f6f4 v[208:211], v[128:133], v[56:61], v[208:211] cbsz:2 blgp:2
	v_mfma_f32_16x16x128_f8f6f4 v[142:145], v[128:133], v[32:37], v[142:145] cbsz:2 blgp:2
	v_mfma_f32_16x16x128_f8f6f4 v[212:215], v[128:133], v[68:73], v[212:215] cbsz:2 blgp:2
	v_cndmask_b32_e64 v158, v134, v204, s[0:1]
	v_fma_mix_f32 v158, v158, v100, v149 op_sel_hi:[0,0,1]
	v_exp_f32_e32 v158, v158
	v_cndmask_b32_e64 v159, v138, v208, s[0:1]
	v_fma_mix_f32 v159, v159, v101, v153 op_sel_hi:[0,0,1]
	v_exp_f32_e32 v159, v159
	v_fma_f32 v158, v158, v186, v186
	v_rcp_f32_e32 v158, v158
	v_add_f32_e32 v159, 1.0, v159
	v_rcp_f32_e32 v159, v159
	v_cndmask_b32_e64 v160, v142, v212, s[0:1]
	v_fma_mix_f32 v161, v158, v160, v157 op_sel_hi:[0,0,1]
	v_exp_f32_e32 v161, v161
	s_add_u32 s48, s48, s40
	v_add_f32_e32 v161, 1.0, v161
	v_rcp_f32_e32 v161, v161
	s_addc_u32 s49, s49, s41
	v_fma_f32 v162, v161, -2.0, 1.0
	v_sub_f32_e32 v163, v176, v162
	v_fma_f32 v176, v159, v163, v162
	v_fma_f32 v164, |v176|, s17, v113
	v_fma_f32 v165, |v176|, s18, v114
	v_fma_f32 v166, |v176|, s19, v115
	v_lshrrev_b32_e32 v167, 26, v176
	v_min3_u32 v164, v164, v165, v166
	v_bfi_b32 v168, 31, v164, v167
	s_nop 1
	v_mul_u32_u24_dpp v170, v168, v180 quad_perm:[1,2,3,3] row_mask:0xf bank_mask:0xf bound_ctrl:1
	v_mad_u32_u24 v171, v168, v181, v170
	ds_write_b8_d16_hi v184, v171 offset:416
	global_store_short_d16_hi v185, v176, s[48:49]
	s_waitcnt lgkmcnt(0)
	s_barrier
	ds_read_b64 v[122:123], v105 offset:416
	ds_read_b64 v[124:125], v105 offset:424
	ds_read_b64 v[126:127], v105 offset:432
	s_barrier
	ds_read_b64 v[128:129], v105 offset:512
	ds_read_b64 v[130:131], v105 offset:520
	ds_read_b64 v[132:133], v105 offset:528
	s_add_i32 s44, s44, 16
	s_waitcnt lgkmcnt(3)
	v_mfma_f32_16x16x128_f8f6f4 v[134:137], v[122:127], v[2:7], 0 cbsz:2 blgp:2
	v_mfma_f32_16x16x128_f8f6f4 v[138:141], v[122:127], v[14:19], 0 cbsz:2 blgp:2
	v_mfma_f32_16x16x128_f8f6f4 v[142:145], v[122:127], v[26:31], v[188:191] cbsz:2 blgp:2
	v_mfma_f32_16x16x128_f8f6f4 v[204:207], v[122:127], v[38:43], 0 cbsz:2 blgp:2
	v_mfma_f32_16x16x128_f8f6f4 v[208:211], v[122:127], v[50:55], 0 cbsz:2 blgp:2
	v_mfma_f32_16x16x128_f8f6f4 v[212:215], v[122:127], v[62:67], v[188:191] cbsz:2 blgp:2
	s_waitcnt lgkmcnt(0)
	v_mfma_f32_16x16x128_f8f6f4 v[134:137], v[128:133], v[8:13], v[134:137] cbsz:2 blgp:2
	v_mfma_f32_16x16x128_f8f6f4 v[204:207], v[128:133], v[44:49], v[204:207] cbsz:2 blgp:2
	v_mfma_f32_16x16x128_f8f6f4 v[138:141], v[128:133], v[20:25], v[138:141] cbsz:2 blgp:2
	v_mfma_f32_16x16x128_f8f6f4 v[208:211], v[128:133], v[56:61], v[208:211] cbsz:2 blgp:2
	v_mfma_f32_16x16x128_f8f6f4 v[142:145], v[128:133], v[32:37], v[142:145] cbsz:2 blgp:2
	v_mfma_f32_16x16x128_f8f6f4 v[212:215], v[128:133], v[68:73], v[212:215] cbsz:2 blgp:2
	v_cndmask_b32_e64 v158, v134, v204, s[0:1]
	v_fma_mix_f32 v158, v158, v100, v149 op_sel:[0,0,1] op_sel_hi:[0,0,1]
	v_exp_f32_e32 v158, v158
	v_cndmask_b32_e64 v159, v138, v208, s[0:1]
	v_fma_mix_f32 v159, v159, v101, v153 op_sel:[0,0,1] op_sel_hi:[0,0,1]
	v_exp_f32_e32 v159, v159
	v_fma_f32 v158, v158, v186, v186
	v_rcp_f32_e32 v158, v158
	v_add_f32_e32 v159, 1.0, v159
	v_rcp_f32_e32 v159, v159
	v_cndmask_b32_e64 v160, v142, v212, s[0:1]
	v_fma_mix_f32 v161, v158, v160, v157 op_sel:[0,0,1] op_sel_hi:[0,0,1]
	v_exp_f32_e32 v161, v161
	s_add_u32 s48, s48, s40
	v_add_f32_e32 v161, 1.0, v161
	v_rcp_f32_e32 v161, v161
	s_addc_u32 s49, s49, s41
	v_fma_f32 v162, v161, -2.0, 1.0
	v_sub_f32_e32 v163, v176, v162
	v_fma_f32 v176, v159, v163, v162
	v_fma_f32 v164, |v176|, s17, v113
	v_fma_f32 v165, |v176|, s18, v114
	v_fma_f32 v166, |v176|, s19, v115
	v_lshrrev_b32_e32 v167, 26, v176
	v_min3_u32 v164, v164, v165, v166
	v_bfi_b32 v168, 31, v164, v167
	s_nop 1
	v_mul_u32_u24_dpp v170, v168, v180 quad_perm:[1,2,3,3] row_mask:0xf bank_mask:0xf bound_ctrl:1
	v_mad_u32_u24 v171, v168, v181, v170
	ds_write_b8_d16_hi v184, v171
	global_store_short_d16_hi v185, v176, s[48:49]
	s_waitcnt lgkmcnt(0)
	s_barrier
	ds_read_b64 v[122:123], v105 offset:0
	ds_read_b64 v[124:125], v105 offset:8
	ds_read_b64 v[126:127], v105 offset:16
	s_cmp_lt_i32 s44, s45
	s_cbranch_scc1 .Lscan_loop_a_f2
	s_barrier
	s_branch .Lscan_exit_f2

.Lscan_enter_b_f2:
	ds_read_b64 v[122:123], v105 offset:0
	ds_read_b64 v[124:125], v105 offset:8
	ds_read_b64 v[126:127], v105 offset:16
	ds_read_b64 v[128:129], v105 offset:96
	ds_read_b64 v[130:131], v105 offset:104
	ds_read_b64 v[132:133], v105 offset:112
	s_waitcnt vmcnt(8)
	global_load_dwordx4 v[146:149], v[196:197], off
	global_load_dwordx4 v[150:153], v[196:197], off offset:512
	global_load_dwordx4 v[154:157], v[196:197], off offset:1024
	v_lshl_add_u64 v[196:197], v[196:197], 0, s[42:43]
	s_waitcnt lgkmcnt(3)
	v_mfma_f32_16x16x128_f8f6f4 v[134:137], v[122:127], v[2:7], 0 cbsz:2 blgp:2
	v_mfma_f32_16x16x128_f8f6f4 v[138:141], v[122:127], v[14:19], 0 cbsz:2 blgp:2
	v_mfma_f32_16x16x128_f8f6f4 v[142:145], v[122:127], v[26:31], v[188:191] cbsz:2 blgp:2
	v_mfma_f32_16x16x128_f8f6f4 v[204:207], v[122:127], v[38:43], 0 cbsz:2 blgp:2
	v_mfma_f32_16x16x128_f8f6f4 v[208:211], v[122:127], v[50:55], 0 cbsz:2 blgp:2
	v_mfma_f32_16x16x128_f8f6f4 v[212:215], v[122:127], v[62:67], v[188:191] cbsz:2 blgp:2
	s_waitcnt lgkmcnt(0)
	v_mfma_f32_16x16x128_f8f6f4 v[134:137], v[128:133], v[8:13], v[134:137] cbsz:2 blgp:2
	v_mfma_f32_16x16x128_f8f6f4 v[204:207], v[128:133], v[44:49], v[204:207] cbsz:2 blgp:2
	v_mfma_f32_16x16x128_f8f6f4 v[138:141], v[128:133], v[20:25], v[138:141] cbsz:2 blgp:2
	v_mfma_f32_16x16x128_f8f6f4 v[208:211], v[128:133], v[56:61], v[208:211] cbsz:2 blgp:2
	v_mfma_f32_16x16x128_f8f6f4 v[142:145], v[128:133], v[32:37], v[142:145] cbsz:2 blgp:2
	v_mfma_f32_16x16x128_f8f6f4 v[212:215], v[128:133], v[68:73], v[212:215] cbsz:2 blgp:2
	v_cndmask_b32_e64 v158, v134, v204, s[0:1]
	v_fma_mix_f32 v158, v158, v100, v82 op_sel_hi:[0,0,1]
	v_exp_f32_e32 v158, v158
	v_cndmask_b32_e64 v159, v138, v208, s[0:1]
	v_fma_mix_f32 v159, v159, v101, v74 op_sel_hi:[0,0,1]
	v_exp_f32_e32 v159, v159
	v_fma_f32 v158, v158, v186, v186
	v_rcp_f32_e32 v158, v158
	v_add_f32_e32 v159, 1.0, v159
	v_rcp_f32_e32 v159, v159
	v_cndmask_b32_e64 v160, v142, v212, s[0:1]
	v_fma_mix_f32 v161, v158, v160, v78 op_sel_hi:[0,0,1]
	v_exp_f32_e32 v161, v161
	s_add_u32 s48, s48, s40
	v_add_f32_e32 v161, 1.0, v161
	v_rcp_f32_e32 v161, v161
	s_addc_u32 s49, s49, s41
	v_fma_f32 v162, v161, -2.0, 1.0
	v_sub_f32_e32 v163, v176, v162
	v_fma_f32 v176, v159, v163, v162
	v_fma_f32 v164, |v176|, s17, v113
	v_fma_f32 v165, |v176|, s18, v114
	v_fma_f32 v166, |v176|, s19, v115
	v_lshrrev_b32_e32 v167, 26, v176
	v_min3_u32 v164, v164, v165, v166
	v_bfi_b32 v168, 31, v164, v167
	s_nop 1
	v_mul_u32_u24_dpp v170, v168, v180 quad_perm:[1,2,3,3] row_mask:0xf bank_mask:0xf bound_ctrl:1
	v_mad_u32_u24 v171, v168, v181, v170
	ds_write_b8_d16_hi v184, v171 offset:416
	s_barrier
	global_store_short_d16_hi v185, v176, s[48:49]
	s_waitcnt lgkmcnt(0)
	s_barrier
	ds_read_b64 v[122:123], v105 offset:416
	ds_read_b64 v[124:125], v105 offset:424
	ds_read_b64 v[126:127], v105 offset:432
	ds_read_b64 v[128:129], v105 offset:512
	ds_read_b64 v[130:131], v105 offset:520
	ds_read_b64 v[132:133], v105 offset:528
	s_waitcnt lgkmcnt(3)
	v_mfma_f32_16x16x128_f8f6f4 v[134:137], v[122:127], v[2:7], 0 cbsz:2 blgp:2
	v_mfma_f32_16x16x128_f8f6f4 v[138:141], v[122:127], v[14:19], 0 cbsz:2 blgp:2
	v_mfma_f32_16x16x128_f8f6f4 v[142:145], v[122:127], v[26:31], v[188:191] cbsz:2 blgp:2
	v_mfma_f32_16x16x128_f8f6f4 v[204:207], v[122:127], v[38:43], 0 cbsz:2 blgp:2
	v_mfma_f32_16x16x128_f8f6f4 v[208:211], v[122:127], v[50:55], 0 cbsz:2 blgp:2
	v_mfma_f32_16x16x128_f8f6f4 v[212:215], v[122:127], v[62:67], v[188:191] cbsz:2 blgp:2
	s_waitcnt lgkmcnt(0)
	v_mfma_f32_16x16x128_f8f6f4 v[134:137], v[128:133], v[8:13], v[134:137] cbsz:2 blgp:2
	v_mfma_f32_16x16x128_f8f6f4 v[204:207], v[128:133], v[44:49], v[204:207] cbsz:2 blgp:2
	v_mfma_f32_16x16x128_f8f6f4 v[138:141], v[128:133], v[20:25], v[138:141] cbsz:2 blgp:2
	v_mfma_f32_16x16x128_f8f6f4 v[208:211], v[128:133], v[56:61], v[208:211] cbsz:2 blgp:2
	v_mfma_f32_16x16x128_f8f6f4 v[142:145], v[128:133], v[32:37], v[142:145] cbsz:2 blgp:2
	v_mfma_f32_16x16x128_f8f6f4 v[212:215], v[128:133], v[68:73], v[212:215] cbsz:2 blgp:2
	v_cndmask_b32_e64 v158, v134, v204, s[0:1]
	v_fma_mix_f32 v158, v158, v100, v82 op_sel:[0,0,1] op_sel_hi:[0,0,1]
	v_exp_f32_e32 v158, v158
	v_cndmask_b32_e64 v159, v138, v208, s[0:1]
	v_fma_mix_f32 v159, v159, v101, v74 op_sel:[0,0,1] op_sel_hi:[0,0,1]
	v_exp_f32_e32 v159, v159
	v_fma_f32 v158, v158, v186, v186
	v_rcp_f32_e32 v158, v158
	v_add_f32_e32 v159, 1.0, v159
	v_rcp_f32_e32 v159, v159
	v_cndmask_b32_e64 v160, v142, v212, s[0:1]
	v_fma_mix_f32 v161, v158, v160, v78 op_sel:[0,0,1] op_sel_hi:[0,0,1]
	v_exp_f32_e32 v161, v161
	s_add_u32 s48, s48, s40
	v_add_f32_e32 v161, 1.0, v161
	v_rcp_f32_e32 v161, v161
	s_addc_u32 s49, s49, s41
	v_fma_f32 v162, v161, -2.0, 1.0
	v_sub_f32_e32 v163, v176, v162
	v_fma_f32 v176, v159, v163, v162
	v_fma_f32 v164, |v176|, s17, v113
	v_fma_f32 v165, |v176|, s18, v114
	v_fma_f32 v166, |v176|, s19, v115
	v_lshrrev_b32_e32 v167, 26, v176
	v_min3_u32 v164, v164, v165, v166
	v_bfi_b32 v168, 31, v164, v167
	s_nop 1
	v_mul_u32_u24_dpp v170, v168, v180 quad_perm:[1,2,3,3] row_mask:0xf bank_mask:0xf bound_ctrl:1
	v_mad_u32_u24 v171, v168, v181, v170
	ds_write_b8_d16_hi v184, v171
	s_barrier
	global_store_short_d16_hi v185, v176, s[48:49]
	s_waitcnt lgkmcnt(0)
	s_barrier
	ds_read_b64 v[122:123], v105 offset:0
	ds_read_b64 v[124:125], v105 offset:8
	ds_read_b64 v[126:127], v105 offset:16
	ds_read_b64 v[128:129], v105 offset:96
	ds_read_b64 v[130:131], v105 offset:104
	ds_read_b64 v[132:133], v105 offset:112
	s_waitcnt lgkmcnt(3)
	v_mfma_f32_16x16x128_f8f6f4 v[134:137], v[122:127], v[2:7], 0 cbsz:2 blgp:2
	v_mfma_f32_16x16x128_f8f6f4 v[138:141], v[122:127], v[14:19], 0 cbsz:2 blgp:2
	v_mfma_f32_16x16x128_f8f6f4 v[142:145], v[122:127], v[26:31], v[188:191] cbsz:2 blgp:2
	v_mfma_f32_16x16x128_f8f6f4 v[204:207], v[122:127], v[38:43], 0 cbsz:2 blgp:2
	v_mfma_f32_16x16x128_f8f6f4 v[208:211], v[122:127], v[50:55], 0 cbsz:2 blgp:2
	v_mfma_f32_16x16x128_f8f6f4 v[212:215], v[122:127], v[62:67], v[188:191] cbsz:2 blgp:2
	s_waitcnt lgkmcnt(0)
	v_mfma_f32_16x16x128_f8f6f4 v[134:137], v[128:133], v[8:13], v[134:137] cbsz:2 blgp:2
	v_mfma_f32_16x16x128_f8f6f4 v[204:207], v[128:133], v[44:49], v[204:207] cbsz:2 blgp:2
	v_mfma_f32_16x16x128_f8f6f4 v[138:141], v[128:133], v[20:25], v[138:141] cbsz:2 blgp:2
	v_mfma_f32_16x16x128_f8f6f4 v[208:211], v[128:133], v[56:61], v[208:211] cbsz:2 blgp:2
	v_mfma_f32_16x16x128_f8f6f4 v[142:145], v[128:133], v[32:37], v[142:145] cbsz:2 blgp:2
	v_mfma_f32_16x16x128_f8f6f4 v[212:215], v[128:133], v[68:73], v[212:215] cbsz:2 blgp:2
	v_cndmask_b32_e64 v158, v134, v204, s[0:1]
	v_fma_mix_f32 v158, v158, v100, v83 op_sel_hi:[0,0,1]
	v_exp_f32_e32 v158, v158
	v_cndmask_b32_e64 v159, v138, v208, s[0:1]
	v_fma_mix_f32 v159, v159, v101, v75 op_sel_hi:[0,0,1]
	v_exp_f32_e32 v159, v159
	v_fma_f32 v158, v158, v186, v186
	v_rcp_f32_e32 v158, v158
	v_add_f32_e32 v159, 1.0, v159
	v_rcp_f32_e32 v159, v159
	v_cndmask_b32_e64 v160, v142, v212, s[0:1]
	v_fma_mix_f32 v161, v158, v160, v79 op_sel_hi:[0,0,1]
	v_exp_f32_e32 v161, v161
	s_add_u32 s48, s48, s40
	v_add_f32_e32 v161, 1.0, v161
	v_rcp_f32_e32 v161, v161
	s_addc_u32 s49, s49, s41
	v_fma_f32 v162, v161, -2.0, 1.0
	v_sub_f32_e32 v163, v176, v162
	v_fma_f32 v176, v159, v163, v162
	v_fma_f32 v164, |v176|, s17, v113
	v_fma_f32 v165, |v176|, s18, v114
	v_fma_f32 v166, |v176|, s19, v115
	v_lshrrev_b32_e32 v167, 26, v176
	v_min3_u32 v164, v164, v165, v166
	v_bfi_b32 v168, 31, v164, v167
	s_nop 1
	v_mul_u32_u24_dpp v170, v168, v180 quad_perm:[1,2,3,3] row_mask:0xf bank_mask:0xf bound_ctrl:1
	v_mad_u32_u24 v171, v168, v181, v170
	ds_write_b8_d16_hi v184, v171 offset:416
	s_barrier
	global_store_short_d16_hi v185, v176, s[48:49]
	s_waitcnt lgkmcnt(0)
	s_barrier
	ds_read_b64 v[122:123], v105 offset:416
	ds_read_b64 v[124:125], v105 offset:424
	ds_read_b64 v[126:127], v105 offset:432
	ds_read_b64 v[128:129], v105 offset:512
	ds_read_b64 v[130:131], v105 offset:520
	ds_read_b64 v[132:133], v105 offset:528
	s_waitcnt lgkmcnt(3)
	v_mfma_f32_16x16x128_f8f6f4 v[134:137], v[122:127], v[2:7], 0 cbsz:2 blgp:2
	v_mfma_f32_16x16x128_f8f6f4 v[138:141], v[122:127], v[14:19], 0 cbsz:2 blgp:2
	v_mfma_f32_16x16x128_f8f6f4 v[142:145], v[122:127], v[26:31], v[188:191] cbsz:2 blgp:2
	v_mfma_f32_16x16x128_f8f6f4 v[204:207], v[122:127], v[38:43], 0 cbsz:2 blgp:2
	v_mfma_f32_16x16x128_f8f6f4 v[208:211], v[122:127], v[50:55], 0 cbsz:2 blgp:2
	v_mfma_f32_16x16x128_f8f6f4 v[212:215], v[122:127], v[62:67], v[188:191] cbsz:2 blgp:2
	s_waitcnt lgkmcnt(0)
	v_mfma_f32_16x16x128_f8f6f4 v[134:137], v[128:133], v[8:13], v[134:137] cbsz:2 blgp:2
	v_mfma_f32_16x16x128_f8f6f4 v[204:207], v[128:133], v[44:49], v[204:207] cbsz:2 blgp:2
	v_mfma_f32_16x16x128_f8f6f4 v[138:141], v[128:133], v[20:25], v[138:141] cbsz:2 blgp:2
	v_mfma_f32_16x16x128_f8f6f4 v[208:211], v[128:133], v[56:61], v[208:211] cbsz:2 blgp:2
	v_mfma_f32_16x16x128_f8f6f4 v[142:145], v[128:133], v[32:37], v[142:145] cbsz:2 blgp:2
	v_mfma_f32_16x16x128_f8f6f4 v[212:215], v[128:133], v[68:73], v[212:215] cbsz:2 blgp:2
	v_cndmask_b32_e64 v158, v134, v204, s[0:1]
	v_fma_mix_f32 v158, v158, v100, v83 op_sel:[0,0,1] op_sel_hi:[0,0,1]
	v_exp_f32_e32 v158, v158
	v_cndmask_b32_e64 v159, v138, v208, s[0:1]
	v_fma_mix_f32 v159, v159, v101, v75 op_sel:[0,0,1] op_sel_hi:[0,0,1]
	v_exp_f32_e32 v159, v159
	v_fma_f32 v158, v158, v186, v186
	v_rcp_f32_e32 v158, v158
	v_add_f32_e32 v159, 1.0, v159
	v_rcp_f32_e32 v159, v159
	v_cndmask_b32_e64 v160, v142, v212, s[0:1]
	v_fma_mix_f32 v161, v158, v160, v79 op_sel:[0,0,1] op_sel_hi:[0,0,1]
	v_exp_f32_e32 v161, v161
	s_add_u32 s48, s48, s40
	v_add_f32_e32 v161, 1.0, v161
	v_rcp_f32_e32 v161, v161
	s_addc_u32 s49, s49, s41
	v_fma_f32 v162, v161, -2.0, 1.0
	v_sub_f32_e32 v163, v176, v162
	v_fma_f32 v176, v159, v163, v162
	v_fma_f32 v164, |v176|, s17, v113
	v_fma_f32 v165, |v176|, s18, v114
	v_fma_f32 v166, |v176|, s19, v115
	v_lshrrev_b32_e32 v167, 26, v176
	v_min3_u32 v164, v164, v165, v166
	v_bfi_b32 v168, 31, v164, v167
	s_nop 1
	v_mul_u32_u24_dpp v170, v168, v180 quad_perm:[1,2,3,3] row_mask:0xf bank_mask:0xf bound_ctrl:1
	v_mad_u32_u24 v171, v168, v181, v170
	ds_write_b8_d16_hi v184, v171
	s_barrier
	global_store_short_d16_hi v185, v176, s[48:49]
	s_waitcnt lgkmcnt(0)
	s_barrier
	ds_read_b64 v[122:123], v105 offset:0
	ds_read_b64 v[124:125], v105 offset:8
	ds_read_b64 v[126:127], v105 offset:16
	ds_read_b64 v[128:129], v105 offset:96
	ds_read_b64 v[130:131], v105 offset:104
	ds_read_b64 v[132:133], v105 offset:112
	s_waitcnt lgkmcnt(3)
	v_mfma_f32_16x16x128_f8f6f4 v[134:137], v[122:127], v[2:7], 0 cbsz:2 blgp:2
	v_mfma_f32_16x16x128_f8f6f4 v[138:141], v[122:127], v[14:19], 0 cbsz:2 blgp:2
	v_mfma_f32_16x16x128_f8f6f4 v[142:145], v[122:127], v[26:31], v[188:191] cbsz:2 blgp:2
	v_mfma_f32_16x16x128_f8f6f4 v[204:207], v[122:127], v[38:43], 0 cbsz:2 blgp:2
	v_mfma_f32_16x16x128_f8f6f4 v[208:211], v[122:127], v[50:55], 0 cbsz:2 blgp:2
	v_mfma_f32_16x16x128_f8f6f4 v[212:215], v[122:127], v[62:67], v[188:191] cbsz:2 blgp:2
	s_waitcnt lgkmcnt(0)
	v_mfma_f32_16x16x128_f8f6f4 v[134:137], v[128:133], v[8:13], v[134:137] cbsz:2 blgp:2
	v_mfma_f32_16x16x128_f8f6f4 v[204:207], v[128:133], v[44:49], v[204:207] cbsz:2 blgp:2
	v_mfma_f32_16x16x128_f8f6f4 v[138:141], v[128:133], v[20:25], v[138:141] cbsz:2 blgp:2
	v_mfma_f32_16x16x128_f8f6f4 v[208:211], v[128:133], v[56:61], v[208:211] cbsz:2 blgp:2
	v_mfma_f32_16x16x128_f8f6f4 v[142:145], v[128:133], v[32:37], v[142:145] cbsz:2 blgp:2
	v_mfma_f32_16x16x128_f8f6f4 v[212:215], v[128:133], v[68:73], v[212:215] cbsz:2 blgp:2
	v_cndmask_b32_e64 v158, v134, v204, s[0:1]
	v_fma_mix_f32 v158, v158, v100, v84 op_sel_hi:[0,0,1]
	v_exp_f32_e32 v158, v158
	v_cndmask_b32_e64 v159, v138, v208, s[0:1]
	v_fma_mix_f32 v159, v159, v101, v76 op_sel_hi:[0,0,1]
	v_exp_f32_e32 v159, v159
	v_fma_f32 v158, v158, v186, v186
	v_rcp_f32_e32 v158, v158
	v_add_f32_e32 v159, 1.0, v159
	v_rcp_f32_e32 v159, v159
	v_cndmask_b32_e64 v160, v142, v212, s[0:1]
	v_fma_mix_f32 v161, v158, v160, v80 op_sel_hi:[0,0,1]
	v_exp_f32_e32 v161, v161
	s_add_u32 s48, s48, s40
	v_add_f32_e32 v161, 1.0, v161
	v_rcp_f32_e32 v161, v161
	s_addc_u32 s49, s49, s41
	v_fma_f32 v162, v161, -2.0, 1.0
	v_sub_f32_e32 v163, v176, v162
	v_fma_f32 v176, v159, v163, v162
	v_fma_f32 v164, |v176|, s17, v113
	v_fma_f32 v165, |v176|, s18, v114
	v_fma_f32 v166, |v176|, s19, v115
	v_lshrrev_b32_e32 v167, 26, v176
	v_min3_u32 v164, v164, v165, v166
	v_bfi_b32 v168, 31, v164, v167
	s_nop 1
	v_mul_u32_u24_dpp v170, v168, v180 quad_perm:[1,2,3,3] row_mask:0xf bank_mask:0xf bound_ctrl:1
	v_mad_u32_u24 v171, v168, v181, v170
	ds_write_b8_d16_hi v184, v171 offset:416
	s_barrier
	global_store_short_d16_hi v185, v176, s[48:49]
	s_waitcnt lgkmcnt(0)
	s_barrier
	ds_read_b64 v[122:123], v105 offset:416
	ds_read_b64 v[124:125], v105 offset:424
	ds_read_b64 v[126:127], v105 offset:432
	ds_read_b64 v[128:129], v105 offset:512
	ds_read_b64 v[130:131], v105 offset:520
	ds_read_b64 v[132:133], v105 offset:528
	s_waitcnt lgkmcnt(3)
	v_mfma_f32_16x16x128_f8f6f4 v[134:137], v[122:127], v[2:7], 0 cbsz:2 blgp:2
	v_mfma_f32_16x16x128_f8f6f4 v[138:141], v[122:127], v[14:19], 0 cbsz:2 blgp:2
	v_mfma_f32_16x16x128_f8f6f4 v[142:145], v[122:127], v[26:31], v[188:191] cbsz:2 blgp:2
	v_mfma_f32_16x16x128_f8f6f4 v[204:207], v[122:127], v[38:43], 0 cbsz:2 blgp:2
	v_mfma_f32_16x16x128_f8f6f4 v[208:211], v[122:127], v[50:55], 0 cbsz:2 blgp:2
	v_mfma_f32_16x16x128_f8f6f4 v[212:215], v[122:127], v[62:67], v[188:191] cbsz:2 blgp:2
	s_waitcnt lgkmcnt(0)
	v_mfma_f32_16x16x128_f8f6f4 v[134:137], v[128:133], v[8:13], v[134:137] cbsz:2 blgp:2
	v_mfma_f32_16x16x128_f8f6f4 v[204:207], v[128:133], v[44:49], v[204:207] cbsz:2 blgp:2
	v_mfma_f32_16x16x128_f8f6f4 v[138:141], v[128:133], v[20:25], v[138:141] cbsz:2 blgp:2
	v_mfma_f32_16x16x128_f8f6f4 v[208:211], v[128:133], v[56:61], v[208:211] cbsz:2 blgp:2
	v_mfma_f32_16x16x128_f8f6f4 v[142:145], v[128:133], v[32:37], v[142:145] cbsz:2 blgp:2
	v_mfma_f32_16x16x128_f8f6f4 v[212:215], v[128:133], v[68:73], v[212:215] cbsz:2 blgp:2
	v_cndmask_b32_e64 v158, v134, v204, s[0:1]
	v_fma_mix_f32 v158, v158, v100, v84 op_sel:[0,0,1] op_sel_hi:[0,0,1]
	v_exp_f32_e32 v158, v158
	v_cndmask_b32_e64 v159, v138, v208, s[0:1]
	v_fma_mix_f32 v159, v159, v101, v76 op_sel:[0,0,1] op_sel_hi:[0,0,1]
	v_exp_f32_e32 v159, v159
	v_fma_f32 v158, v158, v186, v186
	v_rcp_f32_e32 v158, v158
	v_add_f32_e32 v159, 1.0, v159
	v_rcp_f32_e32 v159, v159
	v_cndmask_b32_e64 v160, v142, v212, s[0:1]
	v_fma_mix_f32 v161, v158, v160, v80 op_sel:[0,0,1] op_sel_hi:[0,0,1]
	v_exp_f32_e32 v161, v161
	s_add_u32 s48, s48, s40
	v_add_f32_e32 v161, 1.0, v161
	v_rcp_f32_e32 v161, v161
	s_addc_u32 s49, s49, s41
	v_fma_f32 v162, v161, -2.0, 1.0
	v_sub_f32_e32 v163, v176, v162
	v_fma_f32 v176, v159, v163, v162
	v_fma_f32 v164, |v176|, s17, v113
	v_fma_f32 v165, |v176|, s18, v114
	v_fma_f32 v166, |v176|, s19, v115
	v_lshrrev_b32_e32 v167, 26, v176
	v_min3_u32 v164, v164, v165, v166
	v_bfi_b32 v168, 31, v164, v167
	s_nop 1
	v_mul_u32_u24_dpp v170, v168, v180 quad_perm:[1,2,3,3] row_mask:0xf bank_mask:0xf bound_ctrl:1
	v_mad_u32_u24 v171, v168, v181, v170
	ds_write_b8_d16_hi v184, v171
	s_barrier
	global_store_short_d16_hi v185, v176, s[48:49]
	s_waitcnt lgkmcnt(0)
	s_barrier
	ds_read_b64 v[122:123], v105 offset:0
	ds_read_b64 v[124:125], v105 offset:8
	ds_read_b64 v[126:127], v105 offset:16
	ds_read_b64 v[128:129], v105 offset:96
	ds_read_b64 v[130:131], v105 offset:104
	ds_read_b64 v[132:133], v105 offset:112
	s_waitcnt lgkmcnt(3)
	v_mfma_f32_16x16x128_f8f6f4 v[134:137], v[122:127], v[2:7], 0 cbsz:2 blgp:2
	v_mfma_f32_16x16x128_f8f6f4 v[138:141], v[122:127], v[14:19], 0 cbsz:2 blgp:2
	v_mfma_f32_16x16x128_f8f6f4 v[142:145], v[122:127], v[26:31], v[188:191] cbsz:2 blgp:2
	v_mfma_f32_16x16x128_f8f6f4 v[204:207], v[122:127], v[38:43], 0 cbsz:2 blgp:2
	v_mfma_f32_16x16x128_f8f6f4 v[208:211], v[122:127], v[50:55], 0 cbsz:2 blgp:2
	v_mfma_f32_16x16x128_f8f6f4 v[212:215], v[122:127], v[62:67], v[188:191] cbsz:2 blgp:2
	s_waitcnt lgkmcnt(0)
	v_mfma_f32_16x16x128_f8f6f4 v[134:137], v[128:133], v[8:13], v[134:137] cbsz:2 blgp:2
	v_mfma_f32_16x16x128_f8f6f4 v[204:207], v[128:133], v[44:49], v[204:207] cbsz:2 blgp:2
	v_mfma_f32_16x16x128_f8f6f4 v[138:141], v[128:133], v[20:25], v[138:141] cbsz:2 blgp:2
	v_mfma_f32_16x16x128_f8f6f4 v[208:211], v[128:133], v[56:61], v[208:211] cbsz:2 blgp:2
	v_mfma_f32_16x16x128_f8f6f4 v[142:145], v[128:133], v[32:37], v[142:145] cbsz:2 blgp:2
	v_mfma_f32_16x16x128_f8f6f4 v[212:215], v[128:133], v[68:73], v[212:215] cbsz:2 blgp:2
	v_cndmask_b32_e64 v158, v134, v204, s[0:1]
	v_fma_mix_f32 v158, v158, v100, v85 op_sel_hi:[0,0,1]
	v_exp_f32_e32 v158, v158
	v_cndmask_b32_e64 v159, v138, v208, s[0:1]
	v_fma_mix_f32 v159, v159, v101, v77 op_sel_hi:[0,0,1]
	v_exp_f32_e32 v159, v159
	v_fma_f32 v158, v158, v186, v186
	v_rcp_f32_e32 v158, v158
	v_add_f32_e32 v159, 1.0, v159
	v_rcp_f32_e32 v159, v159
	v_cndmask_b32_e64 v160, v142, v212, s[0:1]
	v_fma_mix_f32 v161, v158, v160, v81 op_sel_hi:[0,0,1]
	v_exp_f32_e32 v161, v161
	s_add_u32 s48, s48, s40
	v_add_f32_e32 v161, 1.0, v161
	v_rcp_f32_e32 v161, v161
	s_addc_u32 s49, s49, s41
	v_fma_f32 v162, v161, -2.0, 1.0
	v_sub_f32_e32 v163, v176, v162
	v_fma_f32 v176, v159, v163, v162
	v_fma_f32 v164, |v176|, s17, v113
	v_fma_f32 v165, |v176|, s18, v114
	v_fma_f32 v166, |v176|, s19, v115
	v_lshrrev_b32_e32 v167, 26, v176
	v_min3_u32 v164, v164, v165, v166
	v_bfi_b32 v168, 31, v164, v167
	s_nop 1
	v_mul_u32_u24_dpp v170, v168, v180 quad_perm:[1,2,3,3] row_mask:0xf bank_mask:0xf bound_ctrl:1
	v_mad_u32_u24 v171, v168, v181, v170
	ds_write_b8_d16_hi v184, v171 offset:416
	s_barrier
	global_store_short_d16_hi v185, v176, s[48:49]
	s_waitcnt lgkmcnt(0)
	s_barrier
	ds_read_b64 v[122:123], v105 offset:416
	ds_read_b64 v[124:125], v105 offset:424
	ds_read_b64 v[126:127], v105 offset:432
	ds_read_b64 v[128:129], v105 offset:512
	ds_read_b64 v[130:131], v105 offset:520
	ds_read_b64 v[132:133], v105 offset:528
	s_waitcnt lgkmcnt(3)
	v_mfma_f32_16x16x128_f8f6f4 v[134:137], v[122:127], v[2:7], 0 cbsz:2 blgp:2
	v_mfma_f32_16x16x128_f8f6f4 v[138:141], v[122:127], v[14:19], 0 cbsz:2 blgp:2
	v_mfma_f32_16x16x128_f8f6f4 v[142:145], v[122:127], v[26:31], v[188:191] cbsz:2 blgp:2
	v_mfma_f32_16x16x128_f8f6f4 v[204:207], v[122:127], v[38:43], 0 cbsz:2 blgp:2
	v_mfma_f32_16x16x128_f8f6f4 v[208:211], v[122:127], v[50:55], 0 cbsz:2 blgp:2
	v_mfma_f32_16x16x128_f8f6f4 v[212:215], v[122:127], v[62:67], v[188:191] cbsz:2 blgp:2
	s_waitcnt lgkmcnt(0)
	v_mfma_f32_16x16x128_f8f6f4 v[134:137], v[128:133], v[8:13], v[134:137] cbsz:2 blgp:2
	v_mfma_f32_16x16x128_f8f6f4 v[204:207], v[128:133], v[44:49], v[204:207] cbsz:2 blgp:2
	v_mfma_f32_16x16x128_f8f6f4 v[138:141], v[128:133], v[20:25], v[138:141] cbsz:2 blgp:2
	v_mfma_f32_16x16x128_f8f6f4 v[208:211], v[128:133], v[56:61], v[208:211] cbsz:2 blgp:2
	v_mfma_f32_16x16x128_f8f6f4 v[142:145], v[128:133], v[32:37], v[142:145] cbsz:2 blgp:2
	v_mfma_f32_16x16x128_f8f6f4 v[212:215], v[128:133], v[68:73], v[212:215] cbsz:2 blgp:2
	v_cndmask_b32_e64 v158, v134, v204, s[0:1]
	v_fma_mix_f32 v158, v158, v100, v85 op_sel:[0,0,1] op_sel_hi:[0,0,1]
	v_exp_f32_e32 v158, v158
	v_cndmask_b32_e64 v159, v138, v208, s[0:1]
	v_fma_mix_f32 v159, v159, v101, v77 op_sel:[0,0,1] op_sel_hi:[0,0,1]
	v_exp_f32_e32 v159, v159
	v_fma_f32 v158, v158, v186, v186
	v_rcp_f32_e32 v158, v158
	v_add_f32_e32 v159, 1.0, v159
	v_rcp_f32_e32 v159, v159
	v_cndmask_b32_e64 v160, v142, v212, s[0:1]
	v_fma_mix_f32 v161, v158, v160, v81 op_sel:[0,0,1] op_sel_hi:[0,0,1]
	v_exp_f32_e32 v161, v161
	s_add_u32 s48, s48, s40
	v_add_f32_e32 v161, 1.0, v161
	v_rcp_f32_e32 v161, v161
	s_addc_u32 s49, s49, s41
	v_fma_f32 v162, v161, -2.0, 1.0
	v_sub_f32_e32 v163, v176, v162
	v_fma_f32 v176, v159, v163, v162
	v_fma_f32 v164, |v176|, s17, v113
	v_fma_f32 v165, |v176|, s18, v114
	v_fma_f32 v166, |v176|, s19, v115
	v_lshrrev_b32_e32 v167, 26, v176
	v_min3_u32 v164, v164, v165, v166
	v_bfi_b32 v168, 31, v164, v167
	s_nop 1
	v_mul_u32_u24_dpp v170, v168, v180 quad_perm:[1,2,3,3] row_mask:0xf bank_mask:0xf bound_ctrl:1
	v_mad_u32_u24 v171, v168, v181, v170
	ds_write_b8_d16_hi v184, v171
	s_barrier
	global_store_short_d16_hi v185, v176, s[48:49]
	s_waitcnt lgkmcnt(0)
	s_barrier
	ds_read_b64 v[122:123], v105 offset:0
	ds_read_b64 v[124:125], v105 offset:8
	ds_read_b64 v[126:127], v105 offset:16
	ds_read_b64 v[128:129], v105 offset:96
	ds_read_b64 v[130:131], v105 offset:104
	ds_read_b64 v[132:133], v105 offset:112
	s_waitcnt vmcnt(8)
	global_load_dwordx4 v[82:85], v[196:197], off
	global_load_dwordx4 v[74:77], v[196:197], off offset:512
	global_load_dwordx4 v[78:81], v[196:197], off offset:1024
	v_lshl_add_u64 v[196:197], v[196:197], 0, s[42:43]
	s_waitcnt lgkmcnt(3)
	v_mfma_f32_16x16x128_f8f6f4 v[134:137], v[122:127], v[2:7], 0 cbsz:2 blgp:2
	v_mfma_f32_16x16x128_f8f6f4 v[138:141], v[122:127], v[14:19], 0 cbsz:2 blgp:2
	v_mfma_f32_16x16x128_f8f6f4 v[142:145], v[122:127], v[26:31], v[188:191] cbsz:2 blgp:2
	v_mfma_f32_16x16x128_f8f6f4 v[204:207], v[122:127], v[38:43], 0 cbsz:2 blgp:2
	v_mfma_f32_16x16x128_f8f6f4 v[208:211], v[122:127], v[50:55], 0 cbsz:2 blgp:2
	v_mfma_f32_16x16x128_f8f6f4 v[212:215], v[122:127], v[62:67], v[188:191] cbsz:2 blgp:2
	s_waitcnt lgkmcnt(0)
	v_mfma_f32_16x16x128_f8f6f4 v[134:137], v[128:133], v[8:13], v[134:137] cbsz:2 blgp:2
	v_mfma_f32_16x16x128_f8f6f4 v[204:207], v[128:133], v[44:49], v[204:207] cbsz:2 blgp:2
	v_mfma_f32_16x16x128_f8f6f4 v[138:141], v[128:133], v[20:25], v[138:141] cbsz:2 blgp:2
	v_mfma_f32_16x16x128_f8f6f4 v[208:211], v[128:133], v[56:61], v[208:211] cbsz:2 blgp:2
	v_mfma_f32_16x16x128_f8f6f4 v[142:145], v[128:133], v[32:37], v[142:145] cbsz:2 blgp:2
	v_mfma_f32_16x16x128_f8f6f4 v[212:215], v[128:133], v[68:73], v[212:215] cbsz:2 blgp:2
	v_cndmask_b32_e64 v158, v134, v204, s[0:1]
	v_fma_mix_f32 v158, v158, v100, v146 op_sel_hi:[0,0,1]
	v_exp_f32_e32 v158, v158
	v_cndmask_b32_e64 v159, v138, v208, s[0:1]
	v_fma_mix_f32 v159, v159, v101, v150 op_sel_hi:[0,0,1]
	v_exp_f32_e32 v159, v159
	v_fma_f32 v158, v158, v186, v186
	v_rcp_f32_e32 v158, v158
	v_add_f32_e32 v159, 1.0, v159
	v_rcp_f32_e32 v159, v159
	v_cndmask_b32_e64 v160, v142, v212, s[0:1]
	v_fma_mix_f32 v161, v158, v160, v154 op_sel_hi:[0,0,1]
	v_exp_f32_e32 v161, v161
	s_add_u32 s48, s48, s40
	v_add_f32_e32 v161, 1.0, v161
	v_rcp_f32_e32 v161, v161
	s_addc_u32 s49, s49, s41
	v_fma_f32 v162, v161, -2.0, 1.0
	v_sub_f32_e32 v163, v176, v162
	v_fma_f32 v176, v159, v163, v162
	v_fma_f32 v164, |v176|, s17, v113
	v_fma_f32 v165, |v176|, s18, v114
	v_fma_f32 v166, |v176|, s19, v115
	v_lshrrev_b32_e32 v167, 26, v176
	v_min3_u32 v164, v164, v165, v166
	v_bfi_b32 v168, 31, v164, v167
	s_nop 1
	v_mul_u32_u24_dpp v170, v168, v180 quad_perm:[1,2,3,3] row_mask:0xf bank_mask:0xf bound_ctrl:1
	v_mad_u32_u24 v171, v168, v181, v170
	ds_write_b8_d16_hi v184, v171 offset:416
	s_barrier
	global_store_short_d16_hi v185, v176, s[48:49]
	s_waitcnt lgkmcnt(0)
	s_barrier
	ds_read_b64 v[122:123], v105 offset:416
	ds_read_b64 v[124:125], v105 offset:424
	ds_read_b64 v[126:127], v105 offset:432
	ds_read_b64 v[128:129], v105 offset:512
	ds_read_b64 v[130:131], v105 offset:520
	ds_read_b64 v[132:133], v105 offset:528
	s_waitcnt lgkmcnt(3)
	v_mfma_f32_16x16x128_f8f6f4 v[134:137], v[122:127], v[2:7], 0 cbsz:2 blgp:2
	v_mfma_f32_16x16x128_f8f6f4 v[138:141], v[122:127], v[14:19], 0 cbsz:2 blgp:2
	v_mfma_f32_16x16x128_f8f6f4 v[142:145], v[122:127], v[26:31], v[188:191] cbsz:2 blgp:2
	v_mfma_f32_16x16x128_f8f6f4 v[204:207], v[122:127], v[38:43], 0 cbsz:2 blgp:2
	v_mfma_f32_16x16x128_f8f6f4 v[208:211], v[122:127], v[50:55], 0 cbsz:2 blgp:2
	v_mfma_f32_16x16x128_f8f6f4 v[212:215], v[122:127], v[62:67], v[188:191] cbsz:2 blgp:2
	s_waitcnt lgkmcnt(0)
	v_mfma_f32_16x16x128_f8f6f4 v[134:137], v[128:133], v[8:13], v[134:137] cbsz:2 blgp:2
	v_mfma_f32_16x16x128_f8f6f4 v[204:207], v[128:133], v[44:49], v[204:207] cbsz:2 blgp:2
	v_mfma_f32_16x16x128_f8f6f4 v[138:141], v[128:133], v[20:25], v[138:141] cbsz:2 blgp:2
	v_mfma_f32_16x16x128_f8f6f4 v[208:211], v[128:133], v[56:61], v[208:211] cbsz:2 blgp:2
	v_mfma_f32_16x16x128_f8f6f4 v[142:145], v[128:133], v[32:37], v[142:145] cbsz:2 blgp:2
	v_mfma_f32_16x16x128_f8f6f4 v[212:215], v[128:133], v[68:73], v[212:215] cbsz:2 blgp:2
	v_cndmask_b32_e64 v158, v134, v204, s[0:1]
	v_fma_mix_f32 v158, v158, v100, v146 op_sel:[0,0,1] op_sel_hi:[0,0,1]
	v_exp_f32_e32 v158, v158
	v_cndmask_b32_e64 v159, v138, v208, s[0:1]
	v_fma_mix_f32 v159, v159, v101, v150 op_sel:[0,0,1] op_sel_hi:[0,0,1]
	v_exp_f32_e32 v159, v159
	v_fma_f32 v158, v158, v186, v186
	v_rcp_f32_e32 v158, v158
	v_add_f32_e32 v159, 1.0, v159
	v_rcp_f32_e32 v159, v159
	v_cndmask_b32_e64 v160, v142, v212, s[0:1]
	v_fma_mix_f32 v161, v158, v160, v154 op_sel:[0,0,1] op_sel_hi:[0,0,1]
	v_exp_f32_e32 v161, v161
	s_add_u32 s48, s48, s40
	v_add_f32_e32 v161, 1.0, v161
	v_rcp_f32_e32 v161, v161
	s_addc_u32 s49, s49, s41
	v_fma_f32 v162, v161, -2.0, 1.0
	v_sub_f32_e32 v163, v176, v162
	v_fma_f32 v176, v159, v163, v162
	v_fma_f32 v164, |v176|, s17, v113
	v_fma_f32 v165, |v176|, s18, v114
	v_fma_f32 v166, |v176|, s19, v115
	v_lshrrev_b32_e32 v167, 26, v176
	v_min3_u32 v164, v164, v165, v166
	v_bfi_b32 v168, 31, v164, v167
	s_nop 1
	v_mul_u32_u24_dpp v170, v168, v180 quad_perm:[1,2,3,3] row_mask:0xf bank_mask:0xf bound_ctrl:1
	v_mad_u32_u24 v171, v168, v181, v170
	ds_write_b8_d16_hi v184, v171
	s_barrier
	global_store_short_d16_hi v185, v176, s[48:49]
	s_waitcnt lgkmcnt(0)
	s_barrier
	ds_read_b64 v[122:123], v105 offset:0
	ds_read_b64 v[124:125], v105 offset:8
	ds_read_b64 v[126:127], v105 offset:16
	ds_read_b64 v[128:129], v105 offset:96
	ds_read_b64 v[130:131], v105 offset:104
	ds_read_b64 v[132:133], v105 offset:112
	s_waitcnt lgkmcnt(3)
	v_mfma_f32_16x16x128_f8f6f4 v[134:137], v[122:127], v[2:7], 0 cbsz:2 blgp:2
	v_mfma_f32_16x16x128_f8f6f4 v[138:141], v[122:127], v[14:19], 0 cbsz:2 blgp:2
	v_mfma_f32_16x16x128_f8f6f4 v[142:145], v[122:127], v[26:31], v[188:191] cbsz:2 blgp:2
	v_mfma_f32_16x16x128_f8f6f4 v[204:207], v[122:127], v[38:43], 0 cbsz:2 blgp:2
	v_mfma_f32_16x16x128_f8f6f4 v[208:211], v[122:127], v[50:55], 0 cbsz:2 blgp:2
	v_mfma_f32_16x16x128_f8f6f4 v[212:215], v[122:127], v[62:67], v[188:191] cbsz:2 blgp:2
	s_waitcnt lgkmcnt(0)
	v_mfma_f32_16x16x128_f8f6f4 v[134:137], v[128:133], v[8:13], v[134:137] cbsz:2 blgp:2
	v_mfma_f32_16x16x128_f8f6f4 v[204:207], v[128:133], v[44:49], v[204:207] cbsz:2 blgp:2
	v_mfma_f32_16x16x128_f8f6f4 v[138:141], v[128:133], v[20:25], v[138:141] cbsz:2 blgp:2
	v_mfma_f32_16x16x128_f8f6f4 v[208:211], v[128:133], v[56:61], v[208:211] cbsz:2 blgp:2
	v_mfma_f32_16x16x128_f8f6f4 v[142:145], v[128:133], v[32:37], v[142:145] cbsz:2 blgp:2
	v_mfma_f32_16x16x128_f8f6f4 v[212:215], v[128:133], v[68:73], v[212:215] cbsz:2 blgp:2
	v_cndmask_b32_e64 v158, v134, v204, s[0:1]
	v_fma_mix_f32 v158, v158, v100, v147 op_sel_hi:[0,0,1]
	v_exp_f32_e32 v158, v158
	v_cndmask_b32_e64 v159, v138, v208, s[0:1]
	v_fma_mix_f32 v159, v159, v101, v151 op_sel_hi:[0,0,1]
	v_exp_f32_e32 v159, v159
	v_fma_f32 v158, v158, v186, v186
	v_rcp_f32_e32 v158, v158
	v_add_f32_e32 v159, 1.0, v159
	v_rcp_f32_e32 v159, v159
	v_cndmask_b32_e64 v160, v142, v212, s[0:1]
	v_fma_mix_f32 v161, v158, v160, v155 op_sel_hi:[0,0,1]
	v_exp_f32_e32 v161, v161
	s_add_u32 s48, s48, s40
	v_add_f32_e32 v161, 1.0, v161
	v_rcp_f32_e32 v161, v161
	s_addc_u32 s49, s49, s41
	v_fma_f32 v162, v161, -2.0, 1.0
	v_sub_f32_e32 v163, v176, v162
	v_fma_f32 v176, v159, v163, v162
	v_fma_f32 v164, |v176|, s17, v113
	v_fma_f32 v165, |v176|, s18, v114
	v_fma_f32 v166, |v176|, s19, v115
	v_lshrrev_b32_e32 v167, 26, v176
	v_min3_u32 v164, v164, v165, v166
	v_bfi_b32 v168, 31, v164, v167
	s_nop 1
	v_mul_u32_u24_dpp v170, v168, v180 quad_perm:[1,2,3,3] row_mask:0xf bank_mask:0xf bound_ctrl:1
	v_mad_u32_u24 v171, v168, v181, v170
	ds_write_b8_d16_hi v184, v171 offset:416
	s_barrier
	global_store_short_d16_hi v185, v176, s[48:49]
	s_waitcnt lgkmcnt(0)
	s_barrier
	ds_read_b64 v[122:123], v105 offset:416
	ds_read_b64 v[124:125], v105 offset:424
	ds_read_b64 v[126:127], v105 offset:432
	ds_read_b64 v[128:129], v105 offset:512
	ds_read_b64 v[130:131], v105 offset:520
	ds_read_b64 v[132:133], v105 offset:528
	s_waitcnt lgkmcnt(3)
	v_mfma_f32_16x16x128_f8f6f4 v[134:137], v[122:127], v[2:7], 0 cbsz:2 blgp:2
	v_mfma_f32_16x16x128_f8f6f4 v[138:141], v[122:127], v[14:19], 0 cbsz:2 blgp:2
	v_mfma_f32_16x16x128_f8f6f4 v[142:145], v[122:127], v[26:31], v[188:191] cbsz:2 blgp:2
	v_mfma_f32_16x16x128_f8f6f4 v[204:207], v[122:127], v[38:43], 0 cbsz:2 blgp:2
	v_mfma_f32_16x16x128_f8f6f4 v[208:211], v[122:127], v[50:55], 0 cbsz:2 blgp:2
	v_mfma_f32_16x16x128_f8f6f4 v[212:215], v[122:127], v[62:67], v[188:191] cbsz:2 blgp:2
	s_waitcnt lgkmcnt(0)
	v_mfma_f32_16x16x128_f8f6f4 v[134:137], v[128:133], v[8:13], v[134:137] cbsz:2 blgp:2
	v_mfma_f32_16x16x128_f8f6f4 v[204:207], v[128:133], v[44:49], v[204:207] cbsz:2 blgp:2
	v_mfma_f32_16x16x128_f8f6f4 v[138:141], v[128:133], v[20:25], v[138:141] cbsz:2 blgp:2
	v_mfma_f32_16x16x128_f8f6f4 v[208:211], v[128:133], v[56:61], v[208:211] cbsz:2 blgp:2
	v_mfma_f32_16x16x128_f8f6f4 v[142:145], v[128:133], v[32:37], v[142:145] cbsz:2 blgp:2
	v_mfma_f32_16x16x128_f8f6f4 v[212:215], v[128:133], v[68:73], v[212:215] cbsz:2 blgp:2
	v_cndmask_b32_e64 v158, v134, v204, s[0:1]
	v_fma_mix_f32 v158, v158, v100, v147 op_sel:[0,0,1] op_sel_hi:[0,0,1]
	v_exp_f32_e32 v158, v158
	v_cndmask_b32_e64 v159, v138, v208, s[0:1]
	v_fma_mix_f32 v159, v159, v101, v151 op_sel:[0,0,1] op_sel_hi:[0,0,1]
	v_exp_f32_e32 v159, v159
	v_fma_f32 v158, v158, v186, v186
	v_rcp_f32_e32 v158, v158
	v_add_f32_e32 v159, 1.0, v159
	v_rcp_f32_e32 v159, v159
	v_cndmask_b32_e64 v160, v142, v212, s[0:1]
	v_fma_mix_f32 v161, v158, v160, v155 op_sel:[0,0,1] op_sel_hi:[0,0,1]
	v_exp_f32_e32 v161, v161
	s_add_u32 s48, s48, s40
	v_add_f32_e32 v161, 1.0, v161
	v_rcp_f32_e32 v161, v161
	s_addc_u32 s49, s49, s41
	v_fma_f32 v162, v161, -2.0, 1.0
	v_sub_f32_e32 v163, v176, v162
	v_fma_f32 v176, v159, v163, v162
	v_fma_f32 v164, |v176|, s17, v113
	v_fma_f32 v165, |v176|, s18, v114
	v_fma_f32 v166, |v176|, s19, v115
	v_lshrrev_b32_e32 v167, 26, v176
	v_min3_u32 v164, v164, v165, v166
	v_bfi_b32 v168, 31, v164, v167
	s_nop 1
	v_mul_u32_u24_dpp v170, v168, v180 quad_perm:[1,2,3,3] row_mask:0xf bank_mask:0xf bound_ctrl:1
	v_mad_u32_u24 v171, v168, v181, v170
	ds_write_b8_d16_hi v184, v171
	s_barrier
	global_store_short_d16_hi v185, v176, s[48:49]
	s_waitcnt lgkmcnt(0)
	s_barrier
	ds_read_b64 v[122:123], v105 offset:0
	ds_read_b64 v[124:125], v105 offset:8
	ds_read_b64 v[126:127], v105 offset:16
	ds_read_b64 v[128:129], v105 offset:96
	ds_read_b64 v[130:131], v105 offset:104
	ds_read_b64 v[132:133], v105 offset:112
	s_waitcnt lgkmcnt(3)
	v_mfma_f32_16x16x128_f8f6f4 v[134:137], v[122:127], v[2:7], 0 cbsz:2 blgp:2
	v_mfma_f32_16x16x128_f8f6f4 v[138:141], v[122:127], v[14:19], 0 cbsz:2 blgp:2
	v_mfma_f32_16x16x128_f8f6f4 v[142:145], v[122:127], v[26:31], v[188:191] cbsz:2 blgp:2
	v_mfma_f32_16x16x128_f8f6f4 v[204:207], v[122:127], v[38:43], 0 cbsz:2 blgp:2
	v_mfma_f32_16x16x128_f8f6f4 v[208:211], v[122:127], v[50:55], 0 cbsz:2 blgp:2
	v_mfma_f32_16x16x128_f8f6f4 v[212:215], v[122:127], v[62:67], v[188:191] cbsz:2 blgp:2
	s_waitcnt lgkmcnt(0)
	v_mfma_f32_16x16x128_f8f6f4 v[134:137], v[128:133], v[8:13], v[134:137] cbsz:2 blgp:2
	v_mfma_f32_16x16x128_f8f6f4 v[204:207], v[128:133], v[44:49], v[204:207] cbsz:2 blgp:2
	v_mfma_f32_16x16x128_f8f6f4 v[138:141], v[128:133], v[20:25], v[138:141] cbsz:2 blgp:2
	v_mfma_f32_16x16x128_f8f6f4 v[208:211], v[128:133], v[56:61], v[208:211] cbsz:2 blgp:2
	v_mfma_f32_16x16x128_f8f6f4 v[142:145], v[128:133], v[32:37], v[142:145] cbsz:2 blgp:2
	v_mfma_f32_16x16x128_f8f6f4 v[212:215], v[128:133], v[68:73], v[212:215] cbsz:2 blgp:2
	v_cndmask_b32_e64 v158, v134, v204, s[0:1]
	v_fma_mix_f32 v158, v158, v100, v148 op_sel_hi:[0,0,1]
	v_exp_f32_e32 v158, v158
	v_cndmask_b32_e64 v159, v138, v208, s[0:1]
	v_fma_mix_f32 v159, v159, v101, v152 op_sel_hi:[0,0,1]
	v_exp_f32_e32 v159, v159
	v_fma_f32 v158, v158, v186, v186
	v_rcp_f32_e32 v158, v158
	v_add_f32_e32 v159, 1.0, v159
	v_rcp_f32_e32 v159, v159
	v_cndmask_b32_e64 v160, v142, v212, s[0:1]
	v_fma_mix_f32 v161, v158, v160, v156 op_sel_hi:[0,0,1]
	v_exp_f32_e32 v161, v161
	s_add_u32 s48, s48, s40
	v_add_f32_e32 v161, 1.0, v161
	v_rcp_f32_e32 v161, v161
	s_addc_u32 s49, s49, s41
	v_fma_f32 v162, v161, -2.0, 1.0
	v_sub_f32_e32 v163, v176, v162
	v_fma_f32 v176, v159, v163, v162
	v_fma_f32 v164, |v176|, s17, v113
	v_fma_f32 v165, |v176|, s18, v114
	v_fma_f32 v166, |v176|, s19, v115
	v_lshrrev_b32_e32 v167, 26, v176
	v_min3_u32 v164, v164, v165, v166
	v_bfi_b32 v168, 31, v164, v167
	s_nop 1
	v_mul_u32_u24_dpp v170, v168, v180 quad_perm:[1,2,3,3] row_mask:0xf bank_mask:0xf bound_ctrl:1
	v_mad_u32_u24 v171, v168, v181, v170
	ds_write_b8_d16_hi v184, v171 offset:416
	s_barrier
	global_store_short_d16_hi v185, v176, s[48:49]
	s_waitcnt lgkmcnt(0)
	s_barrier
	ds_read_b64 v[122:123], v105 offset:416
	ds_read_b64 v[124:125], v105 offset:424
	ds_read_b64 v[126:127], v105 offset:432
	ds_read_b64 v[128:129], v105 offset:512
	ds_read_b64 v[130:131], v105 offset:520
	ds_read_b64 v[132:133], v105 offset:528
	s_waitcnt lgkmcnt(3)
	v_mfma_f32_16x16x128_f8f6f4 v[134:137], v[122:127], v[2:7], 0 cbsz:2 blgp:2
	v_mfma_f32_16x16x128_f8f6f4 v[138:141], v[122:127], v[14:19], 0 cbsz:2 blgp:2
	v_mfma_f32_16x16x128_f8f6f4 v[142:145], v[122:127], v[26:31], v[188:191] cbsz:2 blgp:2
	v_mfma_f32_16x16x128_f8f6f4 v[204:207], v[122:127], v[38:43], 0 cbsz:2 blgp:2
	v_mfma_f32_16x16x128_f8f6f4 v[208:211], v[122:127], v[50:55], 0 cbsz:2 blgp:2
	v_mfma_f32_16x16x128_f8f6f4 v[212:215], v[122:127], v[62:67], v[188:191] cbsz:2 blgp:2
	s_waitcnt lgkmcnt(0)
	v_mfma_f32_16x16x128_f8f6f4 v[134:137], v[128:133], v[8:13], v[134:137] cbsz:2 blgp:2
	v_mfma_f32_16x16x128_f8f6f4 v[204:207], v[128:133], v[44:49], v[204:207] cbsz:2 blgp:2
	v_mfma_f32_16x16x128_f8f6f4 v[138:141], v[128:133], v[20:25], v[138:141] cbsz:2 blgp:2
	v_mfma_f32_16x16x128_f8f6f4 v[208:211], v[128:133], v[56:61], v[208:211] cbsz:2 blgp:2
	v_mfma_f32_16x16x128_f8f6f4 v[142:145], v[128:133], v[32:37], v[142:145] cbsz:2 blgp:2
	v_mfma_f32_16x16x128_f8f6f4 v[212:215], v[128:133], v[68:73], v[212:215] cbsz:2 blgp:2
	v_cndmask_b32_e64 v158, v134, v204, s[0:1]
	v_fma_mix_f32 v158, v158, v100, v148 op_sel:[0,0,1] op_sel_hi:[0,0,1]
	v_exp_f32_e32 v158, v158
	v_cndmask_b32_e64 v159, v138, v208, s[0:1]
	v_fma_mix_f32 v159, v159, v101, v152 op_sel:[0,0,1] op_sel_hi:[0,0,1]
	v_exp_f32_e32 v159, v159
	v_fma_f32 v158, v158, v186, v186
	v_rcp_f32_e32 v158, v158
	v_add_f32_e32 v159, 1.0, v159
	v_rcp_f32_e32 v159, v159
	v_cndmask_b32_e64 v160, v142, v212, s[0:1]
	v_fma_mix_f32 v161, v158, v160, v156 op_sel:[0,0,1] op_sel_hi:[0,0,1]
	v_exp_f32_e32 v161, v161
	s_add_u32 s48, s48, s40
	v_add_f32_e32 v161, 1.0, v161
	v_rcp_f32_e32 v161, v161
	s_addc_u32 s49, s49, s41
	v_fma_f32 v162, v161, -2.0, 1.0
	v_sub_f32_e32 v163, v176, v162
	v_fma_f32 v176, v159, v163, v162
	v_fma_f32 v164, |v176|, s17, v113
	v_fma_f32 v165, |v176|, s18, v114
	v_fma_f32 v166, |v176|, s19, v115
	v_lshrrev_b32_e32 v167, 26, v176
	v_min3_u32 v164, v164, v165, v166
	v_bfi_b32 v168, 31, v164, v167
	s_nop 1
	v_mul_u32_u24_dpp v170, v168, v180 quad_perm:[1,2,3,3] row_mask:0xf bank_mask:0xf bound_ctrl:1
	v_mad_u32_u24 v171, v168, v181, v170
	ds_write_b8_d16_hi v184, v171
	s_barrier
	global_store_short_d16_hi v185, v176, s[48:49]
	s_waitcnt lgkmcnt(0)
	s_barrier
	ds_read_b64 v[122:123], v105 offset:0
	ds_read_b64 v[124:125], v105 offset:8
	ds_read_b64 v[126:127], v105 offset:16
	ds_read_b64 v[128:129], v105 offset:96
	ds_read_b64 v[130:131], v105 offset:104
	ds_read_b64 v[132:133], v105 offset:112
	s_waitcnt lgkmcnt(3)
	v_mfma_f32_16x16x128_f8f6f4 v[134:137], v[122:127], v[2:7], 0 cbsz:2 blgp:2
	v_mfma_f32_16x16x128_f8f6f4 v[138:141], v[122:127], v[14:19], 0 cbsz:2 blgp:2
	v_mfma_f32_16x16x128_f8f6f4 v[142:145], v[122:127], v[26:31], v[188:191] cbsz:2 blgp:2
	v_mfma_f32_16x16x128_f8f6f4 v[204:207], v[122:127], v[38:43], 0 cbsz:2 blgp:2
	v_mfma_f32_16x16x128_f8f6f4 v[208:211], v[122:127], v[50:55], 0 cbsz:2 blgp:2
	v_mfma_f32_16x16x128_f8f6f4 v[212:215], v[122:127], v[62:67], v[188:191] cbsz:2 blgp:2
	s_waitcnt lgkmcnt(0)
	v_mfma_f32_16x16x128_f8f6f4 v[134:137], v[128:133], v[8:13], v[134:137] cbsz:2 blgp:2
	v_mfma_f32_16x16x128_f8f6f4 v[204:207], v[128:133], v[44:49], v[204:207] cbsz:2 blgp:2
	v_mfma_f32_16x16x128_f8f6f4 v[138:141], v[128:133], v[20:25], v[138:141] cbsz:2 blgp:2
	v_mfma_f32_16x16x128_f8f6f4 v[208:211], v[128:133], v[56:61], v[208:211] cbsz:2 blgp:2
	v_mfma_f32_16x16x128_f8f6f4 v[142:145], v[128:133], v[32:37], v[142:145] cbsz:2 blgp:2
	v_mfma_f32_16x16x128_f8f6f4 v[212:215], v[128:133], v[68:73], v[212:215] cbsz:2 blgp:2
	v_cndmask_b32_e64 v158, v134, v204, s[0:1]
	v_fma_mix_f32 v158, v158, v100, v149 op_sel_hi:[0,0,1]
	v_exp_f32_e32 v158, v158
	v_cndmask_b32_e64 v159, v138, v208, s[0:1]
	v_fma_mix_f32 v159, v159, v101, v153 op_sel_hi:[0,0,1]
	v_exp_f32_e32 v159, v159
	v_fma_f32 v158, v158, v186, v186
	v_rcp_f32_e32 v158, v158
	v_add_f32_e32 v159, 1.0, v159
	v_rcp_f32_e32 v159, v159
	v_cndmask_b32_e64 v160, v142, v212, s[0:1]
	v_fma_mix_f32 v161, v158, v160, v157 op_sel_hi:[0,0,1]
	v_exp_f32_e32 v161, v161
	s_add_u32 s48, s48, s40
	v_add_f32_e32 v161, 1.0, v161
	v_rcp_f32_e32 v161, v161
	s_addc_u32 s49, s49, s41
	v_fma_f32 v162, v161, -2.0, 1.0
	v_sub_f32_e32 v163, v176, v162
	v_fma_f32 v176, v159, v163, v162
	v_fma_f32 v164, |v176|, s17, v113
	v_fma_f32 v165, |v176|, s18, v114
	v_fma_f32 v166, |v176|, s19, v115
	v_lshrrev_b32_e32 v167, 26, v176
	v_min3_u32 v164, v164, v165, v166
	v_bfi_b32 v168, 31, v164, v167
	s_nop 1
	v_mul_u32_u24_dpp v170, v168, v180 quad_perm:[1,2,3,3] row_mask:0xf bank_mask:0xf bound_ctrl:1
	v_mad_u32_u24 v171, v168, v181, v170
	ds_write_b8_d16_hi v184, v171 offset:416
	s_barrier
	global_store_short_d16_hi v185, v176, s[48:49]
	s_waitcnt lgkmcnt(0)
	s_barrier
	ds_read_b64 v[122:123], v105 offset:416
	ds_read_b64 v[124:125], v105 offset:424
	ds_read_b64 v[126:127], v105 offset:432
	ds_read_b64 v[128:129], v105 offset:512
	ds_read_b64 v[130:131], v105 offset:520
	ds_read_b64 v[132:133], v105 offset:528
	s_add_i32 s44, s44, 16
	s_waitcnt lgkmcnt(3)
	v_mfma_f32_16x16x128_f8f6f4 v[134:137], v[122:127], v[2:7], 0 cbsz:2 blgp:2
	v_mfma_f32_16x16x128_f8f6f4 v[138:141], v[122:127], v[14:19], 0 cbsz:2 blgp:2
	v_mfma_f32_16x16x128_f8f6f4 v[142:145], v[122:127], v[26:31], v[188:191] cbsz:2 blgp:2
	v_mfma_f32_16x16x128_f8f6f4 v[204:207], v[122:127], v[38:43], 0 cbsz:2 blgp:2
	v_mfma_f32_16x16x128_f8f6f4 v[208:211], v[122:127], v[50:55], 0 cbsz:2 blgp:2
	v_mfma_f32_16x16x128_f8f6f4 v[212:215], v[122:127], v[62:67], v[188:191] cbsz:2 blgp:2
	s_waitcnt lgkmcnt(0)
	v_mfma_f32_16x16x128_f8f6f4 v[134:137], v[128:133], v[8:13], v[134:137] cbsz:2 blgp:2
	v_mfma_f32_16x16x128_f8f6f4 v[204:207], v[128:133], v[44:49], v[204:207] cbsz:2 blgp:2
	v_mfma_f32_16x16x128_f8f6f4 v[138:141], v[128:133], v[20:25], v[138:141] cbsz:2 blgp:2
	v_mfma_f32_16x16x128_f8f6f4 v[208:211], v[128:133], v[56:61], v[208:211] cbsz:2 blgp:2
	v_mfma_f32_16x16x128_f8f6f4 v[142:145], v[128:133], v[32:37], v[142:145] cbsz:2 blgp:2
	v_mfma_f32_16x16x128_f8f6f4 v[212:215], v[128:133], v[68:73], v[212:215] cbsz:2 blgp:2
	v_cndmask_b32_e64 v158, v134, v204, s[0:1]
	v_fma_mix_f32 v158, v158, v100, v149 op_sel:[0,0,1] op_sel_hi:[0,0,1]
	v_exp_f32_e32 v158, v158
	v_cndmask_b32_e64 v159, v138, v208, s[0:1]
	v_fma_mix_f32 v159, v159, v101, v153 op_sel:[0,0,1] op_sel_hi:[0,0,1]
	v_exp_f32_e32 v159, v159
	v_fma_f32 v158, v158, v186, v186
	v_rcp_f32_e32 v158, v158
	v_add_f32_e32 v159, 1.0, v159
	v_rcp_f32_e32 v159, v159
	v_cndmask_b32_e64 v160, v142, v212, s[0:1]
	v_fma_mix_f32 v161, v158, v160, v157 op_sel:[0,0,1] op_sel_hi:[0,0,1]
	v_exp_f32_e32 v161, v161
	s_add_u32 s48, s48, s40
	v_add_f32_e32 v161, 1.0, v161
	v_rcp_f32_e32 v161, v161
	s_addc_u32 s49, s49, s41
	v_fma_f32 v162, v161, -2.0, 1.0
	v_sub_f32_e32 v163, v176, v162
	v_fma_f32 v176, v159, v163, v162
	v_fma_f32 v164, |v176|, s17, v113
	v_fma_f32 v165, |v176|, s18, v114
	v_fma_f32 v166, |v176|, s19, v115
	v_lshrrev_b32_e32 v167, 26, v176
	v_min3_u32 v164, v164, v165, v166
	v_bfi_b32 v168, 31, v164, v167
	s_nop 1
	v_mul_u32_u24_dpp v170, v168, v180 quad_perm:[1,2,3,3] row_mask:0xf bank_mask:0xf bound_ctrl:1
	v_mad_u32_u24 v171, v168, v181, v170
	ds_write_b8_d16_hi v184, v171
	s_barrier
	global_store_short_d16_hi v185, v176, s[48:49]
	s_cmp_lt_i32 s44, s45
	s_cbranch_scc1 .Lscan_loop_b_f2
	s_waitcnt lgkmcnt(0)
	s_barrier
